# packed f32 VALU ops unpacked to scalar pairs in in-proj and SwiGLU GEMM epilogues (1216 ops)
# speedup vs baseline: 1.0025x; 1.0025x over previous
.LBB0_147:
	s_cmp_gt_i32 s4, 1
	s_cselect_b64 s[62:63], -1, 0
	s_cmp_lt_u32 s4, 4
	s_cselect_b64 s[2:3], -1, 0
	v_cndmask_b32_e64 v130, 0, 1, s[2:3]
	s_mov_b64 s[38:39], -1
	s_and_b64 vcc, exec, s[62:63]
	v_cmp_ne_u32_e64 s[2:3], 1, v130
	s_cbranch_vccz .LBB0_151
	v_mov_b64_e32 v[132:133], v[128:129]
	v_mov_b64_e32 v[144:145], v[116:117]
	v_mov_b64_e32 v[140:141], v[120:121]
	v_mov_b64_e32 v[136:137], v[124:125]
	s_and_b64 vcc, exec, s[2:3]
	v_mov_b64_e32 v[130:131], v[126:127]
	v_mov_b64_e32 v[142:143], v[114:115]
	v_mov_b64_e32 v[138:139], v[118:119]
	v_mov_b64_e32 v[134:135], v[122:123]
	s_cbranch_vccnz .LBB0_150
	v_mul_f32 v132, v128, s24
	v_mul_f32 v133, v129, s24
	v_mul_f32 v130, v126, s24
	v_mul_f32 v131, v127, s24
	v_mul_f32 v136, v124, s24
	v_mul_f32 v137, v125, s24
	v_mul_f32 v134, v122, s24
	v_mul_f32 v135, v123, s24
	v_mul_f32 v140, v120, s24
	v_mul_f32 v141, v121, s24
	v_mul_f32 v138, v118, s24
	v_mul_f32 v139, v119, s24
	v_mul_f32 v144, v116, s24
	v_mul_f32 v145, v117, s24
	v_mul_f32 v142, v114, s24
	v_mul_f32 v143, v115, s24

.LBB0_151:
	s_andn2_b64 vcc, exec, s[38:39]
	s_cbranch_vccnz .LBB0_153
	v_mul_f32_e32 v131, v126, v126
	v_mul_f32_e32 v131, 0xbf38aa3b, v131
	v_fma_f32 v130, |v126|, s85, 1.0
	v_exp_f32_e32 v132, v131
	v_fma_f32 v131, |v127|, s85, 1.0
	v_rcp_f32_e32 v130, v130
	v_rcp_f32_e32 v131, v131
	v_mul_f32_e32 v133, v127, v127
	v_mov_b64_e32 v[142:143], s[28:29]
	v_mul_f32_e32 v133, 0xbf38aa3b, v133
	v_fma_f32 v134, v130, s26, v142
	v_fma_f32 v135, v131, s26, v142
	v_exp_f32_e32 v133, v133
	v_fma_f32 v134, v130, v134, s30
	v_fma_f32 v135, v131, v135, s30
	v_cmp_gt_f32_e32 vcc, 0, v129
	v_fma_f32 v134, v130, v134, s34
	v_fma_f32 v135, v131, v135, s34
	s_nop 0
	v_fma_f32 v134, v130, v134, s36
	v_fma_f32 v135, v131, v135, s36
	s_nop 0
	v_mul_f32 v130, v130, v134
	v_mul_f32 v131, v131, v135
	v_mul_f32_e32 v135, v129, v129
	v_mul_f32 v130, v132, v130
	v_mul_f32 v131, v133, v131
	v_mul_f32_e32 v133, v128, v128
	v_mul_f32_e32 v133, 0xbf38aa3b, v133
	v_fma_f32 v132, |v128|, s85, 1.0
	v_exp_f32_e32 v134, v133
	v_fma_f32 v133, |v129|, s85, 1.0
	v_rcp_f32_e32 v132, v132
	v_rcp_f32_e32 v133, v133
	v_mul_f32_e32 v135, 0xbf38aa3b, v135
	v_exp_f32_e32 v135, v135
	v_mul_f32 v130, v126, v130
	v_mul_f32 v131, v127, v131
	v_fma_f32 v136, v132, s26, v142
	v_fma_f32 v137, v133, s26, v142
	s_nop 0
	v_fma_f32 v136, v132, v136, s30
	v_fma_f32 v137, v133, v137, s30
	s_nop 0
	v_fma_f32 v136, v132, v136, s34
	v_fma_f32 v137, v133, v137, s34
	s_nop 0
	v_fma_f32 v136, v132, v136, s36
	v_fma_f32 v137, v133, v137, s36
	s_nop 0
	v_mul_f32 v132, v132, v136
	v_mul_f32 v133, v133, v137
	s_nop 0
	v_mul_f32 v132, v134, v132
	v_mul_f32 v133, v135, v133
	v_sub_f32_e32 v135, v127, v131
	v_mul_f32 v132, v128, v132
	v_mul_f32 v133, v129, v133
	v_sub_f32_e32 v134, v126, v130
	v_sub_f32_e32 v137, v129, v133
	v_sub_f32_e32 v136, v128, v132
	v_cndmask_b32_e32 v133, v137, v133, vcc
	v_cmp_gt_f32_e32 vcc, 0, v128
	v_mul_f32_e32 v129, v123, v123
	v_mul_f32_e32 v129, 0xbf38aa3b, v129
	v_cndmask_b32_e32 v132, v136, v132, vcc
	v_cmp_gt_f32_e32 vcc, 0, v127
	v_mul_f32_e32 v127, v122, v122
	v_mul_f32_e32 v127, 0xbf38aa3b, v127
	v_cndmask_b32_e32 v131, v135, v131, vcc
	v_cmp_gt_f32_e32 vcc, 0, v126
	v_fma_f32 v126, |v122|, s85, 1.0
	v_exp_f32_e32 v128, v127
	v_fma_f32 v127, |v123|, s85, 1.0
	v_rcp_f32_e32 v126, v126
	v_rcp_f32_e32 v127, v127
	v_cndmask_b32_e32 v130, v134, v130, vcc
	v_exp_f32_e32 v129, v129
	v_cmp_gt_f32_e32 vcc, 0, v125
	v_fma_f32 v134, v126, s26, v142
	v_fma_f32 v135, v127, s26, v142
	s_nop 0
	v_fma_f32 v134, v126, v134, s30
	v_fma_f32 v135, v127, v135, s30
	s_nop 0
	v_fma_f32 v134, v126, v134, s34
	v_fma_f32 v135, v127, v135, s34
	s_nop 0
	v_fma_f32 v134, v126, v134, s36
	v_fma_f32 v135, v127, v135, s36
	s_nop 0
	v_mul_f32 v126, v126, v134
	v_mul_f32 v127, v127, v135
	v_mul_f32_e32 v135, v125, v125
	v_mul_f32 v126, v128, v126
	v_mul_f32 v127, v129, v127
	v_mul_f32_e32 v129, v124, v124
	v_mul_f32_e32 v129, 0xbf38aa3b, v129
	v_fma_f32 v128, |v124|, s85, 1.0
	v_exp_f32_e32 v134, v129
	v_fma_f32 v129, |v125|, s85, 1.0
	v_rcp_f32_e32 v128, v128
	v_rcp_f32_e32 v129, v129
	v_mul_f32_e32 v135, 0xbf38aa3b, v135
	v_exp_f32_e32 v135, v135
	v_mul_f32 v126, v122, v126
	v_mul_f32 v127, v123, v127
	v_fma_f32 v136, v128, s26, v142
	v_fma_f32 v137, v129, s26, v142
	s_nop 0
	v_fma_f32 v136, v128, v136, s30
	v_fma_f32 v137, v129, v137, s30
	s_nop 0
	v_fma_f32 v136, v128, v136, s34
	v_fma_f32 v137, v129, v137, s34
	s_nop 0
	v_fma_f32 v136, v128, v136, s36
	v_fma_f32 v137, v129, v137, s36
	s_nop 0
	v_mul_f32 v128, v128, v136
	v_mul_f32 v129, v129, v137
	s_nop 0
	v_mul_f32 v128, v134, v128
	v_mul_f32 v129, v135, v129
	v_sub_f32_e32 v135, v123, v127
	v_mul_f32 v128, v124, v128
	v_mul_f32 v129, v125, v129
	v_sub_f32_e32 v134, v122, v126
	v_sub_f32_e32 v137, v125, v129
	v_sub_f32_e32 v136, v124, v128
	v_cndmask_b32_e32 v137, v137, v129, vcc
	v_cmp_gt_f32_e32 vcc, 0, v124
	v_mul_f32_e32 v125, v119, v119
	v_mul_f32_e32 v125, 0xbf38aa3b, v125
	v_cndmask_b32_e32 v136, v136, v128, vcc
	v_cmp_gt_f32_e32 vcc, 0, v123
	v_mul_f32_e32 v123, v118, v118
	v_mul_f32_e32 v123, 0xbf38aa3b, v123
	v_cndmask_b32_e32 v135, v135, v127, vcc
	v_cmp_gt_f32_e32 vcc, 0, v122
	v_fma_f32 v122, |v118|, s85, 1.0
	v_exp_f32_e32 v124, v123
	v_fma_f32 v123, |v119|, s85, 1.0
	v_rcp_f32_e32 v122, v122
	v_rcp_f32_e32 v123, v123
	v_cndmask_b32_e32 v134, v134, v126, vcc
	v_exp_f32_e32 v125, v125
	v_cmp_gt_f32_e32 vcc, 0, v121
	v_fma_f32 v126, v122, s26, v142
	v_fma_f32 v127, v123, s26, v142
	s_nop 0
	v_fma_f32 v126, v122, v126, s30
	v_fma_f32 v127, v123, v127, s30
	s_nop 0
	v_fma_f32 v126, v122, v126, s34
	v_fma_f32 v127, v123, v127, s34
	s_nop 0
	v_fma_f32 v126, v122, v126, s36
	v_fma_f32 v127, v123, v127, s36
	s_nop 0
	v_mul_f32 v122, v122, v126
	v_mul_f32 v123, v123, v127
	v_mul_f32_e32 v127, v121, v121
	v_mul_f32 v122, v124, v122
	v_mul_f32 v123, v125, v123
	v_mul_f32_e32 v125, v120, v120
	v_mul_f32_e32 v125, 0xbf38aa3b, v125
	v_fma_f32 v124, |v120|, s85, 1.0
	v_exp_f32_e32 v126, v125
	v_fma_f32 v125, |v121|, s85, 1.0
	v_rcp_f32_e32 v124, v124
	v_rcp_f32_e32 v125, v125
	v_mul_f32_e32 v127, 0xbf38aa3b, v127
	v_exp_f32_e32 v127, v127
	v_mul_f32 v122, v118, v122
	v_mul_f32 v123, v119, v123
	v_fma_f32 v128, v124, s26, v142
	v_fma_f32 v129, v125, s26, v142
	s_nop 0
	v_fma_f32 v128, v124, v128, s30
	v_fma_f32 v129, v125, v129, s30
	s_nop 0
	v_fma_f32 v128, v124, v128, s34
	v_fma_f32 v129, v125, v129, s34
	s_nop 0
	v_fma_f32 v128, v124, v128, s36
	v_fma_f32 v129, v125, v129, s36
	s_nop 0
	v_mul_f32 v124, v124, v128
	v_mul_f32 v125, v125, v129
	s_nop 0
	v_mul_f32 v124, v126, v124
	v_mul_f32 v125, v127, v125
	v_sub_f32_e32 v127, v119, v123
	v_mul_f32 v124, v120, v124
	v_mul_f32 v125, v121, v125
	v_sub_f32_e32 v126, v118, v122
	v_sub_f32_e32 v129, v121, v125
	v_sub_f32_e32 v128, v120, v124
	v_cndmask_b32_e32 v141, v129, v125, vcc
	v_cmp_gt_f32_e32 vcc, 0, v120
	v_mul_f32_e32 v121, v115, v115
	v_mul_f32_e32 v121, 0xbf38aa3b, v121
	v_cndmask_b32_e32 v140, v128, v124, vcc
	v_cmp_gt_f32_e32 vcc, 0, v119
	v_mul_f32_e32 v119, v114, v114
	v_mul_f32_e32 v119, 0xbf38aa3b, v119
	v_cndmask_b32_e32 v139, v127, v123, vcc
	v_cmp_gt_f32_e32 vcc, 0, v118
	v_fma_f32 v118, |v114|, s85, 1.0
	v_exp_f32_e32 v120, v119
	v_fma_f32 v119, |v115|, s85, 1.0
	v_rcp_f32_e32 v118, v118
	v_rcp_f32_e32 v119, v119
	v_cndmask_b32_e32 v138, v126, v122, vcc
	v_exp_f32_e32 v121, v121
	v_cmp_gt_f32_e32 vcc, 0, v117
	v_fma_f32 v122, v118, s26, v142
	v_fma_f32 v123, v119, s26, v142
	s_nop 0
	v_fma_f32 v122, v118, v122, s30
	v_fma_f32 v123, v119, v123, s30
	s_nop 0
	v_fma_f32 v122, v118, v122, s34
	v_fma_f32 v123, v119, v123, s34
	s_nop 0
	v_fma_f32 v122, v118, v122, s36
	v_fma_f32 v123, v119, v123, s36
	s_nop 0
	v_mul_f32 v118, v118, v122
	v_mul_f32 v119, v119, v123
	v_mul_f32_e32 v123, v117, v117
	v_mul_f32 v118, v120, v118
	v_mul_f32 v119, v121, v119
	v_mul_f32_e32 v121, v116, v116
	v_mul_f32_e32 v121, 0xbf38aa3b, v121
	v_fma_f32 v120, |v116|, s85, 1.0
	v_exp_f32_e32 v122, v121
	v_fma_f32 v121, |v117|, s85, 1.0
	v_rcp_f32_e32 v120, v120
	v_rcp_f32_e32 v121, v121
	v_mul_f32_e32 v123, 0xbf38aa3b, v123
	v_exp_f32_e32 v123, v123
	v_mul_f32 v118, v114, v118
	v_mul_f32 v119, v115, v119
	v_fma_f32 v124, v120, s26, v142
	v_fma_f32 v125, v121, s26, v142
	s_nop 0
	v_fma_f32 v124, v120, v124, s30
	v_fma_f32 v125, v121, v125, s30
	s_nop 0
	v_fma_f32 v124, v120, v124, s34
	v_fma_f32 v125, v121, v125, s34
	s_nop 0
	v_fma_f32 v124, v120, v124, s36
	v_fma_f32 v125, v121, v125, s36
	s_nop 0
	v_mul_f32 v120, v120, v124
	v_mul_f32 v121, v121, v125
	s_nop 0
	v_mul_f32 v120, v122, v120
	v_mul_f32 v121, v123, v121
	v_sub_f32_e32 v123, v115, v119
	v_mul_f32 v120, v116, v120
	v_mul_f32 v121, v117, v121
	v_sub_f32_e32 v122, v114, v118
	v_sub_f32_e32 v125, v117, v121
	v_sub_f32_e32 v124, v116, v120
	v_cndmask_b32_e32 v145, v125, v121, vcc
	v_cmp_gt_f32_e32 vcc, 0, v116
	s_nop 1
	v_cndmask_b32_e32 v144, v124, v120, vcc
	v_cmp_gt_f32_e32 vcc, 0, v115
	s_nop 1
	v_cndmask_b32_e32 v143, v123, v119, vcc
	v_cmp_gt_f32_e32 vcc, 0, v114
	s_nop 1
	v_cndmask_b32_e32 v142, v122, v118, vcc
.LBB0_153:
	v_cvt_pk_bf16_f32 v114, v130, v131
	v_cvt_pk_bf16_f32 v115, v132, v133
	s_lshl_b32 s4, s4, 8
	v_cvt_pk_bf16_f32 v116, v134, v135
	s_ashr_i32 s5, s4, 31
	v_lshl_add_u32 v168, s54, 8, v164
	v_lshl_add_u64 v[162:163], s[4:5], 1, v[154:155]
	v_mad_i64_i32 v[118:119], s[4:5], v168, s86, v[162:163]
	v_cvt_pk_bf16_f32 v117, v136, v137
	global_store_dwordx4 v[118:119], v[114:117], off
	s_nop 1
	v_cvt_pk_bf16_f32 v114, v138, v139
	v_cvt_pk_bf16_f32 v115, v140, v141
	v_cvt_pk_bf16_f32 v116, v142, v143
	v_cvt_pk_bf16_f32 v117, v144, v145
	global_store_dwordx4 v[118:119], v[114:117], off offset:256
	s_andn2_b64 vcc, exec, s[62:63]
	s_mov_b64 s[38:39], -1
	v_cndmask_b32_e64 v114, 0, 1, s[62:63]
	v_cmp_ne_u32_e64 s[4:5], 1, v114
	s_cbranch_vccnz .LBB0_157
	v_mov_b64_e32 v[116:117], v[112:113]
	v_mov_b64_e32 v[128:129], v[100:101]
	v_mov_b64_e32 v[124:125], v[104:105]
	v_mov_b64_e32 v[120:121], v[108:109]
	s_and_b64 vcc, exec, s[2:3]
	v_mov_b64_e32 v[114:115], v[110:111]
	v_mov_b64_e32 v[126:127], v[98:99]
	v_mov_b64_e32 v[122:123], v[102:103]
	v_mov_b64_e32 v[118:119], v[106:107]
	s_cbranch_vccnz .LBB0_156
	v_mul_f32 v116, v112, s24
	v_mul_f32 v117, v113, s24
	v_mul_f32 v114, v110, s24
	v_mul_f32 v115, v111, s24
	v_mul_f32 v120, v108, s24
	v_mul_f32 v121, v109, s24
	v_mul_f32 v118, v106, s24
	v_mul_f32 v119, v107, s24
	v_mul_f32 v124, v104, s24
	v_mul_f32 v125, v105, s24
	v_mul_f32 v122, v102, s24
	v_mul_f32 v123, v103, s24
	v_mul_f32 v128, v100, s24
	v_mul_f32 v129, v101, s24
	v_mul_f32 v126, v98, s24
	v_mul_f32 v127, v99, s24

.LBB0_157:
	s_andn2_b64 vcc, exec, s[38:39]
	s_cbranch_vccnz .LBB0_159
	v_mul_f32_e32 v115, v110, v110
	v_mul_f32_e32 v115, 0xbf38aa3b, v115
	v_fma_f32 v114, |v110|, s85, 1.0
	v_exp_f32_e32 v116, v115
	v_fma_f32 v115, |v111|, s85, 1.0
	v_rcp_f32_e32 v114, v114
	v_rcp_f32_e32 v115, v115
	v_mul_f32_e32 v117, v111, v111
	v_mov_b64_e32 v[126:127], s[28:29]
	v_mul_f32_e32 v117, 0xbf38aa3b, v117
	v_fma_f32 v118, v114, s26, v126
	v_fma_f32 v119, v115, s26, v126
	v_exp_f32_e32 v117, v117
	v_fma_f32 v118, v114, v118, s30
	v_fma_f32 v119, v115, v119, s30
	v_cmp_gt_f32_e32 vcc, 0, v113
	v_fma_f32 v118, v114, v118, s34
	v_fma_f32 v119, v115, v119, s34
	s_nop 0
	v_fma_f32 v118, v114, v118, s36
	v_fma_f32 v119, v115, v119, s36
	s_nop 0
	v_mul_f32 v114, v114, v118
	v_mul_f32 v115, v115, v119
	v_mul_f32_e32 v119, v113, v113
	v_mul_f32 v114, v116, v114
	v_mul_f32 v115, v117, v115
	v_mul_f32_e32 v117, v112, v112
	v_mul_f32_e32 v117, 0xbf38aa3b, v117
	v_fma_f32 v116, |v112|, s85, 1.0
	v_exp_f32_e32 v118, v117
	v_fma_f32 v117, |v113|, s85, 1.0
	v_rcp_f32_e32 v116, v116
	v_rcp_f32_e32 v117, v117
	v_mul_f32_e32 v119, 0xbf38aa3b, v119
	v_exp_f32_e32 v119, v119
	v_mul_f32 v114, v110, v114
	v_mul_f32 v115, v111, v115
	v_fma_f32 v120, v116, s26, v126
	v_fma_f32 v121, v117, s26, v126
	s_nop 0
	v_fma_f32 v120, v116, v120, s30
	v_fma_f32 v121, v117, v121, s30
	s_nop 0
	v_fma_f32 v120, v116, v120, s34
	v_fma_f32 v121, v117, v121, s34
	s_nop 0
	v_fma_f32 v120, v116, v120, s36
	v_fma_f32 v121, v117, v121, s36
	s_nop 0
	v_mul_f32 v116, v116, v120
	v_mul_f32 v117, v117, v121
	s_nop 0
	v_mul_f32 v116, v118, v116
	v_mul_f32 v117, v119, v117
	v_sub_f32_e32 v119, v111, v115
	v_mul_f32 v116, v112, v116
	v_mul_f32 v117, v113, v117
	v_sub_f32_e32 v118, v110, v114
	v_sub_f32_e32 v121, v113, v117
	v_sub_f32_e32 v120, v112, v116
	v_cndmask_b32_e32 v117, v121, v117, vcc
	v_cmp_gt_f32_e32 vcc, 0, v112
	v_mul_f32_e32 v113, v107, v107
	v_mul_f32_e32 v113, 0xbf38aa3b, v113
	v_cndmask_b32_e32 v116, v120, v116, vcc
	v_cmp_gt_f32_e32 vcc, 0, v111
	v_mul_f32_e32 v111, v106, v106
	v_mul_f32_e32 v111, 0xbf38aa3b, v111
	v_cndmask_b32_e32 v115, v119, v115, vcc
	v_cmp_gt_f32_e32 vcc, 0, v110
	v_fma_f32 v110, |v106|, s85, 1.0
	v_exp_f32_e32 v112, v111
	v_fma_f32 v111, |v107|, s85, 1.0
	v_rcp_f32_e32 v110, v110
	v_rcp_f32_e32 v111, v111
	v_cndmask_b32_e32 v114, v118, v114, vcc
	v_exp_f32_e32 v113, v113
	v_cmp_gt_f32_e32 vcc, 0, v109
	v_fma_f32 v118, v110, s26, v126
	v_fma_f32 v119, v111, s26, v126
	s_nop 0
	v_fma_f32 v118, v110, v118, s30
	v_fma_f32 v119, v111, v119, s30
	s_nop 0
	v_fma_f32 v118, v110, v118, s34
	v_fma_f32 v119, v111, v119, s34
	s_nop 0
	v_fma_f32 v118, v110, v118, s36
	v_fma_f32 v119, v111, v119, s36
	s_nop 0
	v_mul_f32 v110, v110, v118
	v_mul_f32 v111, v111, v119
	v_mul_f32_e32 v119, v109, v109
	v_mul_f32 v110, v112, v110
	v_mul_f32 v111, v113, v111
	v_mul_f32_e32 v113, v108, v108
	v_mul_f32_e32 v113, 0xbf38aa3b, v113
	v_fma_f32 v112, |v108|, s85, 1.0
	v_exp_f32_e32 v118, v113
	v_fma_f32 v113, |v109|, s85, 1.0
	v_rcp_f32_e32 v112, v112
	v_rcp_f32_e32 v113, v113
	v_mul_f32_e32 v119, 0xbf38aa3b, v119
	v_exp_f32_e32 v119, v119
	v_mul_f32 v110, v106, v110
	v_mul_f32 v111, v107, v111
	v_fma_f32 v120, v112, s26, v126
	v_fma_f32 v121, v113, s26, v126
	s_nop 0
	v_fma_f32 v120, v112, v120, s30
	v_fma_f32 v121, v113, v121, s30
	s_nop 0
	v_fma_f32 v120, v112, v120, s34
	v_fma_f32 v121, v113, v121, s34
	s_nop 0
	v_fma_f32 v120, v112, v120, s36
	v_fma_f32 v121, v113, v121, s36
	s_nop 0
	v_mul_f32 v112, v112, v120
	v_mul_f32 v113, v113, v121
	s_nop 0
	v_mul_f32 v112, v118, v112
	v_mul_f32 v113, v119, v113
	v_sub_f32_e32 v119, v107, v111
	v_mul_f32 v112, v108, v112
	v_mul_f32 v113, v109, v113
	v_sub_f32_e32 v118, v106, v110
	v_sub_f32_e32 v121, v109, v113
	v_sub_f32_e32 v120, v108, v112
	v_cndmask_b32_e32 v121, v121, v113, vcc
	v_cmp_gt_f32_e32 vcc, 0, v108
	v_mul_f32_e32 v109, v103, v103
	v_mul_f32_e32 v109, 0xbf38aa3b, v109
	v_cndmask_b32_e32 v120, v120, v112, vcc
	v_cmp_gt_f32_e32 vcc, 0, v107
	v_mul_f32_e32 v107, v102, v102
	v_mul_f32_e32 v107, 0xbf38aa3b, v107
	v_cndmask_b32_e32 v119, v119, v111, vcc
	v_cmp_gt_f32_e32 vcc, 0, v106
	v_fma_f32 v106, |v102|, s85, 1.0
	v_exp_f32_e32 v108, v107
	v_fma_f32 v107, |v103|, s85, 1.0
	v_rcp_f32_e32 v106, v106
	v_rcp_f32_e32 v107, v107
	v_cndmask_b32_e32 v118, v118, v110, vcc
	v_exp_f32_e32 v109, v109
	v_cmp_gt_f32_e32 vcc, 0, v105
	v_fma_f32 v110, v106, s26, v126
	v_fma_f32 v111, v107, s26, v126
	s_nop 0
	v_fma_f32 v110, v106, v110, s30
	v_fma_f32 v111, v107, v111, s30
	s_nop 0
	v_fma_f32 v110, v106, v110, s34
	v_fma_f32 v111, v107, v111, s34
	s_nop 0
	v_fma_f32 v110, v106, v110, s36
	v_fma_f32 v111, v107, v111, s36
	s_nop 0
	v_mul_f32 v106, v106, v110
	v_mul_f32 v107, v107, v111
	v_mul_f32_e32 v111, v105, v105
	v_mul_f32 v106, v108, v106
	v_mul_f32 v107, v109, v107
	v_mul_f32_e32 v109, v104, v104
	v_mul_f32_e32 v109, 0xbf38aa3b, v109
	v_fma_f32 v108, |v104|, s85, 1.0
	v_exp_f32_e32 v110, v109
	v_fma_f32 v109, |v105|, s85, 1.0
	v_rcp_f32_e32 v108, v108
	v_rcp_f32_e32 v109, v109
	v_mul_f32_e32 v111, 0xbf38aa3b, v111
	v_exp_f32_e32 v111, v111
	v_mul_f32 v106, v102, v106
	v_mul_f32 v107, v103, v107
	v_fma_f32 v112, v108, s26, v126
	v_fma_f32 v113, v109, s26, v126
	s_nop 0
	v_fma_f32 v112, v108, v112, s30
	v_fma_f32 v113, v109, v113, s30
	s_nop 0
	v_fma_f32 v112, v108, v112, s34
	v_fma_f32 v113, v109, v113, s34
	s_nop 0
	v_fma_f32 v112, v108, v112, s36
	v_fma_f32 v113, v109, v113, s36
	s_nop 0
	v_mul_f32 v108, v108, v112
	v_mul_f32 v109, v109, v113
	s_nop 0
	v_mul_f32 v108, v110, v108
	v_mul_f32 v109, v111, v109
	v_sub_f32_e32 v111, v103, v107
	v_mul_f32 v108, v104, v108
	v_mul_f32 v109, v105, v109
	v_sub_f32_e32 v110, v102, v106
	v_sub_f32_e32 v113, v105, v109
	v_sub_f32_e32 v112, v104, v108
	v_cndmask_b32_e32 v125, v113, v109, vcc
	v_cmp_gt_f32_e32 vcc, 0, v104
	v_mul_f32_e32 v105, v99, v99
	v_mul_f32_e32 v105, 0xbf38aa3b, v105
	v_cndmask_b32_e32 v124, v112, v108, vcc
	v_cmp_gt_f32_e32 vcc, 0, v103
	v_mul_f32_e32 v103, v98, v98
	v_mul_f32_e32 v103, 0xbf38aa3b, v103
	v_cndmask_b32_e32 v123, v111, v107, vcc
	v_cmp_gt_f32_e32 vcc, 0, v102
	v_fma_f32 v102, |v98|, s85, 1.0
	v_exp_f32_e32 v104, v103
	v_fma_f32 v103, |v99|, s85, 1.0
	v_rcp_f32_e32 v102, v102
	v_rcp_f32_e32 v103, v103
	v_cndmask_b32_e32 v122, v110, v106, vcc
	v_exp_f32_e32 v105, v105
	v_cmp_gt_f32_e32 vcc, 0, v101
	v_fma_f32 v106, v102, s26, v126
	v_fma_f32 v107, v103, s26, v126
	s_nop 0
	v_fma_f32 v106, v102, v106, s30
	v_fma_f32 v107, v103, v107, s30
	s_nop 0
	v_fma_f32 v106, v102, v106, s34
	v_fma_f32 v107, v103, v107, s34
	s_nop 0
	v_fma_f32 v106, v102, v106, s36
	v_fma_f32 v107, v103, v107, s36
	s_nop 0
	v_mul_f32 v102, v102, v106
	v_mul_f32 v103, v103, v107
	v_mul_f32_e32 v107, v101, v101
	v_mul_f32 v102, v104, v102
	v_mul_f32 v103, v105, v103
	v_mul_f32_e32 v105, v100, v100
	v_mul_f32_e32 v105, 0xbf38aa3b, v105
	v_fma_f32 v104, |v100|, s85, 1.0
	v_exp_f32_e32 v106, v105
	v_fma_f32 v105, |v101|, s85, 1.0
	v_rcp_f32_e32 v104, v104
	v_rcp_f32_e32 v105, v105
	v_mul_f32_e32 v107, 0xbf38aa3b, v107
	v_exp_f32_e32 v107, v107
	v_mul_f32 v102, v98, v102
	v_mul_f32 v103, v99, v103
	v_fma_f32 v108, v104, s26, v126
	v_fma_f32 v109, v105, s26, v126
	s_nop 0
	v_fma_f32 v108, v104, v108, s30
	v_fma_f32 v109, v105, v109, s30
	s_nop 0
	v_fma_f32 v108, v104, v108, s34
	v_fma_f32 v109, v105, v109, s34
	s_nop 0
	v_fma_f32 v108, v104, v108, s36
	v_fma_f32 v109, v105, v109, s36
	s_nop 0
	v_mul_f32 v104, v104, v108
	v_mul_f32 v105, v105, v109
	s_nop 0
	v_mul_f32 v104, v106, v104
	v_mul_f32 v105, v107, v105
	v_sub_f32_e32 v107, v99, v103
	v_mul_f32 v104, v100, v104
	v_mul_f32 v105, v101, v105
	v_sub_f32_e32 v106, v98, v102
	v_sub_f32_e32 v109, v101, v105
	v_sub_f32_e32 v108, v100, v104
	v_cndmask_b32_e32 v129, v109, v105, vcc
	v_cmp_gt_f32_e32 vcc, 0, v100
	s_nop 1
	v_cndmask_b32_e32 v128, v108, v104, vcc
	v_cmp_gt_f32_e32 vcc, 0, v99
	s_nop 1
	v_cndmask_b32_e32 v127, v107, v103, vcc
	v_cmp_gt_f32_e32 vcc, 0, v98
	s_nop 1
	v_cndmask_b32_e32 v126, v106, v102, vcc
.LBB0_159:
	v_or_b32_e32 v98, 16, v168
	v_mad_i64_i32 v[102:103], s[38:39], v98, s86, v[162:163]
	v_cvt_pk_bf16_f32 v98, v114, v115
	v_cvt_pk_bf16_f32 v99, v116, v117
	v_cvt_pk_bf16_f32 v100, v118, v119
	v_cvt_pk_bf16_f32 v101, v120, v121
	global_store_dwordx4 v[102:103], v[98:101], off
	s_nop 1
	v_cvt_pk_bf16_f32 v98, v122, v123
	v_cvt_pk_bf16_f32 v99, v124, v125
	v_cvt_pk_bf16_f32 v100, v126, v127
	v_cvt_pk_bf16_f32 v101, v128, v129
	s_and_b64 vcc, exec, s[4:5]
	s_mov_b64 s[38:39], -1
	global_store_dwordx4 v[102:103], v[98:101], off offset:256
	s_cbranch_vccnz .LBB0_163
	s_nop 0
	v_mov_b64_e32 v[100:101], v[96:97]
	v_mov_b64_e32 v[112:113], v[84:85]
	v_mov_b64_e32 v[108:109], v[88:89]
	v_mov_b64_e32 v[104:105], v[92:93]
	s_and_b64 vcc, exec, s[2:3]
	v_mov_b64_e32 v[98:99], v[94:95]
	v_mov_b64_e32 v[110:111], v[82:83]
	v_mov_b64_e32 v[106:107], v[86:87]
	v_mov_b64_e32 v[102:103], v[90:91]
	s_cbranch_vccnz .LBB0_162
	v_mul_f32 v100, v96, s24
	v_mul_f32 v101, v97, s24
	v_mul_f32 v98, v94, s24
	v_mul_f32 v99, v95, s24
	v_mul_f32 v104, v92, s24
	v_mul_f32 v105, v93, s24
	v_mul_f32 v102, v90, s24
	v_mul_f32 v103, v91, s24
	v_mul_f32 v108, v88, s24
	v_mul_f32 v109, v89, s24
	v_mul_f32 v106, v86, s24
	v_mul_f32 v107, v87, s24
	v_mul_f32 v112, v84, s24
	v_mul_f32 v113, v85, s24
	v_mul_f32 v110, v82, s24
	v_mul_f32 v111, v83, s24

.LBB0_163:
	s_andn2_b64 vcc, exec, s[38:39]
	s_cbranch_vccnz .LBB0_165
	v_mul_f32_e32 v99, v94, v94
	v_mul_f32_e32 v99, 0xbf38aa3b, v99
	v_fma_f32 v98, |v94|, s85, 1.0
	v_exp_f32_e32 v100, v99
	v_fma_f32 v99, |v95|, s85, 1.0
	v_rcp_f32_e32 v98, v98
	v_rcp_f32_e32 v99, v99
	v_mul_f32_e32 v101, v95, v95
	v_mov_b64_e32 v[110:111], s[28:29]
	v_mul_f32_e32 v101, 0xbf38aa3b, v101
	v_fma_f32 v102, v98, s26, v110
	v_fma_f32 v103, v99, s26, v110
	v_exp_f32_e32 v101, v101
	v_fma_f32 v102, v98, v102, s30
	v_fma_f32 v103, v99, v103, s30
	v_cmp_gt_f32_e32 vcc, 0, v97
	v_fma_f32 v102, v98, v102, s34
	v_fma_f32 v103, v99, v103, s34
	s_nop 0
	v_fma_f32 v102, v98, v102, s36
	v_fma_f32 v103, v99, v103, s36
	s_nop 0
	v_mul_f32 v98, v98, v102
	v_mul_f32 v99, v99, v103
	v_mul_f32_e32 v103, v97, v97
	v_mul_f32 v98, v100, v98
	v_mul_f32 v99, v101, v99
	v_mul_f32_e32 v101, v96, v96
	v_mul_f32_e32 v101, 0xbf38aa3b, v101
	v_fma_f32 v100, |v96|, s85, 1.0
	v_exp_f32_e32 v102, v101
	v_fma_f32 v101, |v97|, s85, 1.0
	v_rcp_f32_e32 v100, v100
	v_rcp_f32_e32 v101, v101
	v_mul_f32_e32 v103, 0xbf38aa3b, v103
	v_exp_f32_e32 v103, v103
	v_mul_f32 v98, v94, v98
	v_mul_f32 v99, v95, v99
	v_fma_f32 v104, v100, s26, v110
	v_fma_f32 v105, v101, s26, v110
	s_nop 0
	v_fma_f32 v104, v100, v104, s30
	v_fma_f32 v105, v101, v105, s30
	s_nop 0
	v_fma_f32 v104, v100, v104, s34
	v_fma_f32 v105, v101, v105, s34
	s_nop 0
	v_fma_f32 v104, v100, v104, s36
	v_fma_f32 v105, v101, v105, s36
	s_nop 0
	v_mul_f32 v100, v100, v104
	v_mul_f32 v101, v101, v105
	s_nop 0
	v_mul_f32 v100, v102, v100
	v_mul_f32 v101, v103, v101
	v_sub_f32_e32 v103, v95, v99
	v_mul_f32 v100, v96, v100
	v_mul_f32 v101, v97, v101
	v_sub_f32_e32 v102, v94, v98
	v_sub_f32_e32 v105, v97, v101
	v_sub_f32_e32 v104, v96, v100
	v_cndmask_b32_e32 v101, v105, v101, vcc
	v_cmp_gt_f32_e32 vcc, 0, v96
	v_mul_f32_e32 v97, v91, v91
	v_mul_f32_e32 v97, 0xbf38aa3b, v97
	v_cndmask_b32_e32 v100, v104, v100, vcc
	v_cmp_gt_f32_e32 vcc, 0, v95
	v_mul_f32_e32 v95, v90, v90
	v_mul_f32_e32 v95, 0xbf38aa3b, v95
	v_cndmask_b32_e32 v99, v103, v99, vcc
	v_cmp_gt_f32_e32 vcc, 0, v94
	v_fma_f32 v94, |v90|, s85, 1.0
	v_exp_f32_e32 v96, v95
	v_fma_f32 v95, |v91|, s85, 1.0
	v_rcp_f32_e32 v94, v94
	v_rcp_f32_e32 v95, v95
	v_cndmask_b32_e32 v98, v102, v98, vcc
	v_exp_f32_e32 v97, v97
	v_cmp_gt_f32_e32 vcc, 0, v93
	v_fma_f32 v102, v94, s26, v110
	v_fma_f32 v103, v95, s26, v110
	s_nop 0
	v_fma_f32 v102, v94, v102, s30
	v_fma_f32 v103, v95, v103, s30
	s_nop 0
	v_fma_f32 v102, v94, v102, s34
	v_fma_f32 v103, v95, v103, s34
	s_nop 0
	v_fma_f32 v102, v94, v102, s36
	v_fma_f32 v103, v95, v103, s36
	s_nop 0
	v_mul_f32 v94, v94, v102
	v_mul_f32 v95, v95, v103
	v_mul_f32_e32 v103, v93, v93
	v_mul_f32 v94, v96, v94
	v_mul_f32 v95, v97, v95
	v_mul_f32_e32 v97, v92, v92
	v_mul_f32_e32 v97, 0xbf38aa3b, v97
	v_fma_f32 v96, |v92|, s85, 1.0
	v_exp_f32_e32 v102, v97
	v_fma_f32 v97, |v93|, s85, 1.0
	v_rcp_f32_e32 v96, v96
	v_rcp_f32_e32 v97, v97
	v_mul_f32_e32 v103, 0xbf38aa3b, v103
	v_exp_f32_e32 v103, v103
	v_mul_f32 v94, v90, v94
	v_mul_f32 v95, v91, v95
	v_fma_f32 v104, v96, s26, v110
	v_fma_f32 v105, v97, s26, v110
	s_nop 0
	v_fma_f32 v104, v96, v104, s30
	v_fma_f32 v105, v97, v105, s30
	s_nop 0
	v_fma_f32 v104, v96, v104, s34
	v_fma_f32 v105, v97, v105, s34
	s_nop 0
	v_fma_f32 v104, v96, v104, s36
	v_fma_f32 v105, v97, v105, s36
	s_nop 0
	v_mul_f32 v96, v96, v104
	v_mul_f32 v97, v97, v105
	s_nop 0
	v_mul_f32 v96, v102, v96
	v_mul_f32 v97, v103, v97
	v_sub_f32_e32 v103, v91, v95
	v_mul_f32 v96, v92, v96
	v_mul_f32 v97, v93, v97
	v_sub_f32_e32 v102, v90, v94
	v_sub_f32_e32 v105, v93, v97
	v_sub_f32_e32 v104, v92, v96
	v_cndmask_b32_e32 v105, v105, v97, vcc
	v_cmp_gt_f32_e32 vcc, 0, v92
	v_mul_f32_e32 v93, v87, v87
	v_mul_f32_e32 v93, 0xbf38aa3b, v93
	v_cndmask_b32_e32 v104, v104, v96, vcc
	v_cmp_gt_f32_e32 vcc, 0, v91
	v_mul_f32_e32 v91, v86, v86
	v_mul_f32_e32 v91, 0xbf38aa3b, v91
	v_cndmask_b32_e32 v103, v103, v95, vcc
	v_cmp_gt_f32_e32 vcc, 0, v90
	v_fma_f32 v90, |v86|, s85, 1.0
	v_exp_f32_e32 v92, v91
	v_fma_f32 v91, |v87|, s85, 1.0
	v_rcp_f32_e32 v90, v90
	v_rcp_f32_e32 v91, v91
	v_cndmask_b32_e32 v102, v102, v94, vcc
	v_exp_f32_e32 v93, v93
	v_cmp_gt_f32_e32 vcc, 0, v89
	v_fma_f32 v94, v90, s26, v110
	v_fma_f32 v95, v91, s26, v110
	s_nop 0
	v_fma_f32 v94, v90, v94, s30
	v_fma_f32 v95, v91, v95, s30
	s_nop 0
	v_fma_f32 v94, v90, v94, s34
	v_fma_f32 v95, v91, v95, s34
	s_nop 0
	v_fma_f32 v94, v90, v94, s36
	v_fma_f32 v95, v91, v95, s36
	s_nop 0
	v_mul_f32 v90, v90, v94
	v_mul_f32 v91, v91, v95
	v_mul_f32_e32 v95, v89, v89
	v_mul_f32 v90, v92, v90
	v_mul_f32 v91, v93, v91
	v_mul_f32_e32 v93, v88, v88
	v_mul_f32_e32 v93, 0xbf38aa3b, v93
	v_fma_f32 v92, |v88|, s85, 1.0
	v_exp_f32_e32 v94, v93
	v_fma_f32 v93, |v89|, s85, 1.0
	v_rcp_f32_e32 v92, v92
	v_rcp_f32_e32 v93, v93
	v_mul_f32_e32 v95, 0xbf38aa3b, v95
	v_exp_f32_e32 v95, v95
	v_mul_f32 v90, v86, v90
	v_mul_f32 v91, v87, v91
	v_fma_f32 v96, v92, s26, v110
	v_fma_f32 v97, v93, s26, v110
	s_nop 0
	v_fma_f32 v96, v92, v96, s30
	v_fma_f32 v97, v93, v97, s30
	s_nop 0
	v_fma_f32 v96, v92, v96, s34
	v_fma_f32 v97, v93, v97, s34
	s_nop 0
	v_fma_f32 v96, v92, v96, s36
	v_fma_f32 v97, v93, v97, s36
	s_nop 0
	v_mul_f32 v92, v92, v96
	v_mul_f32 v93, v93, v97
	s_nop 0
	v_mul_f32 v92, v94, v92
	v_mul_f32 v93, v95, v93
	v_sub_f32_e32 v95, v87, v91
	v_mul_f32 v92, v88, v92
	v_mul_f32 v93, v89, v93
	v_sub_f32_e32 v94, v86, v90
	v_sub_f32_e32 v97, v89, v93
	v_sub_f32_e32 v96, v88, v92
	v_cndmask_b32_e32 v109, v97, v93, vcc
	v_cmp_gt_f32_e32 vcc, 0, v88
	v_mul_f32_e32 v89, v83, v83
	v_mul_f32_e32 v89, 0xbf38aa3b, v89
	v_cndmask_b32_e32 v108, v96, v92, vcc
	v_cmp_gt_f32_e32 vcc, 0, v87
	v_mul_f32_e32 v87, v82, v82
	v_mul_f32_e32 v87, 0xbf38aa3b, v87
	v_cndmask_b32_e32 v107, v95, v91, vcc
	v_cmp_gt_f32_e32 vcc, 0, v86
	v_fma_f32 v86, |v82|, s85, 1.0
	v_exp_f32_e32 v88, v87
	v_fma_f32 v87, |v83|, s85, 1.0
	v_rcp_f32_e32 v86, v86
	v_rcp_f32_e32 v87, v87
	v_cndmask_b32_e32 v106, v94, v90, vcc
	v_exp_f32_e32 v89, v89
	v_cmp_gt_f32_e32 vcc, 0, v85
	v_fma_f32 v90, v86, s26, v110
	v_fma_f32 v91, v87, s26, v110
	s_nop 0
	v_fma_f32 v90, v86, v90, s30
	v_fma_f32 v91, v87, v91, s30
	s_nop 0
	v_fma_f32 v90, v86, v90, s34
	v_fma_f32 v91, v87, v91, s34
	s_nop 0
	v_fma_f32 v90, v86, v90, s36
	v_fma_f32 v91, v87, v91, s36
	s_nop 0
	v_mul_f32 v86, v86, v90
	v_mul_f32 v87, v87, v91
	v_mul_f32_e32 v91, v85, v85
	v_mul_f32 v86, v88, v86
	v_mul_f32 v87, v89, v87
	v_mul_f32_e32 v89, v84, v84
	v_mul_f32_e32 v89, 0xbf38aa3b, v89
	v_fma_f32 v88, |v84|, s85, 1.0
	v_exp_f32_e32 v90, v89
	v_fma_f32 v89, |v85|, s85, 1.0
	v_rcp_f32_e32 v88, v88
	v_rcp_f32_e32 v89, v89
	v_mul_f32_e32 v91, 0xbf38aa3b, v91
	v_exp_f32_e32 v91, v91
	v_mul_f32 v86, v82, v86
	v_mul_f32 v87, v83, v87
	v_fma_f32 v92, v88, s26, v110
	v_fma_f32 v93, v89, s26, v110
	s_nop 0
	v_fma_f32 v92, v88, v92, s30
	v_fma_f32 v93, v89, v93, s30
	s_nop 0
	v_fma_f32 v92, v88, v92, s34
	v_fma_f32 v93, v89, v93, s34
	s_nop 0
	v_fma_f32 v92, v88, v92, s36
	v_fma_f32 v93, v89, v93, s36
	s_nop 0
	v_mul_f32 v88, v88, v92
	v_mul_f32 v89, v89, v93
	s_nop 0
	v_mul_f32 v88, v90, v88
	v_mul_f32 v89, v91, v89
	v_sub_f32_e32 v91, v83, v87
	v_mul_f32 v88, v84, v88
	v_mul_f32 v89, v85, v89
	v_sub_f32_e32 v90, v82, v86
	v_sub_f32_e32 v93, v85, v89
	v_sub_f32_e32 v92, v84, v88
	v_cndmask_b32_e32 v113, v93, v89, vcc
	v_cmp_gt_f32_e32 vcc, 0, v84
	s_nop 1
	v_cndmask_b32_e32 v112, v92, v88, vcc
	v_cmp_gt_f32_e32 vcc, 0, v83
	s_nop 1
	v_cndmask_b32_e32 v111, v91, v87, vcc
	v_cmp_gt_f32_e32 vcc, 0, v82
	s_nop 1
	v_cndmask_b32_e32 v110, v90, v86, vcc
.LBB0_165:
	v_or_b32_e32 v82, 32, v168
	v_mad_i64_i32 v[86:87], s[38:39], v82, s86, v[162:163]
	v_cvt_pk_bf16_f32 v82, v98, v99
	v_cvt_pk_bf16_f32 v83, v100, v101
	v_cvt_pk_bf16_f32 v84, v102, v103
	v_cvt_pk_bf16_f32 v85, v104, v105
	global_store_dwordx4 v[86:87], v[82:85], off
	s_nop 1
	v_cvt_pk_bf16_f32 v82, v106, v107
	v_cvt_pk_bf16_f32 v83, v108, v109
	v_cvt_pk_bf16_f32 v84, v110, v111
	v_cvt_pk_bf16_f32 v85, v112, v113
	s_and_b64 vcc, exec, s[4:5]
	s_mov_b64 s[38:39], -1
	global_store_dwordx4 v[86:87], v[82:85], off offset:256
	s_cbranch_vccnz .LBB0_169
	s_nop 0
	v_mov_b64_e32 v[84:85], v[80:81]
	v_mov_b64_e32 v[96:97], v[68:69]
	v_mov_b64_e32 v[92:93], v[72:73]
	v_mov_b64_e32 v[88:89], v[76:77]
	s_and_b64 vcc, exec, s[2:3]
	v_mov_b64_e32 v[82:83], v[78:79]
	v_mov_b64_e32 v[94:95], v[66:67]
	v_mov_b64_e32 v[90:91], v[70:71]
	v_mov_b64_e32 v[86:87], v[74:75]
	s_cbranch_vccnz .LBB0_168
	v_mul_f32 v84, v80, s24
	v_mul_f32 v85, v81, s24
	v_mul_f32 v82, v78, s24
	v_mul_f32 v83, v79, s24
	v_mul_f32 v88, v76, s24
	v_mul_f32 v89, v77, s24
	v_mul_f32 v86, v74, s24
	v_mul_f32 v87, v75, s24
	v_mul_f32 v92, v72, s24
	v_mul_f32 v93, v73, s24
	v_mul_f32 v90, v70, s24
	v_mul_f32 v91, v71, s24
	v_mul_f32 v96, v68, s24
	v_mul_f32 v97, v69, s24
	v_mul_f32 v94, v66, s24
	v_mul_f32 v95, v67, s24

.LBB0_169:
	s_andn2_b64 vcc, exec, s[38:39]
	s_cbranch_vccnz .LBB0_171
	v_mul_f32_e32 v83, v78, v78
	v_mul_f32_e32 v83, 0xbf38aa3b, v83
	v_fma_f32 v82, |v78|, s85, 1.0
	v_exp_f32_e32 v84, v83
	v_fma_f32 v83, |v79|, s85, 1.0
	v_rcp_f32_e32 v82, v82
	v_rcp_f32_e32 v83, v83
	v_mul_f32_e32 v85, v79, v79
	v_mov_b64_e32 v[94:95], s[28:29]
	v_mul_f32_e32 v85, 0xbf38aa3b, v85
	v_fma_f32 v86, v82, s26, v94
	v_fma_f32 v87, v83, s26, v94
	v_exp_f32_e32 v85, v85
	v_fma_f32 v86, v82, v86, s30
	v_fma_f32 v87, v83, v87, s30
	v_cmp_gt_f32_e32 vcc, 0, v81
	v_fma_f32 v86, v82, v86, s34
	v_fma_f32 v87, v83, v87, s34
	s_nop 0
	v_fma_f32 v86, v82, v86, s36
	v_fma_f32 v87, v83, v87, s36
	s_nop 0
	v_mul_f32 v82, v82, v86
	v_mul_f32 v83, v83, v87
	v_mul_f32_e32 v87, v81, v81
	v_mul_f32 v82, v84, v82
	v_mul_f32 v83, v85, v83
	v_mul_f32_e32 v85, v80, v80
	v_mul_f32_e32 v85, 0xbf38aa3b, v85
	v_fma_f32 v84, |v80|, s85, 1.0
	v_exp_f32_e32 v86, v85
	v_fma_f32 v85, |v81|, s85, 1.0
	v_rcp_f32_e32 v84, v84
	v_rcp_f32_e32 v85, v85
	v_mul_f32_e32 v87, 0xbf38aa3b, v87
	v_exp_f32_e32 v87, v87
	v_mul_f32 v82, v78, v82
	v_mul_f32 v83, v79, v83
	v_fma_f32 v88, v84, s26, v94
	v_fma_f32 v89, v85, s26, v94
	s_nop 0
	v_fma_f32 v88, v84, v88, s30
	v_fma_f32 v89, v85, v89, s30
	s_nop 0
	v_fma_f32 v88, v84, v88, s34
	v_fma_f32 v89, v85, v89, s34
	s_nop 0
	v_fma_f32 v88, v84, v88, s36
	v_fma_f32 v89, v85, v89, s36
	s_nop 0
	v_mul_f32 v84, v84, v88
	v_mul_f32 v85, v85, v89
	s_nop 0
	v_mul_f32 v84, v86, v84
	v_mul_f32 v85, v87, v85
	v_sub_f32_e32 v87, v79, v83
	v_mul_f32 v84, v80, v84
	v_mul_f32 v85, v81, v85
	v_sub_f32_e32 v86, v78, v82
	v_sub_f32_e32 v89, v81, v85
	v_sub_f32_e32 v88, v80, v84
	v_cndmask_b32_e32 v85, v89, v85, vcc
	v_cmp_gt_f32_e32 vcc, 0, v80
	v_mul_f32_e32 v81, v75, v75
	v_mul_f32_e32 v81, 0xbf38aa3b, v81
	v_cndmask_b32_e32 v84, v88, v84, vcc
	v_cmp_gt_f32_e32 vcc, 0, v79
	v_mul_f32_e32 v79, v74, v74
	v_mul_f32_e32 v79, 0xbf38aa3b, v79
	v_cndmask_b32_e32 v83, v87, v83, vcc
	v_cmp_gt_f32_e32 vcc, 0, v78
	v_fma_f32 v78, |v74|, s85, 1.0
	v_exp_f32_e32 v80, v79
	v_fma_f32 v79, |v75|, s85, 1.0
	v_rcp_f32_e32 v78, v78
	v_rcp_f32_e32 v79, v79
	v_cndmask_b32_e32 v82, v86, v82, vcc
	v_exp_f32_e32 v81, v81
	v_cmp_gt_f32_e32 vcc, 0, v77
	v_fma_f32 v86, v78, s26, v94
	v_fma_f32 v87, v79, s26, v94
	s_nop 0
	v_fma_f32 v86, v78, v86, s30
	v_fma_f32 v87, v79, v87, s30
	s_nop 0
	v_fma_f32 v86, v78, v86, s34
	v_fma_f32 v87, v79, v87, s34
	s_nop 0
	v_fma_f32 v86, v78, v86, s36
	v_fma_f32 v87, v79, v87, s36
	s_nop 0
	v_mul_f32 v78, v78, v86
	v_mul_f32 v79, v79, v87
	v_mul_f32_e32 v87, v77, v77
	v_mul_f32 v78, v80, v78
	v_mul_f32 v79, v81, v79
	v_mul_f32_e32 v81, v76, v76
	v_mul_f32_e32 v81, 0xbf38aa3b, v81
	v_fma_f32 v80, |v76|, s85, 1.0
	v_exp_f32_e32 v86, v81
	v_fma_f32 v81, |v77|, s85, 1.0
	v_rcp_f32_e32 v80, v80
	v_rcp_f32_e32 v81, v81
	v_mul_f32_e32 v87, 0xbf38aa3b, v87
	v_exp_f32_e32 v87, v87
	v_mul_f32 v78, v74, v78
	v_mul_f32 v79, v75, v79
	v_fma_f32 v88, v80, s26, v94
	v_fma_f32 v89, v81, s26, v94
	s_nop 0
	v_fma_f32 v88, v80, v88, s30
	v_fma_f32 v89, v81, v89, s30
	s_nop 0
	v_fma_f32 v88, v80, v88, s34
	v_fma_f32 v89, v81, v89, s34
	s_nop 0
	v_fma_f32 v88, v80, v88, s36
	v_fma_f32 v89, v81, v89, s36
	s_nop 0
	v_mul_f32 v80, v80, v88
	v_mul_f32 v81, v81, v89
	s_nop 0
	v_mul_f32 v80, v86, v80
	v_mul_f32 v81, v87, v81
	v_sub_f32_e32 v87, v75, v79
	v_mul_f32 v80, v76, v80
	v_mul_f32 v81, v77, v81
	v_sub_f32_e32 v86, v74, v78
	v_sub_f32_e32 v89, v77, v81
	v_sub_f32_e32 v88, v76, v80
	v_cndmask_b32_e32 v89, v89, v81, vcc
	v_cmp_gt_f32_e32 vcc, 0, v76
	v_mul_f32_e32 v77, v71, v71
	v_mul_f32_e32 v77, 0xbf38aa3b, v77
	v_cndmask_b32_e32 v88, v88, v80, vcc
	v_cmp_gt_f32_e32 vcc, 0, v75
	v_mul_f32_e32 v75, v70, v70
	v_mul_f32_e32 v75, 0xbf38aa3b, v75
	v_cndmask_b32_e32 v87, v87, v79, vcc
	v_cmp_gt_f32_e32 vcc, 0, v74
	v_fma_f32 v74, |v70|, s85, 1.0
	v_exp_f32_e32 v76, v75
	v_fma_f32 v75, |v71|, s85, 1.0
	v_rcp_f32_e32 v74, v74
	v_rcp_f32_e32 v75, v75
	v_cndmask_b32_e32 v86, v86, v78, vcc
	v_exp_f32_e32 v77, v77
	v_cmp_gt_f32_e32 vcc, 0, v73
	v_fma_f32 v78, v74, s26, v94
	v_fma_f32 v79, v75, s26, v94
	s_nop 0
	v_fma_f32 v78, v74, v78, s30
	v_fma_f32 v79, v75, v79, s30
	s_nop 0
	v_fma_f32 v78, v74, v78, s34
	v_fma_f32 v79, v75, v79, s34
	s_nop 0
	v_fma_f32 v78, v74, v78, s36
	v_fma_f32 v79, v75, v79, s36
	s_nop 0
	v_mul_f32 v74, v74, v78
	v_mul_f32 v75, v75, v79
	v_mul_f32_e32 v79, v73, v73
	v_mul_f32 v74, v76, v74
	v_mul_f32 v75, v77, v75
	v_mul_f32_e32 v77, v72, v72
	v_mul_f32_e32 v77, 0xbf38aa3b, v77
	v_fma_f32 v76, |v72|, s85, 1.0
	v_exp_f32_e32 v78, v77
	v_fma_f32 v77, |v73|, s85, 1.0
	v_rcp_f32_e32 v76, v76
	v_rcp_f32_e32 v77, v77
	v_mul_f32_e32 v79, 0xbf38aa3b, v79
	v_exp_f32_e32 v79, v79
	v_mul_f32 v74, v70, v74
	v_mul_f32 v75, v71, v75
	v_fma_f32 v80, v76, s26, v94
	v_fma_f32 v81, v77, s26, v94
	s_nop 0
	v_fma_f32 v80, v76, v80, s30
	v_fma_f32 v81, v77, v81, s30
	s_nop 0
	v_fma_f32 v80, v76, v80, s34
	v_fma_f32 v81, v77, v81, s34
	s_nop 0
	v_fma_f32 v80, v76, v80, s36
	v_fma_f32 v81, v77, v81, s36
	s_nop 0
	v_mul_f32 v76, v76, v80
	v_mul_f32 v77, v77, v81
	s_nop 0
	v_mul_f32 v76, v78, v76
	v_mul_f32 v77, v79, v77
	v_sub_f32_e32 v79, v71, v75
	v_mul_f32 v76, v72, v76
	v_mul_f32 v77, v73, v77
	v_sub_f32_e32 v78, v70, v74
	v_sub_f32_e32 v81, v73, v77
	v_sub_f32_e32 v80, v72, v76
	v_cndmask_b32_e32 v93, v81, v77, vcc
	v_cmp_gt_f32_e32 vcc, 0, v72
	v_mul_f32_e32 v73, v67, v67
	v_mul_f32_e32 v73, 0xbf38aa3b, v73
	v_cndmask_b32_e32 v92, v80, v76, vcc
	v_cmp_gt_f32_e32 vcc, 0, v71
	v_mul_f32_e32 v71, v66, v66
	v_mul_f32_e32 v71, 0xbf38aa3b, v71
	v_cndmask_b32_e32 v91, v79, v75, vcc
	v_cmp_gt_f32_e32 vcc, 0, v70
	v_fma_f32 v70, |v66|, s85, 1.0
	v_exp_f32_e32 v72, v71
	v_fma_f32 v71, |v67|, s85, 1.0
	v_rcp_f32_e32 v70, v70
	v_rcp_f32_e32 v71, v71
	v_cndmask_b32_e32 v90, v78, v74, vcc
	v_exp_f32_e32 v73, v73
	v_cmp_gt_f32_e32 vcc, 0, v69
	v_fma_f32 v74, v70, s26, v94
	v_fma_f32 v75, v71, s26, v94
	s_nop 0
	v_fma_f32 v74, v70, v74, s30
	v_fma_f32 v75, v71, v75, s30
	s_nop 0
	v_fma_f32 v74, v70, v74, s34
	v_fma_f32 v75, v71, v75, s34
	s_nop 0
	v_fma_f32 v74, v70, v74, s36
	v_fma_f32 v75, v71, v75, s36
	s_nop 0
	v_mul_f32 v70, v70, v74
	v_mul_f32 v71, v71, v75
	v_mul_f32_e32 v75, v69, v69
	v_mul_f32 v70, v72, v70
	v_mul_f32 v71, v73, v71
	v_mul_f32_e32 v73, v68, v68
	v_mul_f32_e32 v73, 0xbf38aa3b, v73
	v_fma_f32 v72, |v68|, s85, 1.0
	v_exp_f32_e32 v74, v73
	v_fma_f32 v73, |v69|, s85, 1.0
	v_rcp_f32_e32 v72, v72
	v_rcp_f32_e32 v73, v73
	v_mul_f32_e32 v75, 0xbf38aa3b, v75
	v_exp_f32_e32 v75, v75
	v_mul_f32 v70, v66, v70
	v_mul_f32 v71, v67, v71
	v_fma_f32 v76, v72, s26, v94
	v_fma_f32 v77, v73, s26, v94
	s_nop 0
	v_fma_f32 v76, v72, v76, s30
	v_fma_f32 v77, v73, v77, s30
	s_nop 0
	v_fma_f32 v76, v72, v76, s34
	v_fma_f32 v77, v73, v77, s34
	s_nop 0
	v_fma_f32 v76, v72, v76, s36
	v_fma_f32 v77, v73, v77, s36
	s_nop 0
	v_mul_f32 v72, v72, v76
	v_mul_f32 v73, v73, v77
	s_nop 0
	v_mul_f32 v72, v74, v72
	v_mul_f32 v73, v75, v73
	v_sub_f32_e32 v75, v67, v71
	v_mul_f32 v72, v68, v72
	v_mul_f32 v73, v69, v73
	v_sub_f32_e32 v74, v66, v70
	v_sub_f32_e32 v77, v69, v73
	v_sub_f32_e32 v76, v68, v72
	v_cndmask_b32_e32 v97, v77, v73, vcc
	v_cmp_gt_f32_e32 vcc, 0, v68
	s_nop 1
	v_cndmask_b32_e32 v96, v76, v72, vcc
	v_cmp_gt_f32_e32 vcc, 0, v67
	s_nop 1
	v_cndmask_b32_e32 v95, v75, v71, vcc
	v_cmp_gt_f32_e32 vcc, 0, v66
	s_nop 1
	v_cndmask_b32_e32 v94, v74, v70, vcc
.LBB0_171:
	v_or_b32_e32 v66, 48, v168
	v_mad_i64_i32 v[70:71], s[38:39], v66, s86, v[162:163]
	v_cvt_pk_bf16_f32 v66, v82, v83
	v_cvt_pk_bf16_f32 v67, v84, v85
	v_cvt_pk_bf16_f32 v68, v86, v87
	v_cvt_pk_bf16_f32 v69, v88, v89
	global_store_dwordx4 v[70:71], v[66:69], off
	s_nop 1
	v_cvt_pk_bf16_f32 v66, v90, v91
	v_cvt_pk_bf16_f32 v67, v92, v93
	v_cvt_pk_bf16_f32 v68, v94, v95
	v_cvt_pk_bf16_f32 v69, v96, v97
	s_and_b64 vcc, exec, s[4:5]
	s_mov_b64 s[38:39], -1
	global_store_dwordx4 v[70:71], v[66:69], off offset:256
	s_cbranch_vccnz .LBB0_175
	s_nop 0
	v_mov_b64_e32 v[68:69], v[64:65]
	v_mov_b64_e32 v[80:81], v[52:53]
	v_mov_b64_e32 v[76:77], v[56:57]
	v_mov_b64_e32 v[72:73], v[60:61]
	s_and_b64 vcc, exec, s[2:3]
	v_mov_b64_e32 v[66:67], v[62:63]
	v_mov_b64_e32 v[78:79], v[50:51]
	v_mov_b64_e32 v[74:75], v[54:55]
	v_mov_b64_e32 v[70:71], v[58:59]
	s_cbranch_vccnz .LBB0_174
	v_mul_f32 v68, v64, s24
	v_mul_f32 v69, v65, s24
	v_mul_f32 v66, v62, s24
	v_mul_f32 v67, v63, s24
	v_mul_f32 v72, v60, s24
	v_mul_f32 v73, v61, s24
	v_mul_f32 v70, v58, s24
	v_mul_f32 v71, v59, s24
	v_mul_f32 v76, v56, s24
	v_mul_f32 v77, v57, s24
	v_mul_f32 v74, v54, s24
	v_mul_f32 v75, v55, s24
	v_mul_f32 v80, v52, s24
	v_mul_f32 v81, v53, s24
	v_mul_f32 v78, v50, s24
	v_mul_f32 v79, v51, s24

.LBB0_175:
	s_andn2_b64 vcc, exec, s[38:39]
	s_cbranch_vccnz .LBB0_177
	v_mul_f32_e32 v67, v62, v62
	v_mul_f32_e32 v67, 0xbf38aa3b, v67
	v_fma_f32 v66, |v62|, s85, 1.0
	v_exp_f32_e32 v68, v67
	v_fma_f32 v67, |v63|, s85, 1.0
	v_rcp_f32_e32 v66, v66
	v_rcp_f32_e32 v67, v67
	v_mul_f32_e32 v69, v63, v63
	v_mov_b64_e32 v[78:79], s[28:29]
	v_mul_f32_e32 v69, 0xbf38aa3b, v69
	v_fma_f32 v70, v66, s26, v78
	v_fma_f32 v71, v67, s26, v78
	v_exp_f32_e32 v69, v69
	v_fma_f32 v70, v66, v70, s30
	v_fma_f32 v71, v67, v71, s30
	v_cmp_gt_f32_e32 vcc, 0, v65
	v_fma_f32 v70, v66, v70, s34
	v_fma_f32 v71, v67, v71, s34
	s_nop 0
	v_fma_f32 v70, v66, v70, s36
	v_fma_f32 v71, v67, v71, s36
	s_nop 0
	v_mul_f32 v66, v66, v70
	v_mul_f32 v67, v67, v71
	v_mul_f32_e32 v71, v65, v65
	v_mul_f32 v66, v68, v66
	v_mul_f32 v67, v69, v67
	v_mul_f32_e32 v69, v64, v64
	v_mul_f32_e32 v69, 0xbf38aa3b, v69
	v_fma_f32 v68, |v64|, s85, 1.0
	v_exp_f32_e32 v70, v69
	v_fma_f32 v69, |v65|, s85, 1.0
	v_rcp_f32_e32 v68, v68
	v_rcp_f32_e32 v69, v69
	v_mul_f32_e32 v71, 0xbf38aa3b, v71
	v_exp_f32_e32 v71, v71
	v_mul_f32 v66, v62, v66
	v_mul_f32 v67, v63, v67
	v_fma_f32 v72, v68, s26, v78
	v_fma_f32 v73, v69, s26, v78
	s_nop 0
	v_fma_f32 v72, v68, v72, s30
	v_fma_f32 v73, v69, v73, s30
	s_nop 0
	v_fma_f32 v72, v68, v72, s34
	v_fma_f32 v73, v69, v73, s34
	s_nop 0
	v_fma_f32 v72, v68, v72, s36
	v_fma_f32 v73, v69, v73, s36
	s_nop 0
	v_mul_f32 v68, v68, v72
	v_mul_f32 v69, v69, v73
	s_nop 0
	v_mul_f32 v68, v70, v68
	v_mul_f32 v69, v71, v69
	v_sub_f32_e32 v71, v63, v67
	v_mul_f32 v68, v64, v68
	v_mul_f32 v69, v65, v69
	v_sub_f32_e32 v70, v62, v66
	v_sub_f32_e32 v73, v65, v69
	v_sub_f32_e32 v72, v64, v68
	v_cndmask_b32_e32 v69, v73, v69, vcc
	v_cmp_gt_f32_e32 vcc, 0, v64
	v_mul_f32_e32 v65, v59, v59
	v_mul_f32_e32 v65, 0xbf38aa3b, v65
	v_cndmask_b32_e32 v68, v72, v68, vcc
	v_cmp_gt_f32_e32 vcc, 0, v63
	v_mul_f32_e32 v63, v58, v58
	v_mul_f32_e32 v63, 0xbf38aa3b, v63
	v_cndmask_b32_e32 v67, v71, v67, vcc
	v_cmp_gt_f32_e32 vcc, 0, v62
	v_fma_f32 v62, |v58|, s85, 1.0
	v_exp_f32_e32 v64, v63
	v_fma_f32 v63, |v59|, s85, 1.0
	v_rcp_f32_e32 v62, v62
	v_rcp_f32_e32 v63, v63
	v_cndmask_b32_e32 v66, v70, v66, vcc
	v_exp_f32_e32 v65, v65
	v_cmp_gt_f32_e32 vcc, 0, v61
	v_fma_f32 v70, v62, s26, v78
	v_fma_f32 v71, v63, s26, v78
	s_nop 0
	v_fma_f32 v70, v62, v70, s30
	v_fma_f32 v71, v63, v71, s30
	s_nop 0
	v_fma_f32 v70, v62, v70, s34
	v_fma_f32 v71, v63, v71, s34
	s_nop 0
	v_fma_f32 v70, v62, v70, s36
	v_fma_f32 v71, v63, v71, s36
	s_nop 0
	v_mul_f32 v62, v62, v70
	v_mul_f32 v63, v63, v71
	v_mul_f32_e32 v71, v61, v61
	v_mul_f32 v62, v64, v62
	v_mul_f32 v63, v65, v63
	v_mul_f32_e32 v65, v60, v60
	v_mul_f32_e32 v65, 0xbf38aa3b, v65
	v_fma_f32 v64, |v60|, s85, 1.0
	v_exp_f32_e32 v70, v65
	v_fma_f32 v65, |v61|, s85, 1.0
	v_rcp_f32_e32 v64, v64
	v_rcp_f32_e32 v65, v65
	v_mul_f32_e32 v71, 0xbf38aa3b, v71
	v_exp_f32_e32 v71, v71
	v_mul_f32 v62, v58, v62
	v_mul_f32 v63, v59, v63
	v_fma_f32 v72, v64, s26, v78
	v_fma_f32 v73, v65, s26, v78
	s_nop 0
	v_fma_f32 v72, v64, v72, s30
	v_fma_f32 v73, v65, v73, s30
	s_nop 0
	v_fma_f32 v72, v64, v72, s34
	v_fma_f32 v73, v65, v73, s34
	s_nop 0
	v_fma_f32 v72, v64, v72, s36
	v_fma_f32 v73, v65, v73, s36
	s_nop 0
	v_mul_f32 v64, v64, v72
	v_mul_f32 v65, v65, v73
	s_nop 0
	v_mul_f32 v64, v70, v64
	v_mul_f32 v65, v71, v65
	v_sub_f32_e32 v71, v59, v63
	v_mul_f32 v64, v60, v64
	v_mul_f32 v65, v61, v65
	v_sub_f32_e32 v70, v58, v62
	v_sub_f32_e32 v73, v61, v65
	v_sub_f32_e32 v72, v60, v64
	v_cndmask_b32_e32 v73, v73, v65, vcc
	v_cmp_gt_f32_e32 vcc, 0, v60
	v_mul_f32_e32 v61, v55, v55
	v_mul_f32_e32 v61, 0xbf38aa3b, v61
	v_cndmask_b32_e32 v72, v72, v64, vcc
	v_cmp_gt_f32_e32 vcc, 0, v59
	v_mul_f32_e32 v59, v54, v54
	v_mul_f32_e32 v59, 0xbf38aa3b, v59
	v_cndmask_b32_e32 v71, v71, v63, vcc
	v_cmp_gt_f32_e32 vcc, 0, v58
	v_fma_f32 v58, |v54|, s85, 1.0
	v_exp_f32_e32 v60, v59
	v_fma_f32 v59, |v55|, s85, 1.0
	v_rcp_f32_e32 v58, v58
	v_rcp_f32_e32 v59, v59
	v_cndmask_b32_e32 v70, v70, v62, vcc
	v_exp_f32_e32 v61, v61
	v_cmp_gt_f32_e32 vcc, 0, v57
	v_fma_f32 v62, v58, s26, v78
	v_fma_f32 v63, v59, s26, v78
	s_nop 0
	v_fma_f32 v62, v58, v62, s30
	v_fma_f32 v63, v59, v63, s30
	s_nop 0
	v_fma_f32 v62, v58, v62, s34
	v_fma_f32 v63, v59, v63, s34
	s_nop 0
	v_fma_f32 v62, v58, v62, s36
	v_fma_f32 v63, v59, v63, s36
	s_nop 0
	v_mul_f32 v58, v58, v62
	v_mul_f32 v59, v59, v63
	v_mul_f32_e32 v63, v57, v57
	v_mul_f32 v58, v60, v58
	v_mul_f32 v59, v61, v59
	v_mul_f32_e32 v61, v56, v56
	v_mul_f32_e32 v61, 0xbf38aa3b, v61
	v_fma_f32 v60, |v56|, s85, 1.0
	v_exp_f32_e32 v62, v61
	v_fma_f32 v61, |v57|, s85, 1.0
	v_rcp_f32_e32 v60, v60
	v_rcp_f32_e32 v61, v61
	v_mul_f32_e32 v63, 0xbf38aa3b, v63
	v_exp_f32_e32 v63, v63
	v_mul_f32 v58, v54, v58
	v_mul_f32 v59, v55, v59
	v_fma_f32 v64, v60, s26, v78
	v_fma_f32 v65, v61, s26, v78
	s_nop 0
	v_fma_f32 v64, v60, v64, s30
	v_fma_f32 v65, v61, v65, s30
	s_nop 0
	v_fma_f32 v64, v60, v64, s34
	v_fma_f32 v65, v61, v65, s34
	s_nop 0
	v_fma_f32 v64, v60, v64, s36
	v_fma_f32 v65, v61, v65, s36
	s_nop 0
	v_mul_f32 v60, v60, v64
	v_mul_f32 v61, v61, v65
	s_nop 0
	v_mul_f32 v60, v62, v60
	v_mul_f32 v61, v63, v61
	v_sub_f32_e32 v63, v55, v59
	v_mul_f32 v60, v56, v60
	v_mul_f32 v61, v57, v61
	v_sub_f32_e32 v62, v54, v58
	v_sub_f32_e32 v65, v57, v61
	v_sub_f32_e32 v64, v56, v60
	v_cndmask_b32_e32 v77, v65, v61, vcc
	v_cmp_gt_f32_e32 vcc, 0, v56
	v_mul_f32_e32 v57, v51, v51
	v_mul_f32_e32 v57, 0xbf38aa3b, v57
	v_cndmask_b32_e32 v76, v64, v60, vcc
	v_cmp_gt_f32_e32 vcc, 0, v55
	v_mul_f32_e32 v55, v50, v50
	v_mul_f32_e32 v55, 0xbf38aa3b, v55
	v_cndmask_b32_e32 v75, v63, v59, vcc
	v_cmp_gt_f32_e32 vcc, 0, v54
	v_fma_f32 v54, |v50|, s85, 1.0
	v_exp_f32_e32 v56, v55
	v_fma_f32 v55, |v51|, s85, 1.0
	v_rcp_f32_e32 v54, v54
	v_rcp_f32_e32 v55, v55
	v_cndmask_b32_e32 v74, v62, v58, vcc
	v_exp_f32_e32 v57, v57
	v_cmp_gt_f32_e32 vcc, 0, v53
	v_fma_f32 v58, v54, s26, v78
	v_fma_f32 v59, v55, s26, v78
	s_nop 0
	v_fma_f32 v58, v54, v58, s30
	v_fma_f32 v59, v55, v59, s30
	s_nop 0
	v_fma_f32 v58, v54, v58, s34
	v_fma_f32 v59, v55, v59, s34
	s_nop 0
	v_fma_f32 v58, v54, v58, s36
	v_fma_f32 v59, v55, v59, s36
	s_nop 0
	v_mul_f32 v54, v54, v58
	v_mul_f32 v55, v55, v59
	v_mul_f32_e32 v59, v53, v53
	v_mul_f32 v54, v56, v54
	v_mul_f32 v55, v57, v55
	v_mul_f32_e32 v57, v52, v52
	v_mul_f32_e32 v57, 0xbf38aa3b, v57
	v_fma_f32 v56, |v52|, s85, 1.0
	v_exp_f32_e32 v58, v57
	v_fma_f32 v57, |v53|, s85, 1.0
	v_rcp_f32_e32 v56, v56
	v_rcp_f32_e32 v57, v57
	v_mul_f32_e32 v59, 0xbf38aa3b, v59
	v_exp_f32_e32 v59, v59
	v_mul_f32 v54, v50, v54
	v_mul_f32 v55, v51, v55
	v_fma_f32 v60, v56, s26, v78
	v_fma_f32 v61, v57, s26, v78
	s_nop 0
	v_fma_f32 v60, v56, v60, s30
	v_fma_f32 v61, v57, v61, s30
	s_nop 0
	v_fma_f32 v60, v56, v60, s34
	v_fma_f32 v61, v57, v61, s34
	s_nop 0
	v_fma_f32 v60, v56, v60, s36
	v_fma_f32 v61, v57, v61, s36
	s_nop 0
	v_mul_f32 v56, v56, v60
	v_mul_f32 v57, v57, v61
	s_nop 0
	v_mul_f32 v56, v58, v56
	v_mul_f32 v57, v59, v57
	v_sub_f32_e32 v59, v51, v55
	v_mul_f32 v56, v52, v56
	v_mul_f32 v57, v53, v57
	v_sub_f32_e32 v58, v50, v54
	v_sub_f32_e32 v61, v53, v57
	v_sub_f32_e32 v60, v52, v56
	v_cndmask_b32_e32 v81, v61, v57, vcc
	v_cmp_gt_f32_e32 vcc, 0, v52
	s_nop 1
	v_cndmask_b32_e32 v80, v60, v56, vcc
	v_cmp_gt_f32_e32 vcc, 0, v51
	s_nop 1
	v_cndmask_b32_e32 v79, v59, v55, vcc
	v_cmp_gt_f32_e32 vcc, 0, v50
	s_nop 1
	v_cndmask_b32_e32 v78, v58, v54, vcc
.LBB0_177:
	v_add_u32_e32 v50, 0x80, v168
	v_mad_i64_i32 v[54:55], s[38:39], v50, s86, v[162:163]
	v_cvt_pk_bf16_f32 v50, v66, v67
	v_cvt_pk_bf16_f32 v51, v68, v69
	v_cvt_pk_bf16_f32 v52, v70, v71
	v_cvt_pk_bf16_f32 v53, v72, v73
	global_store_dwordx4 v[54:55], v[50:53], off
	s_nop 1
	v_cvt_pk_bf16_f32 v50, v74, v75
	v_cvt_pk_bf16_f32 v51, v76, v77
	v_cvt_pk_bf16_f32 v52, v78, v79
	v_cvt_pk_bf16_f32 v53, v80, v81
	s_and_b64 vcc, exec, s[4:5]
	s_mov_b64 s[38:39], -1
	global_store_dwordx4 v[54:55], v[50:53], off offset:256
	s_cbranch_vccnz .LBB0_181
	s_nop 0
	v_mov_b64_e32 v[52:53], v[48:49]
	v_mov_b64_e32 v[64:65], v[36:37]
	v_mov_b64_e32 v[60:61], v[40:41]
	v_mov_b64_e32 v[56:57], v[44:45]
	s_and_b64 vcc, exec, s[2:3]
	v_mov_b64_e32 v[50:51], v[46:47]
	v_mov_b64_e32 v[62:63], v[34:35]
	v_mov_b64_e32 v[58:59], v[38:39]
	v_mov_b64_e32 v[54:55], v[42:43]
	s_cbranch_vccnz .LBB0_180
	v_mul_f32 v52, v48, s24
	v_mul_f32 v53, v49, s24
	v_mul_f32 v50, v46, s24
	v_mul_f32 v51, v47, s24
	v_mul_f32 v56, v44, s24
	v_mul_f32 v57, v45, s24
	v_mul_f32 v54, v42, s24
	v_mul_f32 v55, v43, s24
	v_mul_f32 v60, v40, s24
	v_mul_f32 v61, v41, s24
	v_mul_f32 v58, v38, s24
	v_mul_f32 v59, v39, s24
	v_mul_f32 v64, v36, s24
	v_mul_f32 v65, v37, s24
	v_mul_f32 v62, v34, s24
	v_mul_f32 v63, v35, s24

.LBB0_181:
	s_andn2_b64 vcc, exec, s[38:39]
	s_cbranch_vccnz .LBB0_183
	v_mul_f32_e32 v51, v46, v46
	v_mul_f32_e32 v51, 0xbf38aa3b, v51
	v_fma_f32 v50, |v46|, s85, 1.0
	v_exp_f32_e32 v52, v51
	v_fma_f32 v51, |v47|, s85, 1.0
	v_rcp_f32_e32 v50, v50
	v_rcp_f32_e32 v51, v51
	v_mul_f32_e32 v53, v47, v47
	v_mov_b64_e32 v[62:63], s[28:29]
	v_mul_f32_e32 v53, 0xbf38aa3b, v53
	v_fma_f32 v54, v50, s26, v62
	v_fma_f32 v55, v51, s26, v62
	v_exp_f32_e32 v53, v53
	v_fma_f32 v54, v50, v54, s30
	v_fma_f32 v55, v51, v55, s30
	v_cmp_gt_f32_e32 vcc, 0, v49
	v_fma_f32 v54, v50, v54, s34
	v_fma_f32 v55, v51, v55, s34
	s_nop 0
	v_fma_f32 v54, v50, v54, s36
	v_fma_f32 v55, v51, v55, s36
	s_nop 0
	v_mul_f32 v50, v50, v54
	v_mul_f32 v51, v51, v55
	v_mul_f32_e32 v55, v49, v49
	v_mul_f32 v50, v52, v50
	v_mul_f32 v51, v53, v51
	v_mul_f32_e32 v53, v48, v48
	v_mul_f32_e32 v53, 0xbf38aa3b, v53
	v_fma_f32 v52, |v48|, s85, 1.0
	v_exp_f32_e32 v54, v53
	v_fma_f32 v53, |v49|, s85, 1.0
	v_rcp_f32_e32 v52, v52
	v_rcp_f32_e32 v53, v53
	v_mul_f32_e32 v55, 0xbf38aa3b, v55
	v_exp_f32_e32 v55, v55
	v_mul_f32 v50, v46, v50
	v_mul_f32 v51, v47, v51
	v_fma_f32 v56, v52, s26, v62
	v_fma_f32 v57, v53, s26, v62
	s_nop 0
	v_fma_f32 v56, v52, v56, s30
	v_fma_f32 v57, v53, v57, s30
	s_nop 0
	v_fma_f32 v56, v52, v56, s34
	v_fma_f32 v57, v53, v57, s34
	s_nop 0
	v_fma_f32 v56, v52, v56, s36
	v_fma_f32 v57, v53, v57, s36
	s_nop 0
	v_mul_f32 v52, v52, v56
	v_mul_f32 v53, v53, v57
	s_nop 0
	v_mul_f32 v52, v54, v52
	v_mul_f32 v53, v55, v53
	v_sub_f32_e32 v55, v47, v51
	v_mul_f32 v52, v48, v52
	v_mul_f32 v53, v49, v53
	v_sub_f32_e32 v54, v46, v50
	v_sub_f32_e32 v57, v49, v53
	v_sub_f32_e32 v56, v48, v52
	v_cndmask_b32_e32 v53, v57, v53, vcc
	v_cmp_gt_f32_e32 vcc, 0, v48
	v_mul_f32_e32 v49, v43, v43
	v_mul_f32_e32 v49, 0xbf38aa3b, v49
	v_cndmask_b32_e32 v52, v56, v52, vcc
	v_cmp_gt_f32_e32 vcc, 0, v47
	v_mul_f32_e32 v47, v42, v42
	v_mul_f32_e32 v47, 0xbf38aa3b, v47
	v_cndmask_b32_e32 v51, v55, v51, vcc
	v_cmp_gt_f32_e32 vcc, 0, v46
	v_fma_f32 v46, |v42|, s85, 1.0
	v_exp_f32_e32 v48, v47
	v_fma_f32 v47, |v43|, s85, 1.0
	v_rcp_f32_e32 v46, v46
	v_rcp_f32_e32 v47, v47
	v_cndmask_b32_e32 v50, v54, v50, vcc
	v_exp_f32_e32 v49, v49
	v_cmp_gt_f32_e32 vcc, 0, v45
	v_fma_f32 v54, v46, s26, v62
	v_fma_f32 v55, v47, s26, v62
	s_nop 0
	v_fma_f32 v54, v46, v54, s30
	v_fma_f32 v55, v47, v55, s30
	s_nop 0
	v_fma_f32 v54, v46, v54, s34
	v_fma_f32 v55, v47, v55, s34
	s_nop 0
	v_fma_f32 v54, v46, v54, s36
	v_fma_f32 v55, v47, v55, s36
	s_nop 0
	v_mul_f32 v46, v46, v54
	v_mul_f32 v47, v47, v55
	v_mul_f32_e32 v55, v45, v45
	v_mul_f32 v46, v48, v46
	v_mul_f32 v47, v49, v47
	v_mul_f32_e32 v49, v44, v44
	v_mul_f32_e32 v49, 0xbf38aa3b, v49
	v_fma_f32 v48, |v44|, s85, 1.0
	v_exp_f32_e32 v54, v49
	v_fma_f32 v49, |v45|, s85, 1.0
	v_rcp_f32_e32 v48, v48
	v_rcp_f32_e32 v49, v49
	v_mul_f32_e32 v55, 0xbf38aa3b, v55
	v_exp_f32_e32 v55, v55
	v_mul_f32 v46, v42, v46
	v_mul_f32 v47, v43, v47
	v_fma_f32 v56, v48, s26, v62
	v_fma_f32 v57, v49, s26, v62
	s_nop 0
	v_fma_f32 v56, v48, v56, s30
	v_fma_f32 v57, v49, v57, s30
	s_nop 0
	v_fma_f32 v56, v48, v56, s34
	v_fma_f32 v57, v49, v57, s34
	s_nop 0
	v_fma_f32 v56, v48, v56, s36
	v_fma_f32 v57, v49, v57, s36
	s_nop 0
	v_mul_f32 v48, v48, v56
	v_mul_f32 v49, v49, v57
	s_nop 0
	v_mul_f32 v48, v54, v48
	v_mul_f32 v49, v55, v49
	v_sub_f32_e32 v55, v43, v47
	v_mul_f32 v48, v44, v48
	v_mul_f32 v49, v45, v49
	v_sub_f32_e32 v54, v42, v46
	v_sub_f32_e32 v57, v45, v49
	v_sub_f32_e32 v56, v44, v48
	v_cndmask_b32_e32 v57, v57, v49, vcc
	v_cmp_gt_f32_e32 vcc, 0, v44
	v_mul_f32_e32 v45, v39, v39
	v_mul_f32_e32 v45, 0xbf38aa3b, v45
	v_cndmask_b32_e32 v56, v56, v48, vcc
	v_cmp_gt_f32_e32 vcc, 0, v43
	v_mul_f32_e32 v43, v38, v38
	v_mul_f32_e32 v43, 0xbf38aa3b, v43
	v_cndmask_b32_e32 v55, v55, v47, vcc
	v_cmp_gt_f32_e32 vcc, 0, v42
	v_fma_f32 v42, |v38|, s85, 1.0
	v_exp_f32_e32 v44, v43
	v_fma_f32 v43, |v39|, s85, 1.0
	v_rcp_f32_e32 v42, v42
	v_rcp_f32_e32 v43, v43
	v_cndmask_b32_e32 v54, v54, v46, vcc
	v_exp_f32_e32 v45, v45
	v_cmp_gt_f32_e32 vcc, 0, v41
	v_fma_f32 v46, v42, s26, v62
	v_fma_f32 v47, v43, s26, v62
	s_nop 0
	v_fma_f32 v46, v42, v46, s30
	v_fma_f32 v47, v43, v47, s30
	s_nop 0
	v_fma_f32 v46, v42, v46, s34
	v_fma_f32 v47, v43, v47, s34
	s_nop 0
	v_fma_f32 v46, v42, v46, s36
	v_fma_f32 v47, v43, v47, s36
	s_nop 0
	v_mul_f32 v42, v42, v46
	v_mul_f32 v43, v43, v47
	v_mul_f32_e32 v47, v41, v41
	v_mul_f32 v42, v44, v42
	v_mul_f32 v43, v45, v43
	v_mul_f32_e32 v45, v40, v40
	v_mul_f32_e32 v45, 0xbf38aa3b, v45
	v_fma_f32 v44, |v40|, s85, 1.0
	v_exp_f32_e32 v46, v45
	v_fma_f32 v45, |v41|, s85, 1.0
	v_rcp_f32_e32 v44, v44
	v_rcp_f32_e32 v45, v45
	v_mul_f32_e32 v47, 0xbf38aa3b, v47
	v_exp_f32_e32 v47, v47
	v_mul_f32 v42, v38, v42
	v_mul_f32 v43, v39, v43
	v_fma_f32 v48, v44, s26, v62
	v_fma_f32 v49, v45, s26, v62
	s_nop 0
	v_fma_f32 v48, v44, v48, s30
	v_fma_f32 v49, v45, v49, s30
	s_nop 0
	v_fma_f32 v48, v44, v48, s34
	v_fma_f32 v49, v45, v49, s34
	s_nop 0
	v_fma_f32 v48, v44, v48, s36
	v_fma_f32 v49, v45, v49, s36
	s_nop 0
	v_mul_f32 v44, v44, v48
	v_mul_f32 v45, v45, v49
	s_nop 0
	v_mul_f32 v44, v46, v44
	v_mul_f32 v45, v47, v45
	v_sub_f32_e32 v47, v39, v43
	v_mul_f32 v44, v40, v44
	v_mul_f32 v45, v41, v45
	v_sub_f32_e32 v46, v38, v42
	v_sub_f32_e32 v49, v41, v45
	v_sub_f32_e32 v48, v40, v44
	v_cndmask_b32_e32 v61, v49, v45, vcc
	v_cmp_gt_f32_e32 vcc, 0, v40
	v_mul_f32_e32 v41, v35, v35
	v_mul_f32_e32 v41, 0xbf38aa3b, v41
	v_cndmask_b32_e32 v60, v48, v44, vcc
	v_cmp_gt_f32_e32 vcc, 0, v39
	v_mul_f32_e32 v39, v34, v34
	v_mul_f32_e32 v39, 0xbf38aa3b, v39
	v_cndmask_b32_e32 v59, v47, v43, vcc
	v_cmp_gt_f32_e32 vcc, 0, v38
	v_fma_f32 v38, |v34|, s85, 1.0
	v_exp_f32_e32 v40, v39
	v_fma_f32 v39, |v35|, s85, 1.0
	v_rcp_f32_e32 v38, v38
	v_rcp_f32_e32 v39, v39
	v_cndmask_b32_e32 v58, v46, v42, vcc
	v_exp_f32_e32 v41, v41
	v_cmp_gt_f32_e32 vcc, 0, v37
	v_fma_f32 v42, v38, s26, v62
	v_fma_f32 v43, v39, s26, v62
	s_nop 0
	v_fma_f32 v42, v38, v42, s30
	v_fma_f32 v43, v39, v43, s30
	s_nop 0
	v_fma_f32 v42, v38, v42, s34
	v_fma_f32 v43, v39, v43, s34
	s_nop 0
	v_fma_f32 v42, v38, v42, s36
	v_fma_f32 v43, v39, v43, s36
	s_nop 0
	v_mul_f32 v38, v38, v42
	v_mul_f32 v39, v39, v43
	v_mul_f32_e32 v43, v37, v37
	v_mul_f32 v38, v40, v38
	v_mul_f32 v39, v41, v39
	v_mul_f32_e32 v41, v36, v36
	v_mul_f32_e32 v41, 0xbf38aa3b, v41
	v_fma_f32 v40, |v36|, s85, 1.0
	v_exp_f32_e32 v42, v41
	v_fma_f32 v41, |v37|, s85, 1.0
	v_rcp_f32_e32 v40, v40
	v_rcp_f32_e32 v41, v41
	v_mul_f32_e32 v43, 0xbf38aa3b, v43
	v_exp_f32_e32 v43, v43
	v_mul_f32 v38, v34, v38
	v_mul_f32 v39, v35, v39
	v_fma_f32 v44, v40, s26, v62
	v_fma_f32 v45, v41, s26, v62
	s_nop 0
	v_fma_f32 v44, v40, v44, s30
	v_fma_f32 v45, v41, v45, s30
	s_nop 0
	v_fma_f32 v44, v40, v44, s34
	v_fma_f32 v45, v41, v45, s34
	s_nop 0
	v_fma_f32 v44, v40, v44, s36
	v_fma_f32 v45, v41, v45, s36
	s_nop 0
	v_mul_f32 v40, v40, v44
	v_mul_f32 v41, v41, v45
	s_nop 0
	v_mul_f32 v40, v42, v40
	v_mul_f32 v41, v43, v41
	v_sub_f32_e32 v43, v35, v39
	v_mul_f32 v40, v36, v40
	v_mul_f32 v41, v37, v41
	v_sub_f32_e32 v42, v34, v38
	v_sub_f32_e32 v45, v37, v41
	v_sub_f32_e32 v44, v36, v40
	v_cndmask_b32_e32 v65, v45, v41, vcc
	v_cmp_gt_f32_e32 vcc, 0, v36
	s_nop 1
	v_cndmask_b32_e32 v64, v44, v40, vcc
	v_cmp_gt_f32_e32 vcc, 0, v35
	s_nop 1
	v_cndmask_b32_e32 v63, v43, v39, vcc
	v_cmp_gt_f32_e32 vcc, 0, v34
	s_nop 1
	v_cndmask_b32_e32 v62, v42, v38, vcc
.LBB0_183:
	v_add_u32_e32 v34, 0x90, v168
	v_mad_i64_i32 v[38:39], s[38:39], v34, s86, v[162:163]
	v_cvt_pk_bf16_f32 v34, v50, v51
	v_cvt_pk_bf16_f32 v35, v52, v53
	v_cvt_pk_bf16_f32 v36, v54, v55
	v_cvt_pk_bf16_f32 v37, v56, v57
	global_store_dwordx4 v[38:39], v[34:37], off
	s_nop 1
	v_cvt_pk_bf16_f32 v34, v58, v59
	v_cvt_pk_bf16_f32 v35, v60, v61
	v_cvt_pk_bf16_f32 v36, v62, v63
	v_cvt_pk_bf16_f32 v37, v64, v65
	s_and_b64 vcc, exec, s[4:5]
	s_mov_b64 s[38:39], -1
	global_store_dwordx4 v[38:39], v[34:37], off offset:256
	s_cbranch_vccnz .LBB0_187
	s_nop 0
	v_mov_b64_e32 v[36:37], v[32:33]
	v_mov_b64_e32 v[48:49], v[20:21]
	v_mov_b64_e32 v[44:45], v[24:25]
	v_mov_b64_e32 v[40:41], v[28:29]
	s_and_b64 vcc, exec, s[2:3]
	v_mov_b64_e32 v[34:35], v[30:31]
	v_mov_b64_e32 v[46:47], v[18:19]
	v_mov_b64_e32 v[42:43], v[22:23]
	v_mov_b64_e32 v[38:39], v[26:27]
	s_cbranch_vccnz .LBB0_186
	v_mul_f32 v36, v32, s24
	v_mul_f32 v37, v33, s24
	v_mul_f32 v34, v30, s24
	v_mul_f32 v35, v31, s24
	v_mul_f32 v40, v28, s24
	v_mul_f32 v41, v29, s24
	v_mul_f32 v38, v26, s24
	v_mul_f32 v39, v27, s24
	v_mul_f32 v44, v24, s24
	v_mul_f32 v45, v25, s24
	v_mul_f32 v42, v22, s24
	v_mul_f32 v43, v23, s24
	v_mul_f32 v48, v20, s24
	v_mul_f32 v49, v21, s24
	v_mul_f32 v46, v18, s24
	v_mul_f32 v47, v19, s24

.LBB0_187:
	s_andn2_b64 vcc, exec, s[38:39]
	s_cbranch_vccnz .LBB0_189
	v_mul_f32_e32 v35, v30, v30
	v_mul_f32_e32 v35, 0xbf38aa3b, v35
	v_fma_f32 v34, |v30|, s85, 1.0
	v_exp_f32_e32 v36, v35
	v_fma_f32 v35, |v31|, s85, 1.0
	v_rcp_f32_e32 v34, v34
	v_rcp_f32_e32 v35, v35
	v_mul_f32_e32 v37, v31, v31
	v_mov_b64_e32 v[46:47], s[28:29]
	v_mul_f32_e32 v37, 0xbf38aa3b, v37
	v_fma_f32 v38, v34, s26, v46
	v_fma_f32 v39, v35, s26, v46
	v_exp_f32_e32 v37, v37
	v_fma_f32 v38, v34, v38, s30
	v_fma_f32 v39, v35, v39, s30
	v_cmp_gt_f32_e32 vcc, 0, v33
	v_fma_f32 v38, v34, v38, s34
	v_fma_f32 v39, v35, v39, s34
	s_nop 0
	v_fma_f32 v38, v34, v38, s36
	v_fma_f32 v39, v35, v39, s36
	s_nop 0
	v_mul_f32 v34, v34, v38
	v_mul_f32 v35, v35, v39
	v_mul_f32_e32 v39, v33, v33
	v_mul_f32 v34, v36, v34
	v_mul_f32 v35, v37, v35
	v_mul_f32_e32 v37, v32, v32
	v_mul_f32_e32 v37, 0xbf38aa3b, v37
	v_fma_f32 v36, |v32|, s85, 1.0
	v_exp_f32_e32 v38, v37
	v_fma_f32 v37, |v33|, s85, 1.0
	v_rcp_f32_e32 v36, v36
	v_rcp_f32_e32 v37, v37
	v_mul_f32_e32 v39, 0xbf38aa3b, v39
	v_exp_f32_e32 v39, v39
	v_mul_f32 v34, v30, v34
	v_mul_f32 v35, v31, v35
	v_fma_f32 v40, v36, s26, v46
	v_fma_f32 v41, v37, s26, v46
	s_nop 0
	v_fma_f32 v40, v36, v40, s30
	v_fma_f32 v41, v37, v41, s30
	s_nop 0
	v_fma_f32 v40, v36, v40, s34
	v_fma_f32 v41, v37, v41, s34
	s_nop 0
	v_fma_f32 v40, v36, v40, s36
	v_fma_f32 v41, v37, v41, s36
	s_nop 0
	v_mul_f32 v36, v36, v40
	v_mul_f32 v37, v37, v41
	s_nop 0
	v_mul_f32 v36, v38, v36
	v_mul_f32 v37, v39, v37
	v_sub_f32_e32 v39, v31, v35
	v_mul_f32 v36, v32, v36
	v_mul_f32 v37, v33, v37
	v_sub_f32_e32 v38, v30, v34
	v_sub_f32_e32 v41, v33, v37
	v_sub_f32_e32 v40, v32, v36
	v_cndmask_b32_e32 v37, v41, v37, vcc
	v_cmp_gt_f32_e32 vcc, 0, v32
	v_mul_f32_e32 v33, v27, v27
	v_mul_f32_e32 v33, 0xbf38aa3b, v33
	v_cndmask_b32_e32 v36, v40, v36, vcc
	v_cmp_gt_f32_e32 vcc, 0, v31
	v_mul_f32_e32 v31, v26, v26
	v_mul_f32_e32 v31, 0xbf38aa3b, v31
	v_cndmask_b32_e32 v35, v39, v35, vcc
	v_cmp_gt_f32_e32 vcc, 0, v30
	v_fma_f32 v30, |v26|, s85, 1.0
	v_exp_f32_e32 v32, v31
	v_fma_f32 v31, |v27|, s85, 1.0
	v_rcp_f32_e32 v30, v30
	v_rcp_f32_e32 v31, v31
	v_cndmask_b32_e32 v34, v38, v34, vcc
	v_exp_f32_e32 v33, v33
	v_cmp_gt_f32_e32 vcc, 0, v29
	v_fma_f32 v38, v30, s26, v46
	v_fma_f32 v39, v31, s26, v46
	s_nop 0
	v_fma_f32 v38, v30, v38, s30
	v_fma_f32 v39, v31, v39, s30
	s_nop 0
	v_fma_f32 v38, v30, v38, s34
	v_fma_f32 v39, v31, v39, s34
	s_nop 0
	v_fma_f32 v38, v30, v38, s36
	v_fma_f32 v39, v31, v39, s36
	s_nop 0
	v_mul_f32 v30, v30, v38
	v_mul_f32 v31, v31, v39
	v_mul_f32_e32 v39, v29, v29
	v_mul_f32 v30, v32, v30
	v_mul_f32 v31, v33, v31
	v_mul_f32_e32 v33, v28, v28
	v_mul_f32_e32 v33, 0xbf38aa3b, v33
	v_fma_f32 v32, |v28|, s85, 1.0
	v_exp_f32_e32 v38, v33
	v_fma_f32 v33, |v29|, s85, 1.0
	v_rcp_f32_e32 v32, v32
	v_rcp_f32_e32 v33, v33
	v_mul_f32_e32 v39, 0xbf38aa3b, v39
	v_exp_f32_e32 v39, v39
	v_mul_f32 v30, v26, v30
	v_mul_f32 v31, v27, v31
	v_fma_f32 v40, v32, s26, v46
	v_fma_f32 v41, v33, s26, v46
	s_nop 0
	v_fma_f32 v40, v32, v40, s30
	v_fma_f32 v41, v33, v41, s30
	s_nop 0
	v_fma_f32 v40, v32, v40, s34
	v_fma_f32 v41, v33, v41, s34
	s_nop 0
	v_fma_f32 v40, v32, v40, s36
	v_fma_f32 v41, v33, v41, s36
	s_nop 0
	v_mul_f32 v32, v32, v40
	v_mul_f32 v33, v33, v41
	s_nop 0
	v_mul_f32 v32, v38, v32
	v_mul_f32 v33, v39, v33
	v_sub_f32_e32 v39, v27, v31
	v_mul_f32 v32, v28, v32
	v_mul_f32 v33, v29, v33
	v_sub_f32_e32 v38, v26, v30
	v_sub_f32_e32 v41, v29, v33
	v_sub_f32_e32 v40, v28, v32
	v_cndmask_b32_e32 v41, v41, v33, vcc
	v_cmp_gt_f32_e32 vcc, 0, v28
	v_mul_f32_e32 v29, v23, v23
	v_mul_f32_e32 v29, 0xbf38aa3b, v29
	v_cndmask_b32_e32 v40, v40, v32, vcc
	v_cmp_gt_f32_e32 vcc, 0, v27
	v_mul_f32_e32 v27, v22, v22
	v_mul_f32_e32 v27, 0xbf38aa3b, v27
	v_cndmask_b32_e32 v39, v39, v31, vcc
	v_cmp_gt_f32_e32 vcc, 0, v26
	v_fma_f32 v26, |v22|, s85, 1.0
	v_exp_f32_e32 v28, v27
	v_fma_f32 v27, |v23|, s85, 1.0
	v_rcp_f32_e32 v26, v26
	v_rcp_f32_e32 v27, v27
	v_cndmask_b32_e32 v38, v38, v30, vcc
	v_exp_f32_e32 v29, v29
	v_cmp_gt_f32_e32 vcc, 0, v25
	v_fma_f32 v30, v26, s26, v46
	v_fma_f32 v31, v27, s26, v46
	s_nop 0
	v_fma_f32 v30, v26, v30, s30
	v_fma_f32 v31, v27, v31, s30
	s_nop 0
	v_fma_f32 v30, v26, v30, s34
	v_fma_f32 v31, v27, v31, s34
	s_nop 0
	v_fma_f32 v30, v26, v30, s36
	v_fma_f32 v31, v27, v31, s36
	s_nop 0
	v_mul_f32 v26, v26, v30
	v_mul_f32 v27, v27, v31
	v_mul_f32_e32 v31, v25, v25
	v_mul_f32 v26, v28, v26
	v_mul_f32 v27, v29, v27
	v_mul_f32_e32 v29, v24, v24
	v_mul_f32_e32 v29, 0xbf38aa3b, v29
	v_fma_f32 v28, |v24|, s85, 1.0
	v_exp_f32_e32 v30, v29
	v_fma_f32 v29, |v25|, s85, 1.0
	v_rcp_f32_e32 v28, v28
	v_rcp_f32_e32 v29, v29
	v_mul_f32_e32 v31, 0xbf38aa3b, v31
	v_exp_f32_e32 v31, v31
	v_mul_f32 v26, v22, v26
	v_mul_f32 v27, v23, v27
	v_fma_f32 v32, v28, s26, v46
	v_fma_f32 v33, v29, s26, v46
	s_nop 0
	v_fma_f32 v32, v28, v32, s30
	v_fma_f32 v33, v29, v33, s30
	s_nop 0
	v_fma_f32 v32, v28, v32, s34
	v_fma_f32 v33, v29, v33, s34
	s_nop 0
	v_fma_f32 v32, v28, v32, s36
	v_fma_f32 v33, v29, v33, s36
	s_nop 0
	v_mul_f32 v28, v28, v32
	v_mul_f32 v29, v29, v33
	s_nop 0
	v_mul_f32 v28, v30, v28
	v_mul_f32 v29, v31, v29
	v_sub_f32_e32 v31, v23, v27
	v_mul_f32 v28, v24, v28
	v_mul_f32 v29, v25, v29
	v_sub_f32_e32 v30, v22, v26
	v_sub_f32_e32 v33, v25, v29
	v_sub_f32_e32 v32, v24, v28
	v_cndmask_b32_e32 v45, v33, v29, vcc
	v_cmp_gt_f32_e32 vcc, 0, v24
	v_mul_f32_e32 v25, v19, v19
	v_mul_f32_e32 v25, 0xbf38aa3b, v25
	v_cndmask_b32_e32 v44, v32, v28, vcc
	v_cmp_gt_f32_e32 vcc, 0, v23
	v_mul_f32_e32 v23, v18, v18
	v_mul_f32_e32 v23, 0xbf38aa3b, v23
	v_cndmask_b32_e32 v43, v31, v27, vcc
	v_cmp_gt_f32_e32 vcc, 0, v22
	v_fma_f32 v22, |v18|, s85, 1.0
	v_exp_f32_e32 v24, v23
	v_fma_f32 v23, |v19|, s85, 1.0
	v_rcp_f32_e32 v22, v22
	v_rcp_f32_e32 v23, v23
	v_cndmask_b32_e32 v42, v30, v26, vcc
	v_exp_f32_e32 v25, v25
	v_cmp_gt_f32_e32 vcc, 0, v21
	v_fma_f32 v26, v22, s26, v46
	v_fma_f32 v27, v23, s26, v46
	s_nop 0
	v_fma_f32 v26, v22, v26, s30
	v_fma_f32 v27, v23, v27, s30
	s_nop 0
	v_fma_f32 v26, v22, v26, s34
	v_fma_f32 v27, v23, v27, s34
	s_nop 0
	v_fma_f32 v26, v22, v26, s36
	v_fma_f32 v27, v23, v27, s36
	s_nop 0
	v_mul_f32 v22, v22, v26
	v_mul_f32 v23, v23, v27
	v_mul_f32_e32 v27, v21, v21
	v_mul_f32 v22, v24, v22
	v_mul_f32 v23, v25, v23
	v_mul_f32_e32 v25, v20, v20
	v_mul_f32_e32 v25, 0xbf38aa3b, v25
	v_fma_f32 v24, |v20|, s85, 1.0
	v_exp_f32_e32 v26, v25
	v_fma_f32 v25, |v21|, s85, 1.0
	v_rcp_f32_e32 v24, v24
	v_rcp_f32_e32 v25, v25
	v_mul_f32_e32 v27, 0xbf38aa3b, v27
	v_exp_f32_e32 v27, v27
	v_mul_f32 v22, v18, v22
	v_mul_f32 v23, v19, v23
	v_fma_f32 v28, v24, s26, v46
	v_fma_f32 v29, v25, s26, v46
	s_nop 0
	v_fma_f32 v28, v24, v28, s30
	v_fma_f32 v29, v25, v29, s30
	s_nop 0
	v_fma_f32 v28, v24, v28, s34
	v_fma_f32 v29, v25, v29, s34
	s_nop 0
	v_fma_f32 v28, v24, v28, s36
	v_fma_f32 v29, v25, v29, s36
	s_nop 0
	v_mul_f32 v24, v24, v28
	v_mul_f32 v25, v25, v29
	s_nop 0
	v_mul_f32 v24, v26, v24
	v_mul_f32 v25, v27, v25
	v_sub_f32_e32 v27, v19, v23
	v_mul_f32 v24, v20, v24
	v_mul_f32 v25, v21, v25
	v_sub_f32_e32 v26, v18, v22
	v_sub_f32_e32 v29, v21, v25
	v_sub_f32_e32 v28, v20, v24
	v_cndmask_b32_e32 v49, v29, v25, vcc
	v_cmp_gt_f32_e32 vcc, 0, v20
	s_nop 1
	v_cndmask_b32_e32 v48, v28, v24, vcc
	v_cmp_gt_f32_e32 vcc, 0, v19
	s_nop 1
	v_cndmask_b32_e32 v47, v27, v23, vcc
	v_cmp_gt_f32_e32 vcc, 0, v18
	s_nop 1
	v_cndmask_b32_e32 v46, v26, v22, vcc
.LBB0_189:
	v_add_u32_e32 v18, 0xa0, v168
	v_mad_i64_i32 v[22:23], s[38:39], v18, s86, v[162:163]
	v_cvt_pk_bf16_f32 v18, v34, v35
	v_cvt_pk_bf16_f32 v19, v36, v37
	v_cvt_pk_bf16_f32 v20, v38, v39
	v_cvt_pk_bf16_f32 v21, v40, v41
	global_store_dwordx4 v[22:23], v[18:21], off
	s_nop 1
	v_cvt_pk_bf16_f32 v18, v42, v43
	v_cvt_pk_bf16_f32 v19, v44, v45
	v_cvt_pk_bf16_f32 v20, v46, v47
	v_cvt_pk_bf16_f32 v21, v48, v49
	s_and_b64 vcc, exec, s[4:5]
	s_mov_b64 s[4:5], -1
	global_store_dwordx4 v[22:23], v[18:21], off offset:256
	s_cbranch_vccnz .LBB0_193
	s_nop 0
	v_mov_b64_e32 v[20:21], v[16:17]
	v_mov_b64_e32 v[32:33], v[4:5]
	v_mov_b64_e32 v[28:29], v[8:9]
	v_mov_b64_e32 v[24:25], v[12:13]
	s_and_b64 vcc, exec, s[2:3]
	v_mov_b64_e32 v[18:19], v[14:15]
	v_mov_b64_e32 v[30:31], v[2:3]
	v_mov_b64_e32 v[26:27], v[6:7]
	v_mov_b64_e32 v[22:23], v[10:11]
	s_cbranch_vccnz .LBB0_192
	v_mul_f32 v20, v16, s24
	v_mul_f32 v21, v17, s24
	v_mul_f32 v18, v14, s24
	v_mul_f32 v19, v15, s24
	v_mul_f32 v24, v12, s24
	v_mul_f32 v25, v13, s24
	v_mul_f32 v22, v10, s24
	v_mul_f32 v23, v11, s24
	v_mul_f32 v28, v8, s24
	v_mul_f32 v29, v9, s24
	v_mul_f32 v26, v6, s24
	v_mul_f32 v27, v7, s24
	v_mul_f32 v32, v4, s24
	v_mul_f32 v33, v5, s24
	v_mul_f32 v30, v2, s24
	v_mul_f32 v31, v3, s24

.LBB0_193:
	s_andn2_b64 vcc, exec, s[4:5]
	s_cbranch_vccnz .LBB0_195
	v_mul_f32_e32 v19, v14, v14
	v_mul_f32_e32 v19, 0xbf38aa3b, v19
	v_fma_f32 v18, |v14|, s85, 1.0
	v_exp_f32_e32 v20, v19
	v_fma_f32 v19, |v15|, s85, 1.0
	v_rcp_f32_e32 v18, v18
	v_rcp_f32_e32 v19, v19
	v_mul_f32_e32 v21, v15, v15
	v_mov_b64_e32 v[30:31], s[28:29]
	v_mul_f32_e32 v21, 0xbf38aa3b, v21
	v_fma_f32 v22, v18, s26, v30
	v_fma_f32 v23, v19, s26, v30
	v_exp_f32_e32 v21, v21
	v_fma_f32 v22, v18, v22, s30
	v_fma_f32 v23, v19, v23, s30
	v_cmp_gt_f32_e32 vcc, 0, v17
	v_fma_f32 v22, v18, v22, s34
	v_fma_f32 v23, v19, v23, s34
	s_nop 0
	v_fma_f32 v22, v18, v22, s36
	v_fma_f32 v23, v19, v23, s36
	s_nop 0
	v_mul_f32 v18, v18, v22
	v_mul_f32 v19, v19, v23
	v_mul_f32_e32 v23, v17, v17
	v_mul_f32 v18, v20, v18
	v_mul_f32 v19, v21, v19
	v_mul_f32_e32 v21, v16, v16
	v_mul_f32_e32 v21, 0xbf38aa3b, v21
	v_fma_f32 v20, |v16|, s85, 1.0
	v_exp_f32_e32 v22, v21
	v_fma_f32 v21, |v17|, s85, 1.0
	v_rcp_f32_e32 v20, v20
	v_rcp_f32_e32 v21, v21
	v_mul_f32_e32 v23, 0xbf38aa3b, v23
	v_exp_f32_e32 v23, v23
	v_mul_f32 v18, v14, v18
	v_mul_f32 v19, v15, v19
	v_fma_f32 v24, v20, s26, v30
	v_fma_f32 v25, v21, s26, v30
	s_nop 0
	v_fma_f32 v24, v20, v24, s30
	v_fma_f32 v25, v21, v25, s30
	s_nop 0
	v_fma_f32 v24, v20, v24, s34
	v_fma_f32 v25, v21, v25, s34
	s_nop 0
	v_fma_f32 v24, v20, v24, s36
	v_fma_f32 v25, v21, v25, s36
	s_nop 0
	v_mul_f32 v20, v20, v24
	v_mul_f32 v21, v21, v25
	s_nop 0
	v_mul_f32 v20, v22, v20
	v_mul_f32 v21, v23, v21
	v_sub_f32_e32 v23, v15, v19
	v_mul_f32 v20, v16, v20
	v_mul_f32 v21, v17, v21
	v_sub_f32_e32 v22, v14, v18
	v_sub_f32_e32 v25, v17, v21
	v_sub_f32_e32 v24, v16, v20
	v_cndmask_b32_e32 v21, v25, v21, vcc
	v_cmp_gt_f32_e32 vcc, 0, v16
	v_mul_f32_e32 v17, v11, v11
	v_mul_f32_e32 v17, 0xbf38aa3b, v17
	v_cndmask_b32_e32 v20, v24, v20, vcc
	v_cmp_gt_f32_e32 vcc, 0, v15
	v_mul_f32_e32 v15, v10, v10
	v_mul_f32_e32 v15, 0xbf38aa3b, v15
	v_cndmask_b32_e32 v19, v23, v19, vcc
	v_cmp_gt_f32_e32 vcc, 0, v14
	v_fma_f32 v14, |v10|, s85, 1.0
	v_exp_f32_e32 v16, v15
	v_fma_f32 v15, |v11|, s85, 1.0
	v_rcp_f32_e32 v14, v14
	v_rcp_f32_e32 v15, v15
	v_cndmask_b32_e32 v18, v22, v18, vcc
	v_exp_f32_e32 v17, v17
	v_cmp_gt_f32_e32 vcc, 0, v13
	v_fma_f32 v22, v14, s26, v30
	v_fma_f32 v23, v15, s26, v30
	s_nop 0
	v_fma_f32 v22, v14, v22, s30
	v_fma_f32 v23, v15, v23, s30
	s_nop 0
	v_fma_f32 v22, v14, v22, s34
	v_fma_f32 v23, v15, v23, s34
	s_nop 0
	v_fma_f32 v22, v14, v22, s36
	v_fma_f32 v23, v15, v23, s36
	s_nop 0
	v_mul_f32 v14, v14, v22
	v_mul_f32 v15, v15, v23
	v_mul_f32_e32 v23, v13, v13
	v_mul_f32 v14, v16, v14
	v_mul_f32 v15, v17, v15
	v_mul_f32_e32 v17, v12, v12
	v_mul_f32_e32 v17, 0xbf38aa3b, v17
	v_fma_f32 v16, |v12|, s85, 1.0
	v_exp_f32_e32 v22, v17
	v_fma_f32 v17, |v13|, s85, 1.0
	v_rcp_f32_e32 v16, v16
	v_rcp_f32_e32 v17, v17
	v_mul_f32_e32 v23, 0xbf38aa3b, v23
	v_exp_f32_e32 v23, v23
	v_mul_f32 v14, v10, v14
	v_mul_f32 v15, v11, v15
	v_fma_f32 v24, v16, s26, v30
	v_fma_f32 v25, v17, s26, v30
	s_nop 0
	v_fma_f32 v24, v16, v24, s30
	v_fma_f32 v25, v17, v25, s30
	s_nop 0
	v_fma_f32 v24, v16, v24, s34
	v_fma_f32 v25, v17, v25, s34
	s_nop 0
	v_fma_f32 v24, v16, v24, s36
	v_fma_f32 v25, v17, v25, s36
	s_nop 0
	v_mul_f32 v16, v16, v24
	v_mul_f32 v17, v17, v25
	s_nop 0
	v_mul_f32 v16, v22, v16
	v_mul_f32 v17, v23, v17
	v_sub_f32_e32 v23, v11, v15
	v_mul_f32 v16, v12, v16
	v_mul_f32 v17, v13, v17
	v_sub_f32_e32 v22, v10, v14
	v_sub_f32_e32 v25, v13, v17
	v_sub_f32_e32 v24, v12, v16
	v_cndmask_b32_e32 v25, v25, v17, vcc
	v_cmp_gt_f32_e32 vcc, 0, v12
	v_mul_f32_e32 v13, v7, v7
	v_mul_f32_e32 v13, 0xbf38aa3b, v13
	v_cndmask_b32_e32 v24, v24, v16, vcc
	v_cmp_gt_f32_e32 vcc, 0, v11
	v_mul_f32_e32 v11, v6, v6
	v_mul_f32_e32 v11, 0xbf38aa3b, v11
	v_cndmask_b32_e32 v23, v23, v15, vcc
	v_cmp_gt_f32_e32 vcc, 0, v10
	v_fma_f32 v10, |v6|, s85, 1.0
	v_exp_f32_e32 v12, v11
	v_fma_f32 v11, |v7|, s85, 1.0
	v_rcp_f32_e32 v10, v10
	v_rcp_f32_e32 v11, v11
	v_cndmask_b32_e32 v22, v22, v14, vcc
	v_exp_f32_e32 v13, v13
	v_cmp_gt_f32_e32 vcc, 0, v9
	v_fma_f32 v14, v10, s26, v30
	v_fma_f32 v15, v11, s26, v30
	s_nop 0
	v_fma_f32 v14, v10, v14, s30
	v_fma_f32 v15, v11, v15, s30
	s_nop 0
	v_fma_f32 v14, v10, v14, s34
	v_fma_f32 v15, v11, v15, s34
	s_nop 0
	v_fma_f32 v14, v10, v14, s36
	v_fma_f32 v15, v11, v15, s36
	s_nop 0
	v_mul_f32 v10, v10, v14
	v_mul_f32 v11, v11, v15
	v_mul_f32_e32 v15, v9, v9
	v_mul_f32 v10, v12, v10
	v_mul_f32 v11, v13, v11
	v_mul_f32_e32 v13, v8, v8
	v_mul_f32_e32 v13, 0xbf38aa3b, v13
	v_fma_f32 v12, |v8|, s85, 1.0
	v_exp_f32_e32 v14, v13
	v_fma_f32 v13, |v9|, s85, 1.0
	v_rcp_f32_e32 v12, v12
	v_rcp_f32_e32 v13, v13
	v_mul_f32_e32 v15, 0xbf38aa3b, v15
	v_exp_f32_e32 v15, v15
	v_mul_f32 v10, v6, v10
	v_mul_f32 v11, v7, v11
	v_fma_f32 v16, v12, s26, v30
	v_fma_f32 v17, v13, s26, v30
	s_nop 0
	v_fma_f32 v16, v12, v16, s30
	v_fma_f32 v17, v13, v17, s30
	s_nop 0
	v_fma_f32 v16, v12, v16, s34
	v_fma_f32 v17, v13, v17, s34
	s_nop 0
	v_fma_f32 v16, v12, v16, s36
	v_fma_f32 v17, v13, v17, s36
	s_nop 0
	v_mul_f32 v12, v12, v16
	v_mul_f32 v13, v13, v17
	s_nop 0
	v_mul_f32 v12, v14, v12
	v_mul_f32 v13, v15, v13
	v_sub_f32_e32 v15, v7, v11
	v_mul_f32 v12, v8, v12
	v_mul_f32 v13, v9, v13
	v_sub_f32_e32 v14, v6, v10
	v_sub_f32_e32 v17, v9, v13
	v_sub_f32_e32 v16, v8, v12
	v_cndmask_b32_e32 v29, v17, v13, vcc
	v_cmp_gt_f32_e32 vcc, 0, v8
	v_mul_f32_e32 v9, v3, v3
	v_mul_f32_e32 v9, 0xbf38aa3b, v9
	v_cndmask_b32_e32 v28, v16, v12, vcc
	v_cmp_gt_f32_e32 vcc, 0, v7
	v_mul_f32_e32 v7, v2, v2
	v_mul_f32_e32 v7, 0xbf38aa3b, v7
	v_cndmask_b32_e32 v27, v15, v11, vcc
	v_cmp_gt_f32_e32 vcc, 0, v6
	v_fma_f32 v6, |v2|, s85, 1.0
	v_exp_f32_e32 v8, v7
	v_fma_f32 v7, |v3|, s85, 1.0
	v_rcp_f32_e32 v6, v6
	v_rcp_f32_e32 v7, v7
	v_cndmask_b32_e32 v26, v14, v10, vcc
	v_exp_f32_e32 v9, v9
	v_cmp_gt_f32_e32 vcc, 0, v5
	v_fma_f32 v10, v6, s26, v30
	v_fma_f32 v11, v7, s26, v30
	s_nop 0
	v_fma_f32 v10, v6, v10, s30
	v_fma_f32 v11, v7, v11, s30
	s_nop 0
	v_fma_f32 v10, v6, v10, s34
	v_fma_f32 v11, v7, v11, s34
	s_nop 0
	v_fma_f32 v10, v6, v10, s36
	v_fma_f32 v11, v7, v11, s36
	s_nop 0
	v_mul_f32 v6, v6, v10
	v_mul_f32 v7, v7, v11
	v_mul_f32_e32 v11, v5, v5
	v_mul_f32 v6, v8, v6
	v_mul_f32 v7, v9, v7
	v_mul_f32_e32 v9, v4, v4
	v_mul_f32_e32 v9, 0xbf38aa3b, v9
	v_fma_f32 v8, |v4|, s85, 1.0
	v_exp_f32_e32 v10, v9
	v_fma_f32 v9, |v5|, s85, 1.0
	v_rcp_f32_e32 v8, v8
	v_rcp_f32_e32 v9, v9
	v_mul_f32_e32 v11, 0xbf38aa3b, v11
	v_exp_f32_e32 v11, v11
	v_mul_f32 v6, v2, v6
	v_mul_f32 v7, v3, v7
	v_fma_f32 v12, v8, s26, v30
	v_fma_f32 v13, v9, s26, v30
	s_nop 0
	v_fma_f32 v12, v8, v12, s30
	v_fma_f32 v13, v9, v13, s30
	s_nop 0
	v_fma_f32 v12, v8, v12, s34
	v_fma_f32 v13, v9, v13, s34
	s_nop 0
	v_fma_f32 v12, v8, v12, s36
	v_fma_f32 v13, v9, v13, s36
	s_nop 0
	v_mul_f32 v8, v8, v12
	v_mul_f32 v9, v9, v13
	s_nop 0
	v_mul_f32 v8, v10, v8
	v_mul_f32 v9, v11, v9
	v_sub_f32_e32 v11, v3, v7
	v_mul_f32 v8, v4, v8
	v_mul_f32 v9, v5, v9
	v_sub_f32_e32 v10, v2, v6
	v_sub_f32_e32 v13, v5, v9
	v_sub_f32_e32 v12, v4, v8
	v_cndmask_b32_e32 v33, v13, v9, vcc
	v_cmp_gt_f32_e32 vcc, 0, v4
	s_nop 1
	v_cndmask_b32_e32 v32, v12, v8, vcc
	v_cmp_gt_f32_e32 vcc, 0, v3
	s_nop 1
	v_cndmask_b32_e32 v31, v11, v7, vcc
	v_cmp_gt_f32_e32 vcc, 0, v2
	s_nop 1
	v_cndmask_b32_e32 v30, v10, v6, vcc

.LBB0_657:
	v_mul_f32_e32 v144, 0xbfb8aa3b, v126
	v_exp_f32_e32 v144, v144
	v_mul_f32_e32 v145, 0xbfb8aa3b, v127
	v_exp_f32_e32 v145, v145
	v_mul_f32_e32 v153, 0xbfb8aa3b, v129
	v_add_f32_e32 v144, 1.0, v144
	v_rcp_f32_e32 v152, v144
	v_add_f32_e32 v144, 1.0, v145
	v_mul_f32_e32 v145, 0xbfb8aa3b, v128
	v_exp_f32_e32 v145, v145
	v_exp_f32_e32 v155, v153
	v_rcp_f32_e32 v153, v144
	s_lshl_b32 s26, s53, 7
	v_add_f32_e32 v144, 1.0, v145
	v_rcp_f32_e32 v154, v144
	v_add_f32_e32 v144, 1.0, v155
	v_rcp_f32_e32 v155, v144
	v_mul_f32_e32 v144, 0xbfb8aa3b, v122
	v_mul_f32 v126, v126, v152
	v_mul_f32 v127, v127, v153
	v_mul_f32_e32 v153, 0xbfb8aa3b, v123
	v_exp_f32_e32 v156, v144
	v_exp_f32_e32 v153, v153
	v_mul_f32 v128, v128, v154
	v_mul_f32 v129, v129, v155
	v_mul_f32_e32 v154, 0xbfb8aa3b, v124
	v_mul_f32_e32 v155, 0xbfb8aa3b, v125
	v_add_f32_e32 v152, 1.0, v156
	v_exp_f32_e32 v154, v154
	v_exp_f32_e32 v155, v155
	v_add_f32_e32 v153, 1.0, v153
	v_rcp_f32_e32 v152, v152
	v_rcp_f32_e32 v153, v153
	v_add_f32_e32 v154, 1.0, v154
	v_add_f32_e32 v155, 1.0, v155
	v_rcp_f32_e32 v154, v154
	v_rcp_f32_e32 v155, v155
	v_mul_f32 v118, v126, v118
	v_mul_f32 v119, v127, v119
	v_mul_f32 v122, v122, v152
	v_mul_f32 v123, v123, v153
	v_mul_f32 v118, v118, s8
	v_mul_f32 v119, v119, s8
	v_mul_f32 v114, v122, v114
	v_mul_f32 v115, v123, v115
	v_med3_f32 v122, v118, s9, v150
	v_mul_f32 v114, v114, s8
	v_mul_f32 v115, v115, s8
	v_med3_f32 v119, v119, s9, v150
	v_mov_b32_e32 v118, 0
	v_cvt_pk_fp8_f32 v118, v122, v119
	v_med3_f32 v114, v114, s9, v150
	v_med3_f32 v115, v115, s9, v150
	v_mov_b32_e32 v119, 0
	v_mul_f32 v124, v124, v154
	v_mul_f32 v125, v125, v155
	v_cvt_pk_fp8_f32 v119, v114, v115
	v_mul_f32 v120, v128, v120
	v_mul_f32 v121, v129, v121
	v_mul_f32 v116, v124, v116
	v_mul_f32 v117, v125, v117
	v_mul_f32 v120, v120, s8
	v_mul_f32 v121, v121, s8
	v_mul_f32 v116, v116, s8
	v_mul_f32 v117, v117, s8
	v_med3_f32 v120, v120, s9, v150
	v_med3_f32 v121, v121, s9, v150
	v_med3_f32 v114, v116, s9, v150
	v_med3_f32 v115, v117, s9, v150
	v_mul_f32_e32 v116, 0xbfb8aa3b, v110
	v_mul_f32_e32 v117, 0xbfb8aa3b, v111
	v_cvt_pk_fp8_f32 v118, v120, v121 op_sel:[0,0,1]
	v_cvt_pk_fp8_f32 v119, v114, v115 op_sel:[0,0,1]
	v_exp_f32_e32 v116, v116
	v_exp_f32_e32 v117, v117
	s_ashr_i32 s27, s26, 31
	v_lshl_add_u32 v151, s55, 8, v146
	v_lshl_add_u64 v[144:145], v[138:139], 0, s[26:27]
	v_mad_i64_i32 v[114:115], s[26:27], v151, s51, v[144:145]
	global_store_dwordx2 v[114:115], v[118:119], off
	v_add_f32_e32 v114, 1.0, v116
	v_add_f32_e32 v115, 1.0, v117
	v_mul_f32_e32 v116, 0xbfb8aa3b, v112
	v_mul_f32_e32 v117, 0xbfb8aa3b, v113
	v_exp_f32_e32 v116, v116
	v_exp_f32_e32 v117, v117
	v_rcp_f32_e32 v114, v114
	v_rcp_f32_e32 v115, v115
	v_add_f32_e32 v116, 1.0, v116
	v_add_f32_e32 v117, 1.0, v117
	v_rcp_f32_e32 v116, v116
	v_rcp_f32_e32 v117, v117
	v_mul_f32_e32 v118, 0xbfb8aa3b, v106
	v_mul_f32 v110, v110, v114
	v_mul_f32 v111, v111, v115
	v_mul_f32_e32 v115, 0xbfb8aa3b, v107
	v_exp_f32_e32 v118, v118
	v_exp_f32_e32 v115, v115
	v_mul_f32 v112, v112, v116
	v_mul_f32 v113, v113, v117
	v_mul_f32_e32 v116, 0xbfb8aa3b, v108
	v_mul_f32_e32 v117, 0xbfb8aa3b, v109
	v_add_f32_e32 v114, 1.0, v118
	v_exp_f32_e32 v116, v116
	v_exp_f32_e32 v117, v117
	v_add_f32_e32 v115, 1.0, v115
	v_rcp_f32_e32 v114, v114
	v_rcp_f32_e32 v115, v115
	v_add_f32_e32 v116, 1.0, v116
	v_add_f32_e32 v117, 1.0, v117
	v_rcp_f32_e32 v116, v116
	v_rcp_f32_e32 v117, v117
	v_mul_f32 v102, v110, v102
	v_mul_f32 v103, v111, v103
	v_mul_f32 v106, v106, v114
	v_mul_f32 v107, v107, v115
	v_mul_f32 v102, v102, s8
	v_mul_f32 v103, v103, s8
	v_mul_f32 v98, v106, v98
	v_mul_f32 v99, v107, v99
	v_med3_f32 v106, v102, s9, v150
	v_mul_f32 v98, v98, s8
	v_mul_f32 v99, v99, s8
	v_med3_f32 v103, v103, s9, v150
	v_mov_b32_e32 v102, 0
	v_cvt_pk_fp8_f32 v102, v106, v103
	v_med3_f32 v98, v98, s9, v150
	v_med3_f32 v99, v99, s9, v150
	v_mov_b32_e32 v103, 0
	v_mul_f32 v108, v108, v116
	v_mul_f32 v109, v109, v117
	v_cvt_pk_fp8_f32 v103, v98, v99
	v_mul_f32 v104, v112, v104
	v_mul_f32 v105, v113, v105
	v_mul_f32 v100, v108, v100
	v_mul_f32 v101, v109, v101
	v_mul_f32 v104, v104, s8
	v_mul_f32 v105, v105, s8
	v_mul_f32 v100, v100, s8
	v_mul_f32 v101, v101, s8
	v_med3_f32 v104, v104, s9, v150
	v_med3_f32 v105, v105, s9, v150
	v_med3_f32 v98, v100, s9, v150
	v_med3_f32 v99, v101, s9, v150
	v_mul_f32_e32 v100, 0xbfb8aa3b, v94
	v_mul_f32_e32 v101, 0xbfb8aa3b, v95
	v_cvt_pk_fp8_f32 v102, v104, v105 op_sel:[0,0,1]
	v_cvt_pk_fp8_f32 v103, v98, v99 op_sel:[0,0,1]
	v_exp_f32_e32 v100, v100
	v_exp_f32_e32 v101, v101
	v_or_b32_e32 v119, 16, v151
	v_mad_i64_i32 v[98:99], s[26:27], v119, s51, v[144:145]
	global_store_dwordx2 v[98:99], v[102:103], off
	v_add_f32_e32 v98, 1.0, v100
	v_add_f32_e32 v99, 1.0, v101
	v_mul_f32_e32 v100, 0xbfb8aa3b, v96
	v_mul_f32_e32 v101, 0xbfb8aa3b, v97
	v_exp_f32_e32 v100, v100
	v_exp_f32_e32 v101, v101
	v_rcp_f32_e32 v98, v98
	v_rcp_f32_e32 v99, v99
	v_add_f32_e32 v100, 1.0, v100
	v_add_f32_e32 v101, 1.0, v101
	v_rcp_f32_e32 v100, v100
	v_rcp_f32_e32 v101, v101
	v_mul_f32_e32 v102, 0xbfb8aa3b, v90
	v_mul_f32 v94, v94, v98
	v_mul_f32 v95, v95, v99
	v_mul_f32_e32 v99, 0xbfb8aa3b, v91
	v_exp_f32_e32 v102, v102
	v_exp_f32_e32 v99, v99
	v_mul_f32 v96, v96, v100
	v_mul_f32 v97, v97, v101
	v_mul_f32_e32 v100, 0xbfb8aa3b, v92
	v_mul_f32_e32 v101, 0xbfb8aa3b, v93
	v_add_f32_e32 v98, 1.0, v102
	v_exp_f32_e32 v100, v100
	v_exp_f32_e32 v101, v101
	v_add_f32_e32 v99, 1.0, v99
	v_rcp_f32_e32 v98, v98
	v_rcp_f32_e32 v99, v99
	v_add_f32_e32 v100, 1.0, v100
	v_add_f32_e32 v101, 1.0, v101
	v_rcp_f32_e32 v100, v100
	v_rcp_f32_e32 v101, v101
	v_mul_f32 v86, v94, v86
	v_mul_f32 v87, v95, v87
	v_mul_f32 v90, v90, v98
	v_mul_f32 v91, v91, v99
	v_mul_f32 v86, v86, s8
	v_mul_f32 v87, v87, s8
	v_mul_f32 v82, v90, v82
	v_mul_f32 v83, v91, v83
	v_med3_f32 v90, v86, s9, v150
	v_mul_f32 v82, v82, s8
	v_mul_f32 v83, v83, s8
	v_med3_f32 v87, v87, s9, v150
	v_mov_b32_e32 v86, 0
	v_cvt_pk_fp8_f32 v86, v90, v87
	v_med3_f32 v82, v82, s9, v150
	v_med3_f32 v83, v83, s9, v150
	v_mov_b32_e32 v87, 0
	v_mul_f32 v92, v92, v100
	v_mul_f32 v93, v93, v101
	v_cvt_pk_fp8_f32 v87, v82, v83
	v_mul_f32 v88, v96, v88
	v_mul_f32 v89, v97, v89
	v_mul_f32 v84, v92, v84
	v_mul_f32 v85, v93, v85
	v_mul_f32 v88, v88, s8
	v_mul_f32 v89, v89, s8
	v_mul_f32 v84, v84, s8
	v_mul_f32 v85, v85, s8
	v_med3_f32 v88, v88, s9, v150
	v_med3_f32 v89, v89, s9, v150
	v_med3_f32 v82, v84, s9, v150
	v_med3_f32 v83, v85, s9, v150
	v_mul_f32_e32 v84, 0xbfb8aa3b, v78
	v_mul_f32_e32 v85, 0xbfb8aa3b, v79
	v_cvt_pk_fp8_f32 v86, v88, v89 op_sel:[0,0,1]
	v_cvt_pk_fp8_f32 v87, v82, v83 op_sel:[0,0,1]
	v_exp_f32_e32 v84, v84
	v_exp_f32_e32 v85, v85
	v_or_b32_e32 v103, 32, v151
	v_mad_i64_i32 v[82:83], s[26:27], v103, s51, v[144:145]
	global_store_dwordx2 v[82:83], v[86:87], off
	v_add_f32_e32 v82, 1.0, v84
	v_add_f32_e32 v83, 1.0, v85
	v_mul_f32_e32 v84, 0xbfb8aa3b, v80
	v_mul_f32_e32 v85, 0xbfb8aa3b, v81
	v_exp_f32_e32 v84, v84
	v_exp_f32_e32 v85, v85
	v_rcp_f32_e32 v82, v82
	v_rcp_f32_e32 v83, v83
	v_add_f32_e32 v84, 1.0, v84
	v_add_f32_e32 v85, 1.0, v85
	v_rcp_f32_e32 v84, v84
	v_rcp_f32_e32 v85, v85
	v_mul_f32_e32 v86, 0xbfb8aa3b, v74
	v_mul_f32 v78, v78, v82
	v_mul_f32 v79, v79, v83
	v_mul_f32_e32 v83, 0xbfb8aa3b, v75
	v_exp_f32_e32 v86, v86
	v_exp_f32_e32 v83, v83
	v_mul_f32 v80, v80, v84
	v_mul_f32 v81, v81, v85
	v_mul_f32_e32 v84, 0xbfb8aa3b, v76
	v_mul_f32_e32 v85, 0xbfb8aa3b, v77
	v_add_f32_e32 v82, 1.0, v86
	v_exp_f32_e32 v84, v84
	v_exp_f32_e32 v85, v85
	v_add_f32_e32 v83, 1.0, v83
	v_rcp_f32_e32 v82, v82
	v_rcp_f32_e32 v83, v83
	v_add_f32_e32 v84, 1.0, v84
	v_add_f32_e32 v85, 1.0, v85
	v_rcp_f32_e32 v84, v84
	v_rcp_f32_e32 v85, v85
	v_mul_f32 v70, v78, v70
	v_mul_f32 v71, v79, v71
	v_mul_f32 v74, v74, v82
	v_mul_f32 v75, v75, v83
	v_mul_f32 v70, v70, s8
	v_mul_f32 v71, v71, s8
	v_mul_f32 v66, v74, v66
	v_mul_f32 v67, v75, v67
	v_med3_f32 v74, v70, s9, v150
	v_mul_f32 v66, v66, s8
	v_mul_f32 v67, v67, s8
	v_med3_f32 v71, v71, s9, v150
	v_mov_b32_e32 v70, 0
	v_cvt_pk_fp8_f32 v70, v74, v71
	v_med3_f32 v66, v66, s9, v150
	v_med3_f32 v67, v67, s9, v150
	v_mov_b32_e32 v71, 0
	v_mul_f32 v76, v76, v84
	v_mul_f32 v77, v77, v85
	v_cvt_pk_fp8_f32 v71, v66, v67
	v_mul_f32 v72, v80, v72
	v_mul_f32 v73, v81, v73
	v_mul_f32 v68, v76, v68
	v_mul_f32 v69, v77, v69
	v_mul_f32 v72, v72, s8
	v_mul_f32 v73, v73, s8
	v_mul_f32 v68, v68, s8
	v_mul_f32 v69, v69, s8
	v_med3_f32 v72, v72, s9, v150
	v_med3_f32 v73, v73, s9, v150
	v_med3_f32 v66, v68, s9, v150
	v_med3_f32 v67, v69, s9, v150
	v_mul_f32_e32 v68, 0xbfb8aa3b, v62
	v_mul_f32_e32 v69, 0xbfb8aa3b, v63
	v_cvt_pk_fp8_f32 v70, v72, v73 op_sel:[0,0,1]
	v_cvt_pk_fp8_f32 v71, v66, v67 op_sel:[0,0,1]
	v_exp_f32_e32 v68, v68
	v_exp_f32_e32 v69, v69
	v_or_b32_e32 v87, 48, v151
	v_mad_i64_i32 v[66:67], s[26:27], v87, s51, v[144:145]
	global_store_dwordx2 v[66:67], v[70:71], off
	v_add_f32_e32 v66, 1.0, v68
	v_add_f32_e32 v67, 1.0, v69
	v_mul_f32_e32 v68, 0xbfb8aa3b, v64
	v_mul_f32_e32 v69, 0xbfb8aa3b, v65
	v_exp_f32_e32 v68, v68
	v_exp_f32_e32 v69, v69
	v_rcp_f32_e32 v66, v66
	v_rcp_f32_e32 v67, v67
	v_add_f32_e32 v68, 1.0, v68
	v_add_f32_e32 v69, 1.0, v69
	v_rcp_f32_e32 v68, v68
	v_rcp_f32_e32 v69, v69
	v_mul_f32_e32 v70, 0xbfb8aa3b, v58
	v_mul_f32 v62, v62, v66
	v_mul_f32 v63, v63, v67
	v_mul_f32_e32 v67, 0xbfb8aa3b, v59
	v_exp_f32_e32 v70, v70
	v_exp_f32_e32 v67, v67
	v_mul_f32 v64, v64, v68
	v_mul_f32 v65, v65, v69
	v_mul_f32_e32 v68, 0xbfb8aa3b, v60
	v_mul_f32_e32 v69, 0xbfb8aa3b, v61
	v_add_f32_e32 v66, 1.0, v70
	v_exp_f32_e32 v68, v68
	v_exp_f32_e32 v69, v69
	v_add_f32_e32 v67, 1.0, v67
	v_rcp_f32_e32 v66, v66
	v_rcp_f32_e32 v67, v67
	v_add_f32_e32 v68, 1.0, v68
	v_add_f32_e32 v69, 1.0, v69
	v_rcp_f32_e32 v68, v68
	v_rcp_f32_e32 v69, v69
	v_mul_f32 v54, v62, v54
	v_mul_f32 v55, v63, v55
	v_mul_f32 v58, v58, v66
	v_mul_f32 v59, v59, v67
	v_mul_f32 v54, v54, s8
	v_mul_f32 v55, v55, s8
	v_mul_f32 v50, v58, v50
	v_mul_f32 v51, v59, v51
	v_med3_f32 v58, v54, s9, v150
	v_mul_f32 v50, v50, s8
	v_mul_f32 v51, v51, s8
	v_med3_f32 v55, v55, s9, v150
	v_mov_b32_e32 v54, 0
	v_cvt_pk_fp8_f32 v54, v58, v55
	v_med3_f32 v50, v50, s9, v150
	v_med3_f32 v51, v51, s9, v150
	v_mov_b32_e32 v55, 0
	v_mul_f32 v60, v60, v68
	v_mul_f32 v61, v61, v69
	v_cvt_pk_fp8_f32 v55, v50, v51
	v_mul_f32 v56, v64, v56
	v_mul_f32 v57, v65, v57
	v_mul_f32 v52, v60, v52
	v_mul_f32 v53, v61, v53
	v_mul_f32 v56, v56, s8
	v_mul_f32 v57, v57, s8
	v_mul_f32 v52, v52, s8
	v_mul_f32 v53, v53, s8
	v_med3_f32 v56, v56, s9, v150
	v_med3_f32 v57, v57, s9, v150
	v_med3_f32 v50, v52, s9, v150
	v_med3_f32 v51, v53, s9, v150
	v_mul_f32_e32 v52, 0xbfb8aa3b, v46
	v_mul_f32_e32 v53, 0xbfb8aa3b, v47
	v_cvt_pk_fp8_f32 v54, v56, v57 op_sel:[0,0,1]
	v_cvt_pk_fp8_f32 v55, v50, v51 op_sel:[0,0,1]
	v_exp_f32_e32 v52, v52
	v_exp_f32_e32 v53, v53
	v_add_u32_e32 v71, 0x80, v151
	v_mad_i64_i32 v[50:51], s[26:27], v71, s51, v[144:145]
	global_store_dwordx2 v[50:51], v[54:55], off
	v_add_f32_e32 v50, 1.0, v52
	v_add_f32_e32 v51, 1.0, v53
	v_mul_f32_e32 v52, 0xbfb8aa3b, v48
	v_mul_f32_e32 v53, 0xbfb8aa3b, v49
	v_exp_f32_e32 v52, v52
	v_exp_f32_e32 v53, v53
	v_rcp_f32_e32 v50, v50
	v_rcp_f32_e32 v51, v51
	v_add_f32_e32 v52, 1.0, v52
	v_add_f32_e32 v53, 1.0, v53
	v_rcp_f32_e32 v52, v52
	v_rcp_f32_e32 v53, v53
	v_mul_f32_e32 v54, 0xbfb8aa3b, v42
	v_mul_f32 v46, v46, v50
	v_mul_f32 v47, v47, v51
	v_mul_f32_e32 v51, 0xbfb8aa3b, v43
	v_exp_f32_e32 v54, v54
	v_exp_f32_e32 v51, v51
	v_mul_f32 v48, v48, v52
	v_mul_f32 v49, v49, v53
	v_mul_f32_e32 v52, 0xbfb8aa3b, v44
	v_mul_f32_e32 v53, 0xbfb8aa3b, v45
	v_add_f32_e32 v50, 1.0, v54
	v_exp_f32_e32 v52, v52
	v_exp_f32_e32 v53, v53
	v_add_f32_e32 v51, 1.0, v51
	v_rcp_f32_e32 v50, v50
	v_rcp_f32_e32 v51, v51
	v_add_f32_e32 v52, 1.0, v52
	v_add_f32_e32 v53, 1.0, v53
	v_rcp_f32_e32 v52, v52
	v_rcp_f32_e32 v53, v53
	v_mul_f32 v38, v46, v38
	v_mul_f32 v39, v47, v39
	v_mul_f32 v42, v42, v50
	v_mul_f32 v43, v43, v51
	v_mul_f32 v38, v38, s8
	v_mul_f32 v39, v39, s8
	v_mul_f32 v34, v42, v34
	v_mul_f32 v35, v43, v35
	v_med3_f32 v42, v38, s9, v150
	v_mul_f32 v34, v34, s8
	v_mul_f32 v35, v35, s8
	v_med3_f32 v39, v39, s9, v150
	v_mov_b32_e32 v38, 0
	v_cvt_pk_fp8_f32 v38, v42, v39
	v_med3_f32 v34, v34, s9, v150
	v_med3_f32 v35, v35, s9, v150
	v_mov_b32_e32 v39, 0
	v_mul_f32 v44, v44, v52
	v_mul_f32 v45, v45, v53
	v_cvt_pk_fp8_f32 v39, v34, v35
	v_mul_f32 v40, v48, v40
	v_mul_f32 v41, v49, v41
	v_mul_f32 v36, v44, v36
	v_mul_f32 v37, v45, v37
	v_mul_f32 v40, v40, s8
	v_mul_f32 v41, v41, s8
	v_mul_f32 v36, v36, s8
	v_mul_f32 v37, v37, s8
	v_med3_f32 v40, v40, s9, v150
	v_med3_f32 v41, v41, s9, v150
	v_med3_f32 v34, v36, s9, v150
	v_med3_f32 v35, v37, s9, v150
	v_mul_f32_e32 v36, 0xbfb8aa3b, v30
	v_mul_f32_e32 v37, 0xbfb8aa3b, v31
	v_cvt_pk_fp8_f32 v38, v40, v41 op_sel:[0,0,1]
	v_cvt_pk_fp8_f32 v39, v34, v35 op_sel:[0,0,1]
	v_exp_f32_e32 v36, v36
	v_exp_f32_e32 v37, v37
	v_add_u32_e32 v55, 0x90, v151
	v_mad_i64_i32 v[34:35], s[26:27], v55, s51, v[144:145]
	global_store_dwordx2 v[34:35], v[38:39], off
	v_add_f32_e32 v34, 1.0, v36
	v_add_f32_e32 v35, 1.0, v37
	v_mul_f32_e32 v36, 0xbfb8aa3b, v32
	v_mul_f32_e32 v37, 0xbfb8aa3b, v33
	v_exp_f32_e32 v36, v36
	v_exp_f32_e32 v37, v37
	v_rcp_f32_e32 v34, v34
	v_rcp_f32_e32 v35, v35
	v_add_f32_e32 v36, 1.0, v36
	v_add_f32_e32 v37, 1.0, v37
	v_rcp_f32_e32 v36, v36
	v_rcp_f32_e32 v37, v37
	v_mul_f32_e32 v38, 0xbfb8aa3b, v26
	v_mul_f32 v30, v30, v34
	v_mul_f32 v31, v31, v35
	v_mul_f32_e32 v35, 0xbfb8aa3b, v27
	v_exp_f32_e32 v38, v38
	v_exp_f32_e32 v35, v35
	v_mul_f32 v32, v32, v36
	v_mul_f32 v33, v33, v37
	v_mul_f32_e32 v36, 0xbfb8aa3b, v28
	v_mul_f32_e32 v37, 0xbfb8aa3b, v29
	v_add_f32_e32 v34, 1.0, v38
	v_exp_f32_e32 v36, v36
	v_exp_f32_e32 v37, v37
	v_add_f32_e32 v35, 1.0, v35
	v_rcp_f32_e32 v34, v34
	v_rcp_f32_e32 v35, v35
	v_add_f32_e32 v36, 1.0, v36
	v_add_f32_e32 v37, 1.0, v37
	v_rcp_f32_e32 v36, v36
	v_rcp_f32_e32 v37, v37
	v_mul_f32 v22, v30, v22
	v_mul_f32 v23, v31, v23
	v_mul_f32 v26, v26, v34
	v_mul_f32 v27, v27, v35
	v_mul_f32 v22, v22, s8
	v_mul_f32 v23, v23, s8
	v_mul_f32 v18, v26, v18
	v_mul_f32 v19, v27, v19
	v_med3_f32 v26, v22, s9, v150
	v_mul_f32 v18, v18, s8
	v_mul_f32 v19, v19, s8
	v_med3_f32 v23, v23, s9, v150
	v_mov_b32_e32 v22, 0
	v_cvt_pk_fp8_f32 v22, v26, v23
	v_med3_f32 v18, v18, s9, v150
	v_med3_f32 v19, v19, s9, v150
	v_mov_b32_e32 v23, 0
	v_mul_f32 v28, v28, v36
	v_mul_f32 v29, v29, v37
	v_cvt_pk_fp8_f32 v23, v18, v19
	v_mul_f32 v20, v28, v20
	v_mul_f32 v21, v29, v21
	v_mul_f32 v24, v32, v24
	v_mul_f32 v25, v33, v25
	v_mul_f32 v20, v20, s8
	v_mul_f32 v21, v21, s8
	v_mul_f32 v24, v24, s8
	v_mul_f32 v25, v25, s8
	v_med3_f32 v18, v20, s9, v150
	v_med3_f32 v19, v21, s9, v150
	v_cvt_pk_fp8_f32 v23, v18, v19 op_sel:[0,0,1]
	v_mul_f32_e32 v18, 0xbfb8aa3b, v14
	v_exp_f32_e32 v20, v18
	v_mul_f32_e32 v18, 0xbfb8aa3b, v15
	v_med3_f32 v24, v24, s9, v150
	v_med3_f32 v25, v25, s9, v150
	v_exp_f32_e32 v21, v18
	v_cvt_pk_fp8_f32 v22, v24, v25 op_sel:[0,0,1]
	v_add_u32_e32 v39, 0xa0, v151
	v_mad_i64_i32 v[18:19], s[26:27], v39, s51, v[144:145]
	v_add_f32_e32 v20, 1.0, v20
	v_add_f32_e32 v21, 1.0, v21
	v_rcp_f32_e32 v20, v20
	v_rcp_f32_e32 v21, v21
	v_mul_f32_e32 v26, 0xbfb8aa3b, v10
	global_store_dwordx2 v[18:19], v[22:23], off
	v_mul_f32_e32 v19, 0xbfb8aa3b, v11
	v_exp_f32_e32 v26, v26
	v_exp_f32_e32 v19, v19
	v_mul_f32_e32 v24, 0xbfb8aa3b, v16
	v_mul_f32_e32 v25, 0xbfb8aa3b, v17
	v_mul_f32 v14, v14, v20
	v_mul_f32 v15, v15, v21
	v_mul_f32_e32 v20, 0xbfb8aa3b, v12
	v_mul_f32_e32 v21, 0xbfb8aa3b, v13
	v_exp_f32_e32 v24, v24
	v_exp_f32_e32 v25, v25
	v_add_f32_e32 v18, 1.0, v26
	v_exp_f32_e32 v20, v20
	v_exp_f32_e32 v21, v21
	v_add_f32_e32 v19, 1.0, v19
	v_rcp_f32_e32 v18, v18
	v_rcp_f32_e32 v19, v19
	v_add_f32_e32 v24, 1.0, v24
	v_add_f32_e32 v25, 1.0, v25
	v_add_f32_e32 v20, 1.0, v20
	v_add_f32_e32 v21, 1.0, v21
	v_rcp_f32_e32 v24, v24
	v_rcp_f32_e32 v25, v25
	v_rcp_f32_e32 v20, v20
	v_rcp_f32_e32 v21, v21
	v_mul_f32 v6, v14, v6
	v_mul_f32 v7, v15, v7
	v_mul_f32 v10, v10, v18
	v_mul_f32 v11, v11, v19
	v_mul_f32 v6, v6, s8
	v_mul_f32 v7, v7, s8
	v_mul_f32 v2, v10, v2
	v_mul_f32 v3, v11, v3
	v_med3_f32 v10, v6, s9, v150
	v_mul_f32 v2, v2, s8
	v_mul_f32 v3, v3, s8
	v_med3_f32 v7, v7, s9, v150
	v_mov_b32_e32 v6, 0
	v_cvt_pk_fp8_f32 v6, v10, v7
	v_med3_f32 v2, v2, s9, v150
	v_med3_f32 v3, v3, s9, v150
	v_mov_b32_e32 v7, 0
	v_mul_f32 v16, v16, v24
	v_mul_f32 v17, v17, v25
	v_mul_f32 v12, v12, v20
	v_mul_f32 v13, v13, v21
	v_cvt_pk_fp8_f32 v7, v2, v3
	v_mul_f32 v8, v16, v8
	v_mul_f32 v9, v17, v9
	v_mul_f32 v4, v12, v4
	v_mul_f32 v5, v13, v5
	v_mul_f32 v8, v8, s8
	v_mul_f32 v9, v9, s8
	v_mul_f32 v4, v4, s8
	v_mul_f32 v5, v5, s8
	v_med3_f32 v8, v8, s9, v150
	v_med3_f32 v9, v9, s9, v150
	v_med3_f32 v2, v4, s9, v150
	v_med3_f32 v3, v5, s9, v150
	v_cvt_pk_fp8_f32 v6, v8, v9 op_sel:[0,0,1]
	v_cvt_pk_fp8_f32 v7, v2, v3 op_sel:[0,0,1]
	v_add_u32_e32 v2, 0xb0, v151
	v_mad_i64_i32 v[2:3], s[26:27], v2, s51, v[144:145]
	s_cmp_eq_u32 s46, 10
	s_mov_b64 s[26:27], -1
	global_store_dwordx2 v[2:3], v[6:7], off
	s_cbranch_scc1 .LBB0_650
	s_andn2_b64 vcc, exec, s[2:3]
	s_cbranch_vccnz .LBB0_649
	s_barrier
	s_branch .LBB0_649

.LBB0_761:
	s_cmp_gt_i32 s72, 1
	s_cselect_b64 s[52:53], -1, 0
	s_cmp_lt_u32 s72, 4
	s_cselect_b64 s[2:3], -1, 0
	v_cndmask_b32_e64 v130, 0, 1, s[2:3]
	s_mov_b64 s[4:5], -1
	s_and_b64 vcc, exec, s[52:53]
	v_cmp_ne_u32_e64 s[2:3], 1, v130
	s_cbranch_vccz .LBB0_765
	v_mov_b64_e32 v[132:133], v[128:129]
	v_mov_b64_e32 v[144:145], v[116:117]
	v_mov_b64_e32 v[140:141], v[120:121]
	v_mov_b64_e32 v[136:137], v[124:125]
	s_and_b64 vcc, exec, s[2:3]
	v_mov_b64_e32 v[130:131], v[126:127]
	v_mov_b64_e32 v[142:143], v[114:115]
	v_mov_b64_e32 v[138:139], v[118:119]
	v_mov_b64_e32 v[134:135], v[122:123]
	s_cbranch_vccnz .LBB0_764
	v_mul_f32 v132, v128, s20
	v_mul_f32 v133, v129, s20
	v_mul_f32 v130, v126, s20
	v_mul_f32 v131, v127, s20
	v_mul_f32 v136, v124, s20
	v_mul_f32 v137, v125, s20
	v_mul_f32 v134, v122, s20
	v_mul_f32 v135, v123, s20
	v_mul_f32 v140, v120, s20
	v_mul_f32 v141, v121, s20
	v_mul_f32 v138, v118, s20
	v_mul_f32 v139, v119, s20
	v_mul_f32 v144, v116, s20
	v_mul_f32 v145, v117, s20
	v_mul_f32 v142, v114, s20
	v_mul_f32 v143, v115, s20

.LBB0_765:
	s_andn2_b64 vcc, exec, s[4:5]
	s_cbranch_vccnz .LBB0_767
	v_mul_f32_e32 v131, v126, v126
	v_mul_f32_e32 v131, 0xbf38aa3b, v131
	v_fma_f32 v130, |v126|, s76, 1.0
	v_exp_f32_e32 v132, v131
	v_fma_f32 v131, |v127|, s76, 1.0
	v_rcp_f32_e32 v130, v130
	v_rcp_f32_e32 v131, v131
	v_mul_f32_e32 v133, v127, v127
	v_mov_b64_e32 v[142:143], s[24:25]
	v_mul_f32_e32 v133, 0xbf38aa3b, v133
	v_fma_f32 v134, v130, s22, v142
	v_fma_f32 v135, v131, s22, v142
	v_exp_f32_e32 v133, v133
	v_fma_f32 v134, v130, v134, s26
	v_fma_f32 v135, v131, v135, s26
	v_cmp_gt_f32_e32 vcc, 0, v129
	v_fma_f32 v134, v130, v134, s28
	v_fma_f32 v135, v131, v135, s28
	s_nop 0
	v_fma_f32 v134, v130, v134, s30
	v_fma_f32 v135, v131, v135, s30
	s_nop 0
	v_mul_f32 v130, v130, v134
	v_mul_f32 v131, v131, v135
	v_mul_f32_e32 v135, v129, v129
	v_mul_f32 v130, v132, v130
	v_mul_f32 v131, v133, v131
	v_mul_f32_e32 v133, v128, v128
	v_mul_f32_e32 v133, 0xbf38aa3b, v133
	v_fma_f32 v132, |v128|, s76, 1.0
	v_exp_f32_e32 v134, v133
	v_fma_f32 v133, |v129|, s76, 1.0
	v_rcp_f32_e32 v132, v132
	v_rcp_f32_e32 v133, v133
	v_mul_f32_e32 v135, 0xbf38aa3b, v135
	v_exp_f32_e32 v135, v135
	v_mul_f32 v130, v126, v130
	v_mul_f32 v131, v127, v131
	v_fma_f32 v136, v132, s22, v142
	v_fma_f32 v137, v133, s22, v142
	s_nop 0
	v_fma_f32 v136, v132, v136, s26
	v_fma_f32 v137, v133, v137, s26
	s_nop 0
	v_fma_f32 v136, v132, v136, s28
	v_fma_f32 v137, v133, v137, s28
	s_nop 0
	v_fma_f32 v136, v132, v136, s30
	v_fma_f32 v137, v133, v137, s30
	s_nop 0
	v_mul_f32 v132, v132, v136
	v_mul_f32 v133, v133, v137
	s_nop 0
	v_mul_f32 v132, v134, v132
	v_mul_f32 v133, v135, v133
	v_sub_f32_e32 v135, v127, v131
	v_mul_f32 v132, v128, v132
	v_mul_f32 v133, v129, v133
	v_sub_f32_e32 v134, v126, v130
	v_sub_f32_e32 v137, v129, v133
	v_sub_f32_e32 v136, v128, v132
	v_cndmask_b32_e32 v133, v137, v133, vcc
	v_cmp_gt_f32_e32 vcc, 0, v128
	v_mul_f32_e32 v129, v123, v123
	v_mul_f32_e32 v129, 0xbf38aa3b, v129
	v_cndmask_b32_e32 v132, v136, v132, vcc
	v_cmp_gt_f32_e32 vcc, 0, v127
	v_mul_f32_e32 v127, v122, v122
	v_mul_f32_e32 v127, 0xbf38aa3b, v127
	v_cndmask_b32_e32 v131, v135, v131, vcc
	v_cmp_gt_f32_e32 vcc, 0, v126
	v_fma_f32 v126, |v122|, s76, 1.0
	v_exp_f32_e32 v128, v127
	v_fma_f32 v127, |v123|, s76, 1.0
	v_rcp_f32_e32 v126, v126
	v_rcp_f32_e32 v127, v127
	v_cndmask_b32_e32 v130, v134, v130, vcc
	v_exp_f32_e32 v129, v129
	v_cmp_gt_f32_e32 vcc, 0, v125
	v_fma_f32 v134, v126, s22, v142
	v_fma_f32 v135, v127, s22, v142
	s_nop 0
	v_fma_f32 v134, v126, v134, s26
	v_fma_f32 v135, v127, v135, s26
	s_nop 0
	v_fma_f32 v134, v126, v134, s28
	v_fma_f32 v135, v127, v135, s28
	s_nop 0
	v_fma_f32 v134, v126, v134, s30
	v_fma_f32 v135, v127, v135, s30
	s_nop 0
	v_mul_f32 v126, v126, v134
	v_mul_f32 v127, v127, v135
	v_mul_f32_e32 v135, v125, v125
	v_mul_f32 v126, v128, v126
	v_mul_f32 v127, v129, v127
	v_mul_f32_e32 v129, v124, v124
	v_mul_f32_e32 v129, 0xbf38aa3b, v129
	v_fma_f32 v128, |v124|, s76, 1.0
	v_exp_f32_e32 v134, v129
	v_fma_f32 v129, |v125|, s76, 1.0
	v_rcp_f32_e32 v128, v128
	v_rcp_f32_e32 v129, v129
	v_mul_f32_e32 v135, 0xbf38aa3b, v135
	v_exp_f32_e32 v135, v135
	v_mul_f32 v126, v122, v126
	v_mul_f32 v127, v123, v127
	v_fma_f32 v136, v128, s22, v142
	v_fma_f32 v137, v129, s22, v142
	s_nop 0
	v_fma_f32 v136, v128, v136, s26
	v_fma_f32 v137, v129, v137, s26
	s_nop 0
	v_fma_f32 v136, v128, v136, s28
	v_fma_f32 v137, v129, v137, s28
	s_nop 0
	v_fma_f32 v136, v128, v136, s30
	v_fma_f32 v137, v129, v137, s30
	s_nop 0
	v_mul_f32 v128, v128, v136
	v_mul_f32 v129, v129, v137
	s_nop 0
	v_mul_f32 v128, v134, v128
	v_mul_f32 v129, v135, v129
	v_sub_f32_e32 v135, v123, v127
	v_mul_f32 v128, v124, v128
	v_mul_f32 v129, v125, v129
	v_sub_f32_e32 v134, v122, v126
	v_sub_f32_e32 v137, v125, v129
	v_sub_f32_e32 v136, v124, v128
	v_cndmask_b32_e32 v137, v137, v129, vcc
	v_cmp_gt_f32_e32 vcc, 0, v124
	v_mul_f32_e32 v125, v119, v119
	v_mul_f32_e32 v125, 0xbf38aa3b, v125
	v_cndmask_b32_e32 v136, v136, v128, vcc
	v_cmp_gt_f32_e32 vcc, 0, v123
	v_mul_f32_e32 v123, v118, v118
	v_mul_f32_e32 v123, 0xbf38aa3b, v123
	v_cndmask_b32_e32 v135, v135, v127, vcc
	v_cmp_gt_f32_e32 vcc, 0, v122
	v_fma_f32 v122, |v118|, s76, 1.0
	v_exp_f32_e32 v124, v123
	v_fma_f32 v123, |v119|, s76, 1.0
	v_rcp_f32_e32 v122, v122
	v_rcp_f32_e32 v123, v123
	v_cndmask_b32_e32 v134, v134, v126, vcc
	v_exp_f32_e32 v125, v125
	v_cmp_gt_f32_e32 vcc, 0, v121
	v_fma_f32 v126, v122, s22, v142
	v_fma_f32 v127, v123, s22, v142
	s_nop 0
	v_fma_f32 v126, v122, v126, s26
	v_fma_f32 v127, v123, v127, s26
	s_nop 0
	v_fma_f32 v126, v122, v126, s28
	v_fma_f32 v127, v123, v127, s28
	s_nop 0
	v_fma_f32 v126, v122, v126, s30
	v_fma_f32 v127, v123, v127, s30
	s_nop 0
	v_mul_f32 v122, v122, v126
	v_mul_f32 v123, v123, v127
	v_mul_f32_e32 v127, v121, v121
	v_mul_f32 v122, v124, v122
	v_mul_f32 v123, v125, v123
	v_mul_f32_e32 v125, v120, v120
	v_mul_f32_e32 v125, 0xbf38aa3b, v125
	v_fma_f32 v124, |v120|, s76, 1.0
	v_exp_f32_e32 v126, v125
	v_fma_f32 v125, |v121|, s76, 1.0
	v_rcp_f32_e32 v124, v124
	v_rcp_f32_e32 v125, v125
	v_mul_f32_e32 v127, 0xbf38aa3b, v127
	v_exp_f32_e32 v127, v127
	v_mul_f32 v122, v118, v122
	v_mul_f32 v123, v119, v123
	v_fma_f32 v128, v124, s22, v142
	v_fma_f32 v129, v125, s22, v142
	s_nop 0
	v_fma_f32 v128, v124, v128, s26
	v_fma_f32 v129, v125, v129, s26
	s_nop 0
	v_fma_f32 v128, v124, v128, s28
	v_fma_f32 v129, v125, v129, s28
	s_nop 0
	v_fma_f32 v128, v124, v128, s30
	v_fma_f32 v129, v125, v129, s30
	s_nop 0
	v_mul_f32 v124, v124, v128
	v_mul_f32 v125, v125, v129
	s_nop 0
	v_mul_f32 v124, v126, v124
	v_mul_f32 v125, v127, v125
	v_sub_f32_e32 v127, v119, v123
	v_mul_f32 v124, v120, v124
	v_mul_f32 v125, v121, v125
	v_sub_f32_e32 v126, v118, v122
	v_sub_f32_e32 v129, v121, v125
	v_sub_f32_e32 v128, v120, v124
	v_cndmask_b32_e32 v141, v129, v125, vcc
	v_cmp_gt_f32_e32 vcc, 0, v120
	v_mul_f32_e32 v121, v115, v115
	v_mul_f32_e32 v121, 0xbf38aa3b, v121
	v_cndmask_b32_e32 v140, v128, v124, vcc
	v_cmp_gt_f32_e32 vcc, 0, v119
	v_mul_f32_e32 v119, v114, v114
	v_mul_f32_e32 v119, 0xbf38aa3b, v119
	v_cndmask_b32_e32 v139, v127, v123, vcc
	v_cmp_gt_f32_e32 vcc, 0, v118
	v_fma_f32 v118, |v114|, s76, 1.0
	v_exp_f32_e32 v120, v119
	v_fma_f32 v119, |v115|, s76, 1.0
	v_rcp_f32_e32 v118, v118
	v_rcp_f32_e32 v119, v119
	v_cndmask_b32_e32 v138, v126, v122, vcc
	v_exp_f32_e32 v121, v121
	v_cmp_gt_f32_e32 vcc, 0, v117
	v_fma_f32 v122, v118, s22, v142
	v_fma_f32 v123, v119, s22, v142
	s_nop 0
	v_fma_f32 v122, v118, v122, s26
	v_fma_f32 v123, v119, v123, s26
	s_nop 0
	v_fma_f32 v122, v118, v122, s28
	v_fma_f32 v123, v119, v123, s28
	s_nop 0
	v_fma_f32 v122, v118, v122, s30
	v_fma_f32 v123, v119, v123, s30
	s_nop 0
	v_mul_f32 v118, v118, v122
	v_mul_f32 v119, v119, v123
	v_mul_f32_e32 v123, v117, v117
	v_mul_f32 v118, v120, v118
	v_mul_f32 v119, v121, v119
	v_mul_f32_e32 v121, v116, v116
	v_mul_f32_e32 v121, 0xbf38aa3b, v121
	v_fma_f32 v120, |v116|, s76, 1.0
	v_exp_f32_e32 v122, v121
	v_fma_f32 v121, |v117|, s76, 1.0
	v_rcp_f32_e32 v120, v120
	v_rcp_f32_e32 v121, v121
	v_mul_f32_e32 v123, 0xbf38aa3b, v123
	v_exp_f32_e32 v123, v123
	v_mul_f32 v118, v114, v118
	v_mul_f32 v119, v115, v119
	v_fma_f32 v124, v120, s22, v142
	v_fma_f32 v125, v121, s22, v142
	s_nop 0
	v_fma_f32 v124, v120, v124, s26
	v_fma_f32 v125, v121, v125, s26
	s_nop 0
	v_fma_f32 v124, v120, v124, s28
	v_fma_f32 v125, v121, v125, s28
	s_nop 0
	v_fma_f32 v124, v120, v124, s30
	v_fma_f32 v125, v121, v125, s30
	s_nop 0
	v_mul_f32 v120, v120, v124
	v_mul_f32 v121, v121, v125
	s_nop 0
	v_mul_f32 v120, v122, v120
	v_mul_f32 v121, v123, v121
	v_sub_f32_e32 v123, v115, v119
	v_mul_f32 v120, v116, v120
	v_mul_f32 v121, v117, v121
	v_sub_f32_e32 v122, v114, v118
	v_sub_f32_e32 v125, v117, v121
	v_sub_f32_e32 v124, v116, v120
	v_cndmask_b32_e32 v145, v125, v121, vcc
	v_cmp_gt_f32_e32 vcc, 0, v116
	s_nop 1
	v_cndmask_b32_e32 v144, v124, v120, vcc
	v_cmp_gt_f32_e32 vcc, 0, v115
	s_nop 1
	v_cndmask_b32_e32 v143, v123, v119, vcc
	v_cmp_gt_f32_e32 vcc, 0, v114
	s_nop 1
	v_cndmask_b32_e32 v142, v122, v118, vcc
.LBB0_767:
	v_cvt_pk_bf16_f32 v114, v130, v131
	v_cvt_pk_bf16_f32 v115, v132, v133
	s_lshl_b32 s4, s72, 8
	v_cvt_pk_bf16_f32 v116, v134, v135
	s_ashr_i32 s5, s4, 31
	v_lshl_add_u32 v166, s73, 8, v162
	v_lshl_add_u64 v[160:161], s[4:5], 1, v[154:155]
	v_mad_i64_i32 v[118:119], s[4:5], v166, s77, v[160:161]
	v_cvt_pk_bf16_f32 v117, v136, v137
	global_store_dwordx4 v[118:119], v[114:117], off
	s_nop 1
	v_cvt_pk_bf16_f32 v114, v138, v139
	v_cvt_pk_bf16_f32 v115, v140, v141
	v_cvt_pk_bf16_f32 v116, v142, v143
	v_cvt_pk_bf16_f32 v117, v144, v145
	global_store_dwordx4 v[118:119], v[114:117], off offset:256
	s_andn2_b64 vcc, exec, s[52:53]
	s_mov_b64 s[38:39], -1
	v_cndmask_b32_e64 v114, 0, 1, s[52:53]
	v_cmp_ne_u32_e64 s[4:5], 1, v114
	s_cbranch_vccnz .LBB0_771
	v_mov_b64_e32 v[116:117], v[112:113]
	v_mov_b64_e32 v[128:129], v[100:101]
	v_mov_b64_e32 v[124:125], v[104:105]
	v_mov_b64_e32 v[120:121], v[108:109]
	s_and_b64 vcc, exec, s[2:3]
	v_mov_b64_e32 v[114:115], v[110:111]
	v_mov_b64_e32 v[126:127], v[98:99]
	v_mov_b64_e32 v[122:123], v[102:103]
	v_mov_b64_e32 v[118:119], v[106:107]
	s_cbranch_vccnz .LBB0_770
	v_mul_f32 v116, v112, s20
	v_mul_f32 v117, v113, s20
	v_mul_f32 v114, v110, s20
	v_mul_f32 v115, v111, s20
	v_mul_f32 v120, v108, s20
	v_mul_f32 v121, v109, s20
	v_mul_f32 v118, v106, s20
	v_mul_f32 v119, v107, s20
	v_mul_f32 v124, v104, s20
	v_mul_f32 v125, v105, s20
	v_mul_f32 v122, v102, s20
	v_mul_f32 v123, v103, s20
	v_mul_f32 v128, v100, s20
	v_mul_f32 v129, v101, s20
	v_mul_f32 v126, v98, s20
	v_mul_f32 v127, v99, s20

.LBB0_771:
	s_andn2_b64 vcc, exec, s[38:39]
	s_cbranch_vccnz .LBB0_773
	v_mul_f32_e32 v115, v110, v110
	v_mul_f32_e32 v115, 0xbf38aa3b, v115
	v_fma_f32 v114, |v110|, s76, 1.0
	v_exp_f32_e32 v116, v115
	v_fma_f32 v115, |v111|, s76, 1.0
	v_rcp_f32_e32 v114, v114
	v_rcp_f32_e32 v115, v115
	v_mul_f32_e32 v117, v111, v111
	v_mov_b64_e32 v[126:127], s[24:25]
	v_mul_f32_e32 v117, 0xbf38aa3b, v117
	v_fma_f32 v118, v114, s22, v126
	v_fma_f32 v119, v115, s22, v126
	v_exp_f32_e32 v117, v117
	v_fma_f32 v118, v114, v118, s26
	v_fma_f32 v119, v115, v119, s26
	v_cmp_gt_f32_e32 vcc, 0, v113
	v_fma_f32 v118, v114, v118, s28
	v_fma_f32 v119, v115, v119, s28
	s_nop 0
	v_fma_f32 v118, v114, v118, s30
	v_fma_f32 v119, v115, v119, s30
	s_nop 0
	v_mul_f32 v114, v114, v118
	v_mul_f32 v115, v115, v119
	v_mul_f32_e32 v119, v113, v113
	v_mul_f32 v114, v116, v114
	v_mul_f32 v115, v117, v115
	v_mul_f32_e32 v117, v112, v112
	v_mul_f32_e32 v117, 0xbf38aa3b, v117
	v_fma_f32 v116, |v112|, s76, 1.0
	v_exp_f32_e32 v118, v117
	v_fma_f32 v117, |v113|, s76, 1.0
	v_rcp_f32_e32 v116, v116
	v_rcp_f32_e32 v117, v117
	v_mul_f32_e32 v119, 0xbf38aa3b, v119
	v_exp_f32_e32 v119, v119
	v_mul_f32 v114, v110, v114
	v_mul_f32 v115, v111, v115
	v_fma_f32 v120, v116, s22, v126
	v_fma_f32 v121, v117, s22, v126
	s_nop 0
	v_fma_f32 v120, v116, v120, s26
	v_fma_f32 v121, v117, v121, s26
	s_nop 0
	v_fma_f32 v120, v116, v120, s28
	v_fma_f32 v121, v117, v121, s28
	s_nop 0
	v_fma_f32 v120, v116, v120, s30
	v_fma_f32 v121, v117, v121, s30
	s_nop 0
	v_mul_f32 v116, v116, v120
	v_mul_f32 v117, v117, v121
	s_nop 0
	v_mul_f32 v116, v118, v116
	v_mul_f32 v117, v119, v117
	v_sub_f32_e32 v119, v111, v115
	v_mul_f32 v116, v112, v116
	v_mul_f32 v117, v113, v117
	v_sub_f32_e32 v118, v110, v114
	v_sub_f32_e32 v121, v113, v117
	v_sub_f32_e32 v120, v112, v116
	v_cndmask_b32_e32 v117, v121, v117, vcc
	v_cmp_gt_f32_e32 vcc, 0, v112
	v_mul_f32_e32 v113, v107, v107
	v_mul_f32_e32 v113, 0xbf38aa3b, v113
	v_cndmask_b32_e32 v116, v120, v116, vcc
	v_cmp_gt_f32_e32 vcc, 0, v111
	v_mul_f32_e32 v111, v106, v106
	v_mul_f32_e32 v111, 0xbf38aa3b, v111
	v_cndmask_b32_e32 v115, v119, v115, vcc
	v_cmp_gt_f32_e32 vcc, 0, v110
	v_fma_f32 v110, |v106|, s76, 1.0
	v_exp_f32_e32 v112, v111
	v_fma_f32 v111, |v107|, s76, 1.0
	v_rcp_f32_e32 v110, v110
	v_rcp_f32_e32 v111, v111
	v_cndmask_b32_e32 v114, v118, v114, vcc
	v_exp_f32_e32 v113, v113
	v_cmp_gt_f32_e32 vcc, 0, v109
	v_fma_f32 v118, v110, s22, v126
	v_fma_f32 v119, v111, s22, v126
	s_nop 0
	v_fma_f32 v118, v110, v118, s26
	v_fma_f32 v119, v111, v119, s26
	s_nop 0
	v_fma_f32 v118, v110, v118, s28
	v_fma_f32 v119, v111, v119, s28
	s_nop 0
	v_fma_f32 v118, v110, v118, s30
	v_fma_f32 v119, v111, v119, s30
	s_nop 0
	v_mul_f32 v110, v110, v118
	v_mul_f32 v111, v111, v119
	v_mul_f32_e32 v119, v109, v109
	v_mul_f32 v110, v112, v110
	v_mul_f32 v111, v113, v111
	v_mul_f32_e32 v113, v108, v108
	v_mul_f32_e32 v113, 0xbf38aa3b, v113
	v_fma_f32 v112, |v108|, s76, 1.0
	v_exp_f32_e32 v118, v113
	v_fma_f32 v113, |v109|, s76, 1.0
	v_rcp_f32_e32 v112, v112
	v_rcp_f32_e32 v113, v113
	v_mul_f32_e32 v119, 0xbf38aa3b, v119
	v_exp_f32_e32 v119, v119
	v_mul_f32 v110, v106, v110
	v_mul_f32 v111, v107, v111
	v_fma_f32 v120, v112, s22, v126
	v_fma_f32 v121, v113, s22, v126
	s_nop 0
	v_fma_f32 v120, v112, v120, s26
	v_fma_f32 v121, v113, v121, s26
	s_nop 0
	v_fma_f32 v120, v112, v120, s28
	v_fma_f32 v121, v113, v121, s28
	s_nop 0
	v_fma_f32 v120, v112, v120, s30
	v_fma_f32 v121, v113, v121, s30
	s_nop 0
	v_mul_f32 v112, v112, v120
	v_mul_f32 v113, v113, v121
	s_nop 0
	v_mul_f32 v112, v118, v112
	v_mul_f32 v113, v119, v113
	v_sub_f32_e32 v119, v107, v111
	v_mul_f32 v112, v108, v112
	v_mul_f32 v113, v109, v113
	v_sub_f32_e32 v118, v106, v110
	v_sub_f32_e32 v121, v109, v113
	v_sub_f32_e32 v120, v108, v112
	v_cndmask_b32_e32 v121, v121, v113, vcc
	v_cmp_gt_f32_e32 vcc, 0, v108
	v_mul_f32_e32 v109, v103, v103
	v_mul_f32_e32 v109, 0xbf38aa3b, v109
	v_cndmask_b32_e32 v120, v120, v112, vcc
	v_cmp_gt_f32_e32 vcc, 0, v107
	v_mul_f32_e32 v107, v102, v102
	v_mul_f32_e32 v107, 0xbf38aa3b, v107
	v_cndmask_b32_e32 v119, v119, v111, vcc
	v_cmp_gt_f32_e32 vcc, 0, v106
	v_fma_f32 v106, |v102|, s76, 1.0
	v_exp_f32_e32 v108, v107
	v_fma_f32 v107, |v103|, s76, 1.0
	v_rcp_f32_e32 v106, v106
	v_rcp_f32_e32 v107, v107
	v_cndmask_b32_e32 v118, v118, v110, vcc
	v_exp_f32_e32 v109, v109
	v_cmp_gt_f32_e32 vcc, 0, v105
	v_fma_f32 v110, v106, s22, v126
	v_fma_f32 v111, v107, s22, v126
	s_nop 0
	v_fma_f32 v110, v106, v110, s26
	v_fma_f32 v111, v107, v111, s26
	s_nop 0
	v_fma_f32 v110, v106, v110, s28
	v_fma_f32 v111, v107, v111, s28
	s_nop 0
	v_fma_f32 v110, v106, v110, s30
	v_fma_f32 v111, v107, v111, s30
	s_nop 0
	v_mul_f32 v106, v106, v110
	v_mul_f32 v107, v107, v111
	v_mul_f32_e32 v111, v105, v105
	v_mul_f32 v106, v108, v106
	v_mul_f32 v107, v109, v107
	v_mul_f32_e32 v109, v104, v104
	v_mul_f32_e32 v109, 0xbf38aa3b, v109
	v_fma_f32 v108, |v104|, s76, 1.0
	v_exp_f32_e32 v110, v109
	v_fma_f32 v109, |v105|, s76, 1.0
	v_rcp_f32_e32 v108, v108
	v_rcp_f32_e32 v109, v109
	v_mul_f32_e32 v111, 0xbf38aa3b, v111
	v_exp_f32_e32 v111, v111
	v_mul_f32 v106, v102, v106
	v_mul_f32 v107, v103, v107
	v_fma_f32 v112, v108, s22, v126
	v_fma_f32 v113, v109, s22, v126
	s_nop 0
	v_fma_f32 v112, v108, v112, s26
	v_fma_f32 v113, v109, v113, s26
	s_nop 0
	v_fma_f32 v112, v108, v112, s28
	v_fma_f32 v113, v109, v113, s28
	s_nop 0
	v_fma_f32 v112, v108, v112, s30
	v_fma_f32 v113, v109, v113, s30
	s_nop 0
	v_mul_f32 v108, v108, v112
	v_mul_f32 v109, v109, v113
	s_nop 0
	v_mul_f32 v108, v110, v108
	v_mul_f32 v109, v111, v109
	v_sub_f32_e32 v111, v103, v107
	v_mul_f32 v108, v104, v108
	v_mul_f32 v109, v105, v109
	v_sub_f32_e32 v110, v102, v106
	v_sub_f32_e32 v113, v105, v109
	v_sub_f32_e32 v112, v104, v108
	v_cndmask_b32_e32 v125, v113, v109, vcc
	v_cmp_gt_f32_e32 vcc, 0, v104
	v_mul_f32_e32 v105, v99, v99
	v_mul_f32_e32 v105, 0xbf38aa3b, v105
	v_cndmask_b32_e32 v124, v112, v108, vcc
	v_cmp_gt_f32_e32 vcc, 0, v103
	v_mul_f32_e32 v103, v98, v98
	v_mul_f32_e32 v103, 0xbf38aa3b, v103
	v_cndmask_b32_e32 v123, v111, v107, vcc
	v_cmp_gt_f32_e32 vcc, 0, v102
	v_fma_f32 v102, |v98|, s76, 1.0
	v_exp_f32_e32 v104, v103
	v_fma_f32 v103, |v99|, s76, 1.0
	v_rcp_f32_e32 v102, v102
	v_rcp_f32_e32 v103, v103
	v_cndmask_b32_e32 v122, v110, v106, vcc
	v_exp_f32_e32 v105, v105
	v_cmp_gt_f32_e32 vcc, 0, v101
	v_fma_f32 v106, v102, s22, v126
	v_fma_f32 v107, v103, s22, v126
	s_nop 0
	v_fma_f32 v106, v102, v106, s26
	v_fma_f32 v107, v103, v107, s26
	s_nop 0
	v_fma_f32 v106, v102, v106, s28
	v_fma_f32 v107, v103, v107, s28
	s_nop 0
	v_fma_f32 v106, v102, v106, s30
	v_fma_f32 v107, v103, v107, s30
	s_nop 0
	v_mul_f32 v102, v102, v106
	v_mul_f32 v103, v103, v107
	v_mul_f32_e32 v107, v101, v101
	v_mul_f32 v102, v104, v102
	v_mul_f32 v103, v105, v103
	v_mul_f32_e32 v105, v100, v100
	v_mul_f32_e32 v105, 0xbf38aa3b, v105
	v_fma_f32 v104, |v100|, s76, 1.0
	v_exp_f32_e32 v106, v105
	v_fma_f32 v105, |v101|, s76, 1.0
	v_rcp_f32_e32 v104, v104
	v_rcp_f32_e32 v105, v105
	v_mul_f32_e32 v107, 0xbf38aa3b, v107
	v_exp_f32_e32 v107, v107
	v_mul_f32 v102, v98, v102
	v_mul_f32 v103, v99, v103
	v_fma_f32 v108, v104, s22, v126
	v_fma_f32 v109, v105, s22, v126
	s_nop 0
	v_fma_f32 v108, v104, v108, s26
	v_fma_f32 v109, v105, v109, s26
	s_nop 0
	v_fma_f32 v108, v104, v108, s28
	v_fma_f32 v109, v105, v109, s28
	s_nop 0
	v_fma_f32 v108, v104, v108, s30
	v_fma_f32 v109, v105, v109, s30
	s_nop 0
	v_mul_f32 v104, v104, v108
	v_mul_f32 v105, v105, v109
	s_nop 0
	v_mul_f32 v104, v106, v104
	v_mul_f32 v105, v107, v105
	v_sub_f32_e32 v107, v99, v103
	v_mul_f32 v104, v100, v104
	v_mul_f32 v105, v101, v105
	v_sub_f32_e32 v106, v98, v102
	v_sub_f32_e32 v109, v101, v105
	v_sub_f32_e32 v108, v100, v104
	v_cndmask_b32_e32 v129, v109, v105, vcc
	v_cmp_gt_f32_e32 vcc, 0, v100
	s_nop 1
	v_cndmask_b32_e32 v128, v108, v104, vcc
	v_cmp_gt_f32_e32 vcc, 0, v99
	s_nop 1
	v_cndmask_b32_e32 v127, v107, v103, vcc
	v_cmp_gt_f32_e32 vcc, 0, v98
	s_nop 1
	v_cndmask_b32_e32 v126, v106, v102, vcc
.LBB0_773:
	v_or_b32_e32 v98, 16, v166
	v_mad_i64_i32 v[102:103], s[38:39], v98, s77, v[160:161]
	v_cvt_pk_bf16_f32 v98, v114, v115
	v_cvt_pk_bf16_f32 v99, v116, v117
	v_cvt_pk_bf16_f32 v100, v118, v119
	v_cvt_pk_bf16_f32 v101, v120, v121
	global_store_dwordx4 v[102:103], v[98:101], off
	s_nop 1
	v_cvt_pk_bf16_f32 v98, v122, v123
	v_cvt_pk_bf16_f32 v99, v124, v125
	v_cvt_pk_bf16_f32 v100, v126, v127
	v_cvt_pk_bf16_f32 v101, v128, v129
	s_and_b64 vcc, exec, s[4:5]
	s_mov_b64 s[38:39], -1
	global_store_dwordx4 v[102:103], v[98:101], off offset:256
	s_cbranch_vccnz .LBB0_777
	s_nop 0
	v_mov_b64_e32 v[100:101], v[96:97]
	v_mov_b64_e32 v[112:113], v[84:85]
	v_mov_b64_e32 v[108:109], v[88:89]
	v_mov_b64_e32 v[104:105], v[92:93]
	s_and_b64 vcc, exec, s[2:3]
	v_mov_b64_e32 v[98:99], v[94:95]
	v_mov_b64_e32 v[110:111], v[82:83]
	v_mov_b64_e32 v[106:107], v[86:87]
	v_mov_b64_e32 v[102:103], v[90:91]
	s_cbranch_vccnz .LBB0_776
	v_mul_f32 v100, v96, s20
	v_mul_f32 v101, v97, s20
	v_mul_f32 v98, v94, s20
	v_mul_f32 v99, v95, s20
	v_mul_f32 v104, v92, s20
	v_mul_f32 v105, v93, s20
	v_mul_f32 v102, v90, s20
	v_mul_f32 v103, v91, s20
	v_mul_f32 v108, v88, s20
	v_mul_f32 v109, v89, s20
	v_mul_f32 v106, v86, s20
	v_mul_f32 v107, v87, s20
	v_mul_f32 v112, v84, s20
	v_mul_f32 v113, v85, s20
	v_mul_f32 v110, v82, s20
	v_mul_f32 v111, v83, s20

.LBB0_777:
	s_andn2_b64 vcc, exec, s[38:39]
	s_cbranch_vccnz .LBB0_779
	v_mul_f32_e32 v99, v94, v94
	v_mul_f32_e32 v99, 0xbf38aa3b, v99
	v_fma_f32 v98, |v94|, s76, 1.0
	v_exp_f32_e32 v100, v99
	v_fma_f32 v99, |v95|, s76, 1.0
	v_rcp_f32_e32 v98, v98
	v_rcp_f32_e32 v99, v99
	v_mul_f32_e32 v101, v95, v95
	v_mov_b64_e32 v[110:111], s[24:25]
	v_mul_f32_e32 v101, 0xbf38aa3b, v101
	v_fma_f32 v102, v98, s22, v110
	v_fma_f32 v103, v99, s22, v110
	v_exp_f32_e32 v101, v101
	v_fma_f32 v102, v98, v102, s26
	v_fma_f32 v103, v99, v103, s26
	v_cmp_gt_f32_e32 vcc, 0, v97
	v_fma_f32 v102, v98, v102, s28
	v_fma_f32 v103, v99, v103, s28
	s_nop 0
	v_fma_f32 v102, v98, v102, s30
	v_fma_f32 v103, v99, v103, s30
	s_nop 0
	v_mul_f32 v98, v98, v102
	v_mul_f32 v99, v99, v103
	v_mul_f32_e32 v103, v97, v97
	v_mul_f32 v98, v100, v98
	v_mul_f32 v99, v101, v99
	v_mul_f32_e32 v101, v96, v96
	v_mul_f32_e32 v101, 0xbf38aa3b, v101
	v_fma_f32 v100, |v96|, s76, 1.0
	v_exp_f32_e32 v102, v101
	v_fma_f32 v101, |v97|, s76, 1.0
	v_rcp_f32_e32 v100, v100
	v_rcp_f32_e32 v101, v101
	v_mul_f32_e32 v103, 0xbf38aa3b, v103
	v_exp_f32_e32 v103, v103
	v_mul_f32 v98, v94, v98
	v_mul_f32 v99, v95, v99
	v_fma_f32 v104, v100, s22, v110
	v_fma_f32 v105, v101, s22, v110
	s_nop 0
	v_fma_f32 v104, v100, v104, s26
	v_fma_f32 v105, v101, v105, s26
	s_nop 0
	v_fma_f32 v104, v100, v104, s28
	v_fma_f32 v105, v101, v105, s28
	s_nop 0
	v_fma_f32 v104, v100, v104, s30
	v_fma_f32 v105, v101, v105, s30
	s_nop 0
	v_mul_f32 v100, v100, v104
	v_mul_f32 v101, v101, v105
	s_nop 0
	v_mul_f32 v100, v102, v100
	v_mul_f32 v101, v103, v101
	v_sub_f32_e32 v103, v95, v99
	v_mul_f32 v100, v96, v100
	v_mul_f32 v101, v97, v101
	v_sub_f32_e32 v102, v94, v98
	v_sub_f32_e32 v105, v97, v101
	v_sub_f32_e32 v104, v96, v100
	v_cndmask_b32_e32 v101, v105, v101, vcc
	v_cmp_gt_f32_e32 vcc, 0, v96
	v_mul_f32_e32 v97, v91, v91
	v_mul_f32_e32 v97, 0xbf38aa3b, v97
	v_cndmask_b32_e32 v100, v104, v100, vcc
	v_cmp_gt_f32_e32 vcc, 0, v95
	v_mul_f32_e32 v95, v90, v90
	v_mul_f32_e32 v95, 0xbf38aa3b, v95
	v_cndmask_b32_e32 v99, v103, v99, vcc
	v_cmp_gt_f32_e32 vcc, 0, v94
	v_fma_f32 v94, |v90|, s76, 1.0
	v_exp_f32_e32 v96, v95
	v_fma_f32 v95, |v91|, s76, 1.0
	v_rcp_f32_e32 v94, v94
	v_rcp_f32_e32 v95, v95
	v_cndmask_b32_e32 v98, v102, v98, vcc
	v_exp_f32_e32 v97, v97
	v_cmp_gt_f32_e32 vcc, 0, v93
	v_fma_f32 v102, v94, s22, v110
	v_fma_f32 v103, v95, s22, v110
	s_nop 0
	v_fma_f32 v102, v94, v102, s26
	v_fma_f32 v103, v95, v103, s26
	s_nop 0
	v_fma_f32 v102, v94, v102, s28
	v_fma_f32 v103, v95, v103, s28
	s_nop 0
	v_fma_f32 v102, v94, v102, s30
	v_fma_f32 v103, v95, v103, s30
	s_nop 0
	v_mul_f32 v94, v94, v102
	v_mul_f32 v95, v95, v103
	v_mul_f32_e32 v103, v93, v93
	v_mul_f32 v94, v96, v94
	v_mul_f32 v95, v97, v95
	v_mul_f32_e32 v97, v92, v92
	v_mul_f32_e32 v97, 0xbf38aa3b, v97
	v_fma_f32 v96, |v92|, s76, 1.0
	v_exp_f32_e32 v102, v97
	v_fma_f32 v97, |v93|, s76, 1.0
	v_rcp_f32_e32 v96, v96
	v_rcp_f32_e32 v97, v97
	v_mul_f32_e32 v103, 0xbf38aa3b, v103
	v_exp_f32_e32 v103, v103
	v_mul_f32 v94, v90, v94
	v_mul_f32 v95, v91, v95
	v_fma_f32 v104, v96, s22, v110
	v_fma_f32 v105, v97, s22, v110
	s_nop 0
	v_fma_f32 v104, v96, v104, s26
	v_fma_f32 v105, v97, v105, s26
	s_nop 0
	v_fma_f32 v104, v96, v104, s28
	v_fma_f32 v105, v97, v105, s28
	s_nop 0
	v_fma_f32 v104, v96, v104, s30
	v_fma_f32 v105, v97, v105, s30
	s_nop 0
	v_mul_f32 v96, v96, v104
	v_mul_f32 v97, v97, v105
	s_nop 0
	v_mul_f32 v96, v102, v96
	v_mul_f32 v97, v103, v97
	v_sub_f32_e32 v103, v91, v95
	v_mul_f32 v96, v92, v96
	v_mul_f32 v97, v93, v97
	v_sub_f32_e32 v102, v90, v94
	v_sub_f32_e32 v105, v93, v97
	v_sub_f32_e32 v104, v92, v96
	v_cndmask_b32_e32 v105, v105, v97, vcc
	v_cmp_gt_f32_e32 vcc, 0, v92
	v_mul_f32_e32 v93, v87, v87
	v_mul_f32_e32 v93, 0xbf38aa3b, v93
	v_cndmask_b32_e32 v104, v104, v96, vcc
	v_cmp_gt_f32_e32 vcc, 0, v91
	v_mul_f32_e32 v91, v86, v86
	v_mul_f32_e32 v91, 0xbf38aa3b, v91
	v_cndmask_b32_e32 v103, v103, v95, vcc
	v_cmp_gt_f32_e32 vcc, 0, v90
	v_fma_f32 v90, |v86|, s76, 1.0
	v_exp_f32_e32 v92, v91
	v_fma_f32 v91, |v87|, s76, 1.0
	v_rcp_f32_e32 v90, v90
	v_rcp_f32_e32 v91, v91
	v_cndmask_b32_e32 v102, v102, v94, vcc
	v_exp_f32_e32 v93, v93
	v_cmp_gt_f32_e32 vcc, 0, v89
	v_fma_f32 v94, v90, s22, v110
	v_fma_f32 v95, v91, s22, v110
	s_nop 0
	v_fma_f32 v94, v90, v94, s26
	v_fma_f32 v95, v91, v95, s26
	s_nop 0
	v_fma_f32 v94, v90, v94, s28
	v_fma_f32 v95, v91, v95, s28
	s_nop 0
	v_fma_f32 v94, v90, v94, s30
	v_fma_f32 v95, v91, v95, s30
	s_nop 0
	v_mul_f32 v90, v90, v94
	v_mul_f32 v91, v91, v95
	v_mul_f32_e32 v95, v89, v89
	v_mul_f32 v90, v92, v90
	v_mul_f32 v91, v93, v91
	v_mul_f32_e32 v93, v88, v88
	v_mul_f32_e32 v93, 0xbf38aa3b, v93
	v_fma_f32 v92, |v88|, s76, 1.0
	v_exp_f32_e32 v94, v93
	v_fma_f32 v93, |v89|, s76, 1.0
	v_rcp_f32_e32 v92, v92
	v_rcp_f32_e32 v93, v93
	v_mul_f32_e32 v95, 0xbf38aa3b, v95
	v_exp_f32_e32 v95, v95
	v_mul_f32 v90, v86, v90
	v_mul_f32 v91, v87, v91
	v_fma_f32 v96, v92, s22, v110
	v_fma_f32 v97, v93, s22, v110
	s_nop 0
	v_fma_f32 v96, v92, v96, s26
	v_fma_f32 v97, v93, v97, s26
	s_nop 0
	v_fma_f32 v96, v92, v96, s28
	v_fma_f32 v97, v93, v97, s28
	s_nop 0
	v_fma_f32 v96, v92, v96, s30
	v_fma_f32 v97, v93, v97, s30
	s_nop 0
	v_mul_f32 v92, v92, v96
	v_mul_f32 v93, v93, v97
	s_nop 0
	v_mul_f32 v92, v94, v92
	v_mul_f32 v93, v95, v93
	v_sub_f32_e32 v95, v87, v91
	v_mul_f32 v92, v88, v92
	v_mul_f32 v93, v89, v93
	v_sub_f32_e32 v94, v86, v90
	v_sub_f32_e32 v97, v89, v93
	v_sub_f32_e32 v96, v88, v92
	v_cndmask_b32_e32 v109, v97, v93, vcc
	v_cmp_gt_f32_e32 vcc, 0, v88
	v_mul_f32_e32 v89, v83, v83
	v_mul_f32_e32 v89, 0xbf38aa3b, v89
	v_cndmask_b32_e32 v108, v96, v92, vcc
	v_cmp_gt_f32_e32 vcc, 0, v87
	v_mul_f32_e32 v87, v82, v82
	v_mul_f32_e32 v87, 0xbf38aa3b, v87
	v_cndmask_b32_e32 v107, v95, v91, vcc
	v_cmp_gt_f32_e32 vcc, 0, v86
	v_fma_f32 v86, |v82|, s76, 1.0
	v_exp_f32_e32 v88, v87
	v_fma_f32 v87, |v83|, s76, 1.0
	v_rcp_f32_e32 v86, v86
	v_rcp_f32_e32 v87, v87
	v_cndmask_b32_e32 v106, v94, v90, vcc
	v_exp_f32_e32 v89, v89
	v_cmp_gt_f32_e32 vcc, 0, v85
	v_fma_f32 v90, v86, s22, v110
	v_fma_f32 v91, v87, s22, v110
	s_nop 0
	v_fma_f32 v90, v86, v90, s26
	v_fma_f32 v91, v87, v91, s26
	s_nop 0
	v_fma_f32 v90, v86, v90, s28
	v_fma_f32 v91, v87, v91, s28
	s_nop 0
	v_fma_f32 v90, v86, v90, s30
	v_fma_f32 v91, v87, v91, s30
	s_nop 0
	v_mul_f32 v86, v86, v90
	v_mul_f32 v87, v87, v91
	v_mul_f32_e32 v91, v85, v85
	v_mul_f32 v86, v88, v86
	v_mul_f32 v87, v89, v87
	v_mul_f32_e32 v89, v84, v84
	v_mul_f32_e32 v89, 0xbf38aa3b, v89
	v_fma_f32 v88, |v84|, s76, 1.0
	v_exp_f32_e32 v90, v89
	v_fma_f32 v89, |v85|, s76, 1.0
	v_rcp_f32_e32 v88, v88
	v_rcp_f32_e32 v89, v89
	v_mul_f32_e32 v91, 0xbf38aa3b, v91
	v_exp_f32_e32 v91, v91
	v_mul_f32 v86, v82, v86
	v_mul_f32 v87, v83, v87
	v_fma_f32 v92, v88, s22, v110
	v_fma_f32 v93, v89, s22, v110
	s_nop 0
	v_fma_f32 v92, v88, v92, s26
	v_fma_f32 v93, v89, v93, s26
	s_nop 0
	v_fma_f32 v92, v88, v92, s28
	v_fma_f32 v93, v89, v93, s28
	s_nop 0
	v_fma_f32 v92, v88, v92, s30
	v_fma_f32 v93, v89, v93, s30
	s_nop 0
	v_mul_f32 v88, v88, v92
	v_mul_f32 v89, v89, v93
	s_nop 0
	v_mul_f32 v88, v90, v88
	v_mul_f32 v89, v91, v89
	v_sub_f32_e32 v91, v83, v87
	v_mul_f32 v88, v84, v88
	v_mul_f32 v89, v85, v89
	v_sub_f32_e32 v90, v82, v86
	v_sub_f32_e32 v93, v85, v89
	v_sub_f32_e32 v92, v84, v88
	v_cndmask_b32_e32 v113, v93, v89, vcc
	v_cmp_gt_f32_e32 vcc, 0, v84
	s_nop 1
	v_cndmask_b32_e32 v112, v92, v88, vcc
	v_cmp_gt_f32_e32 vcc, 0, v83
	s_nop 1
	v_cndmask_b32_e32 v111, v91, v87, vcc
	v_cmp_gt_f32_e32 vcc, 0, v82
	s_nop 1
	v_cndmask_b32_e32 v110, v90, v86, vcc
.LBB0_779:
	v_or_b32_e32 v82, 32, v166
	v_mad_i64_i32 v[86:87], s[38:39], v82, s77, v[160:161]
	v_cvt_pk_bf16_f32 v82, v98, v99
	v_cvt_pk_bf16_f32 v83, v100, v101
	v_cvt_pk_bf16_f32 v84, v102, v103
	v_cvt_pk_bf16_f32 v85, v104, v105
	global_store_dwordx4 v[86:87], v[82:85], off
	s_nop 1
	v_cvt_pk_bf16_f32 v82, v106, v107
	v_cvt_pk_bf16_f32 v83, v108, v109
	v_cvt_pk_bf16_f32 v84, v110, v111
	v_cvt_pk_bf16_f32 v85, v112, v113
	s_and_b64 vcc, exec, s[4:5]
	s_mov_b64 s[38:39], -1
	global_store_dwordx4 v[86:87], v[82:85], off offset:256
	s_cbranch_vccnz .LBB0_783
	s_nop 0
	v_mov_b64_e32 v[84:85], v[80:81]
	v_mov_b64_e32 v[96:97], v[68:69]
	v_mov_b64_e32 v[92:93], v[72:73]
	v_mov_b64_e32 v[88:89], v[76:77]
	s_and_b64 vcc, exec, s[2:3]
	v_mov_b64_e32 v[82:83], v[78:79]
	v_mov_b64_e32 v[94:95], v[66:67]
	v_mov_b64_e32 v[90:91], v[70:71]
	v_mov_b64_e32 v[86:87], v[74:75]
	s_cbranch_vccnz .LBB0_782
	v_mul_f32 v84, v80, s20
	v_mul_f32 v85, v81, s20
	v_mul_f32 v82, v78, s20
	v_mul_f32 v83, v79, s20
	v_mul_f32 v88, v76, s20
	v_mul_f32 v89, v77, s20
	v_mul_f32 v86, v74, s20
	v_mul_f32 v87, v75, s20
	v_mul_f32 v92, v72, s20
	v_mul_f32 v93, v73, s20
	v_mul_f32 v90, v70, s20
	v_mul_f32 v91, v71, s20
	v_mul_f32 v96, v68, s20
	v_mul_f32 v97, v69, s20
	v_mul_f32 v94, v66, s20
	v_mul_f32 v95, v67, s20

.LBB0_783:
	s_andn2_b64 vcc, exec, s[38:39]
	s_cbranch_vccnz .LBB0_785
	v_mul_f32_e32 v83, v78, v78
	v_mul_f32_e32 v83, 0xbf38aa3b, v83
	v_fma_f32 v82, |v78|, s76, 1.0
	v_exp_f32_e32 v84, v83
	v_fma_f32 v83, |v79|, s76, 1.0
	v_rcp_f32_e32 v82, v82
	v_rcp_f32_e32 v83, v83
	v_mul_f32_e32 v85, v79, v79
	v_mov_b64_e32 v[94:95], s[24:25]
	v_mul_f32_e32 v85, 0xbf38aa3b, v85
	v_fma_f32 v86, v82, s22, v94
	v_fma_f32 v87, v83, s22, v94
	v_exp_f32_e32 v85, v85
	v_fma_f32 v86, v82, v86, s26
	v_fma_f32 v87, v83, v87, s26
	v_cmp_gt_f32_e32 vcc, 0, v81
	v_fma_f32 v86, v82, v86, s28
	v_fma_f32 v87, v83, v87, s28
	s_nop 0
	v_fma_f32 v86, v82, v86, s30
	v_fma_f32 v87, v83, v87, s30
	s_nop 0
	v_mul_f32 v82, v82, v86
	v_mul_f32 v83, v83, v87
	v_mul_f32_e32 v87, v81, v81
	v_mul_f32 v82, v84, v82
	v_mul_f32 v83, v85, v83
	v_mul_f32_e32 v85, v80, v80
	v_mul_f32_e32 v85, 0xbf38aa3b, v85
	v_fma_f32 v84, |v80|, s76, 1.0
	v_exp_f32_e32 v86, v85
	v_fma_f32 v85, |v81|, s76, 1.0
	v_rcp_f32_e32 v84, v84
	v_rcp_f32_e32 v85, v85
	v_mul_f32_e32 v87, 0xbf38aa3b, v87
	v_exp_f32_e32 v87, v87
	v_mul_f32 v82, v78, v82
	v_mul_f32 v83, v79, v83
	v_fma_f32 v88, v84, s22, v94
	v_fma_f32 v89, v85, s22, v94
	s_nop 0
	v_fma_f32 v88, v84, v88, s26
	v_fma_f32 v89, v85, v89, s26
	s_nop 0
	v_fma_f32 v88, v84, v88, s28
	v_fma_f32 v89, v85, v89, s28
	s_nop 0
	v_fma_f32 v88, v84, v88, s30
	v_fma_f32 v89, v85, v89, s30
	s_nop 0
	v_mul_f32 v84, v84, v88
	v_mul_f32 v85, v85, v89
	s_nop 0
	v_mul_f32 v84, v86, v84
	v_mul_f32 v85, v87, v85
	v_sub_f32_e32 v87, v79, v83
	v_mul_f32 v84, v80, v84
	v_mul_f32 v85, v81, v85
	v_sub_f32_e32 v86, v78, v82
	v_sub_f32_e32 v89, v81, v85
	v_sub_f32_e32 v88, v80, v84
	v_cndmask_b32_e32 v85, v89, v85, vcc
	v_cmp_gt_f32_e32 vcc, 0, v80
	v_mul_f32_e32 v81, v75, v75
	v_mul_f32_e32 v81, 0xbf38aa3b, v81
	v_cndmask_b32_e32 v84, v88, v84, vcc
	v_cmp_gt_f32_e32 vcc, 0, v79
	v_mul_f32_e32 v79, v74, v74
	v_mul_f32_e32 v79, 0xbf38aa3b, v79
	v_cndmask_b32_e32 v83, v87, v83, vcc
	v_cmp_gt_f32_e32 vcc, 0, v78
	v_fma_f32 v78, |v74|, s76, 1.0
	v_exp_f32_e32 v80, v79
	v_fma_f32 v79, |v75|, s76, 1.0
	v_rcp_f32_e32 v78, v78
	v_rcp_f32_e32 v79, v79
	v_cndmask_b32_e32 v82, v86, v82, vcc
	v_exp_f32_e32 v81, v81
	v_cmp_gt_f32_e32 vcc, 0, v77
	v_fma_f32 v86, v78, s22, v94
	v_fma_f32 v87, v79, s22, v94
	s_nop 0
	v_fma_f32 v86, v78, v86, s26
	v_fma_f32 v87, v79, v87, s26
	s_nop 0
	v_fma_f32 v86, v78, v86, s28
	v_fma_f32 v87, v79, v87, s28
	s_nop 0
	v_fma_f32 v86, v78, v86, s30
	v_fma_f32 v87, v79, v87, s30
	s_nop 0
	v_mul_f32 v78, v78, v86
	v_mul_f32 v79, v79, v87
	v_mul_f32_e32 v87, v77, v77
	v_mul_f32 v78, v80, v78
	v_mul_f32 v79, v81, v79
	v_mul_f32_e32 v81, v76, v76
	v_mul_f32_e32 v81, 0xbf38aa3b, v81
	v_fma_f32 v80, |v76|, s76, 1.0
	v_exp_f32_e32 v86, v81
	v_fma_f32 v81, |v77|, s76, 1.0
	v_rcp_f32_e32 v80, v80
	v_rcp_f32_e32 v81, v81
	v_mul_f32_e32 v87, 0xbf38aa3b, v87
	v_exp_f32_e32 v87, v87
	v_mul_f32 v78, v74, v78
	v_mul_f32 v79, v75, v79
	v_fma_f32 v88, v80, s22, v94
	v_fma_f32 v89, v81, s22, v94
	s_nop 0
	v_fma_f32 v88, v80, v88, s26
	v_fma_f32 v89, v81, v89, s26
	s_nop 0
	v_fma_f32 v88, v80, v88, s28
	v_fma_f32 v89, v81, v89, s28
	s_nop 0
	v_fma_f32 v88, v80, v88, s30
	v_fma_f32 v89, v81, v89, s30
	s_nop 0
	v_mul_f32 v80, v80, v88
	v_mul_f32 v81, v81, v89
	s_nop 0
	v_mul_f32 v80, v86, v80
	v_mul_f32 v81, v87, v81
	v_sub_f32_e32 v87, v75, v79
	v_mul_f32 v80, v76, v80
	v_mul_f32 v81, v77, v81
	v_sub_f32_e32 v86, v74, v78
	v_sub_f32_e32 v89, v77, v81
	v_sub_f32_e32 v88, v76, v80
	v_cndmask_b32_e32 v89, v89, v81, vcc
	v_cmp_gt_f32_e32 vcc, 0, v76
	v_mul_f32_e32 v77, v71, v71
	v_mul_f32_e32 v77, 0xbf38aa3b, v77
	v_cndmask_b32_e32 v88, v88, v80, vcc
	v_cmp_gt_f32_e32 vcc, 0, v75
	v_mul_f32_e32 v75, v70, v70
	v_mul_f32_e32 v75, 0xbf38aa3b, v75
	v_cndmask_b32_e32 v87, v87, v79, vcc
	v_cmp_gt_f32_e32 vcc, 0, v74
	v_fma_f32 v74, |v70|, s76, 1.0
	v_exp_f32_e32 v76, v75
	v_fma_f32 v75, |v71|, s76, 1.0
	v_rcp_f32_e32 v74, v74
	v_rcp_f32_e32 v75, v75
	v_cndmask_b32_e32 v86, v86, v78, vcc
	v_exp_f32_e32 v77, v77
	v_cmp_gt_f32_e32 vcc, 0, v73
	v_fma_f32 v78, v74, s22, v94
	v_fma_f32 v79, v75, s22, v94
	s_nop 0
	v_fma_f32 v78, v74, v78, s26
	v_fma_f32 v79, v75, v79, s26
	s_nop 0
	v_fma_f32 v78, v74, v78, s28
	v_fma_f32 v79, v75, v79, s28
	s_nop 0
	v_fma_f32 v78, v74, v78, s30
	v_fma_f32 v79, v75, v79, s30
	s_nop 0
	v_mul_f32 v74, v74, v78
	v_mul_f32 v75, v75, v79
	v_mul_f32_e32 v79, v73, v73
	v_mul_f32 v74, v76, v74
	v_mul_f32 v75, v77, v75
	v_mul_f32_e32 v77, v72, v72
	v_mul_f32_e32 v77, 0xbf38aa3b, v77
	v_fma_f32 v76, |v72|, s76, 1.0
	v_exp_f32_e32 v78, v77
	v_fma_f32 v77, |v73|, s76, 1.0
	v_rcp_f32_e32 v76, v76
	v_rcp_f32_e32 v77, v77
	v_mul_f32_e32 v79, 0xbf38aa3b, v79
	v_exp_f32_e32 v79, v79
	v_mul_f32 v74, v70, v74
	v_mul_f32 v75, v71, v75
	v_fma_f32 v80, v76, s22, v94
	v_fma_f32 v81, v77, s22, v94
	s_nop 0
	v_fma_f32 v80, v76, v80, s26
	v_fma_f32 v81, v77, v81, s26
	s_nop 0
	v_fma_f32 v80, v76, v80, s28
	v_fma_f32 v81, v77, v81, s28
	s_nop 0
	v_fma_f32 v80, v76, v80, s30
	v_fma_f32 v81, v77, v81, s30
	s_nop 0
	v_mul_f32 v76, v76, v80
	v_mul_f32 v77, v77, v81
	s_nop 0
	v_mul_f32 v76, v78, v76
	v_mul_f32 v77, v79, v77
	v_sub_f32_e32 v79, v71, v75
	v_mul_f32 v76, v72, v76
	v_mul_f32 v77, v73, v77
	v_sub_f32_e32 v78, v70, v74
	v_sub_f32_e32 v81, v73, v77
	v_sub_f32_e32 v80, v72, v76
	v_cndmask_b32_e32 v93, v81, v77, vcc
	v_cmp_gt_f32_e32 vcc, 0, v72
	v_mul_f32_e32 v73, v67, v67
	v_mul_f32_e32 v73, 0xbf38aa3b, v73
	v_cndmask_b32_e32 v92, v80, v76, vcc
	v_cmp_gt_f32_e32 vcc, 0, v71
	v_mul_f32_e32 v71, v66, v66
	v_mul_f32_e32 v71, 0xbf38aa3b, v71
	v_cndmask_b32_e32 v91, v79, v75, vcc
	v_cmp_gt_f32_e32 vcc, 0, v70
	v_fma_f32 v70, |v66|, s76, 1.0
	v_exp_f32_e32 v72, v71
	v_fma_f32 v71, |v67|, s76, 1.0
	v_rcp_f32_e32 v70, v70
	v_rcp_f32_e32 v71, v71
	v_cndmask_b32_e32 v90, v78, v74, vcc
	v_exp_f32_e32 v73, v73
	v_cmp_gt_f32_e32 vcc, 0, v69
	v_fma_f32 v74, v70, s22, v94
	v_fma_f32 v75, v71, s22, v94
	s_nop 0
	v_fma_f32 v74, v70, v74, s26
	v_fma_f32 v75, v71, v75, s26
	s_nop 0
	v_fma_f32 v74, v70, v74, s28
	v_fma_f32 v75, v71, v75, s28
	s_nop 0
	v_fma_f32 v74, v70, v74, s30
	v_fma_f32 v75, v71, v75, s30
	s_nop 0
	v_mul_f32 v70, v70, v74
	v_mul_f32 v71, v71, v75
	v_mul_f32_e32 v75, v69, v69
	v_mul_f32 v70, v72, v70
	v_mul_f32 v71, v73, v71
	v_mul_f32_e32 v73, v68, v68
	v_mul_f32_e32 v73, 0xbf38aa3b, v73
	v_fma_f32 v72, |v68|, s76, 1.0
	v_exp_f32_e32 v74, v73
	v_fma_f32 v73, |v69|, s76, 1.0
	v_rcp_f32_e32 v72, v72
	v_rcp_f32_e32 v73, v73
	v_mul_f32_e32 v75, 0xbf38aa3b, v75
	v_exp_f32_e32 v75, v75
	v_mul_f32 v70, v66, v70
	v_mul_f32 v71, v67, v71
	v_fma_f32 v76, v72, s22, v94
	v_fma_f32 v77, v73, s22, v94
	s_nop 0
	v_fma_f32 v76, v72, v76, s26
	v_fma_f32 v77, v73, v77, s26
	s_nop 0
	v_fma_f32 v76, v72, v76, s28
	v_fma_f32 v77, v73, v77, s28
	s_nop 0
	v_fma_f32 v76, v72, v76, s30
	v_fma_f32 v77, v73, v77, s30
	s_nop 0
	v_mul_f32 v72, v72, v76
	v_mul_f32 v73, v73, v77
	s_nop 0
	v_mul_f32 v72, v74, v72
	v_mul_f32 v73, v75, v73
	v_sub_f32_e32 v75, v67, v71
	v_mul_f32 v72, v68, v72
	v_mul_f32 v73, v69, v73
	v_sub_f32_e32 v74, v66, v70
	v_sub_f32_e32 v77, v69, v73
	v_sub_f32_e32 v76, v68, v72
	v_cndmask_b32_e32 v97, v77, v73, vcc
	v_cmp_gt_f32_e32 vcc, 0, v68
	s_nop 1
	v_cndmask_b32_e32 v96, v76, v72, vcc
	v_cmp_gt_f32_e32 vcc, 0, v67
	s_nop 1
	v_cndmask_b32_e32 v95, v75, v71, vcc
	v_cmp_gt_f32_e32 vcc, 0, v66
	s_nop 1
	v_cndmask_b32_e32 v94, v74, v70, vcc
.LBB0_785:
	v_or_b32_e32 v66, 48, v166
	v_mad_i64_i32 v[70:71], s[38:39], v66, s77, v[160:161]
	v_cvt_pk_bf16_f32 v66, v82, v83
	v_cvt_pk_bf16_f32 v67, v84, v85
	v_cvt_pk_bf16_f32 v68, v86, v87
	v_cvt_pk_bf16_f32 v69, v88, v89
	global_store_dwordx4 v[70:71], v[66:69], off
	s_nop 1
	v_cvt_pk_bf16_f32 v66, v90, v91
	v_cvt_pk_bf16_f32 v67, v92, v93
	v_cvt_pk_bf16_f32 v68, v94, v95
	v_cvt_pk_bf16_f32 v69, v96, v97
	s_and_b64 vcc, exec, s[4:5]
	s_mov_b64 s[38:39], -1
	global_store_dwordx4 v[70:71], v[66:69], off offset:256
	s_cbranch_vccnz .LBB0_789
	s_nop 0
	v_mov_b64_e32 v[68:69], v[64:65]
	v_mov_b64_e32 v[80:81], v[52:53]
	v_mov_b64_e32 v[76:77], v[56:57]
	v_mov_b64_e32 v[72:73], v[60:61]
	s_and_b64 vcc, exec, s[2:3]
	v_mov_b64_e32 v[66:67], v[62:63]
	v_mov_b64_e32 v[78:79], v[50:51]
	v_mov_b64_e32 v[74:75], v[54:55]
	v_mov_b64_e32 v[70:71], v[58:59]
	s_cbranch_vccnz .LBB0_788
	v_mul_f32 v68, v64, s20
	v_mul_f32 v69, v65, s20
	v_mul_f32 v66, v62, s20
	v_mul_f32 v67, v63, s20
	v_mul_f32 v72, v60, s20
	v_mul_f32 v73, v61, s20
	v_mul_f32 v70, v58, s20
	v_mul_f32 v71, v59, s20
	v_mul_f32 v76, v56, s20
	v_mul_f32 v77, v57, s20
	v_mul_f32 v74, v54, s20
	v_mul_f32 v75, v55, s20
	v_mul_f32 v80, v52, s20
	v_mul_f32 v81, v53, s20
	v_mul_f32 v78, v50, s20
	v_mul_f32 v79, v51, s20

.LBB0_789:
	s_andn2_b64 vcc, exec, s[38:39]
	s_cbranch_vccnz .LBB0_791
	v_mul_f32_e32 v67, v62, v62
	v_mul_f32_e32 v67, 0xbf38aa3b, v67
	v_fma_f32 v66, |v62|, s76, 1.0
	v_exp_f32_e32 v68, v67
	v_fma_f32 v67, |v63|, s76, 1.0
	v_rcp_f32_e32 v66, v66
	v_rcp_f32_e32 v67, v67
	v_mul_f32_e32 v69, v63, v63
	v_mov_b64_e32 v[78:79], s[24:25]
	v_mul_f32_e32 v69, 0xbf38aa3b, v69
	v_fma_f32 v70, v66, s22, v78
	v_fma_f32 v71, v67, s22, v78
	v_exp_f32_e32 v69, v69
	v_fma_f32 v70, v66, v70, s26
	v_fma_f32 v71, v67, v71, s26
	v_cmp_gt_f32_e32 vcc, 0, v65
	v_fma_f32 v70, v66, v70, s28
	v_fma_f32 v71, v67, v71, s28
	s_nop 0
	v_fma_f32 v70, v66, v70, s30
	v_fma_f32 v71, v67, v71, s30
	s_nop 0
	v_mul_f32 v66, v66, v70
	v_mul_f32 v67, v67, v71
	v_mul_f32_e32 v71, v65, v65
	v_mul_f32 v66, v68, v66
	v_mul_f32 v67, v69, v67
	v_mul_f32_e32 v69, v64, v64
	v_mul_f32_e32 v69, 0xbf38aa3b, v69
	v_fma_f32 v68, |v64|, s76, 1.0
	v_exp_f32_e32 v70, v69
	v_fma_f32 v69, |v65|, s76, 1.0
	v_rcp_f32_e32 v68, v68
	v_rcp_f32_e32 v69, v69
	v_mul_f32_e32 v71, 0xbf38aa3b, v71
	v_exp_f32_e32 v71, v71
	v_mul_f32 v66, v62, v66
	v_mul_f32 v67, v63, v67
	v_fma_f32 v72, v68, s22, v78
	v_fma_f32 v73, v69, s22, v78
	s_nop 0
	v_fma_f32 v72, v68, v72, s26
	v_fma_f32 v73, v69, v73, s26
	s_nop 0
	v_fma_f32 v72, v68, v72, s28
	v_fma_f32 v73, v69, v73, s28
	s_nop 0
	v_fma_f32 v72, v68, v72, s30
	v_fma_f32 v73, v69, v73, s30
	s_nop 0
	v_mul_f32 v68, v68, v72
	v_mul_f32 v69, v69, v73
	s_nop 0
	v_mul_f32 v68, v70, v68
	v_mul_f32 v69, v71, v69
	v_sub_f32_e32 v71, v63, v67
	v_mul_f32 v68, v64, v68
	v_mul_f32 v69, v65, v69
	v_sub_f32_e32 v70, v62, v66
	v_sub_f32_e32 v73, v65, v69
	v_sub_f32_e32 v72, v64, v68
	v_cndmask_b32_e32 v69, v73, v69, vcc
	v_cmp_gt_f32_e32 vcc, 0, v64
	v_mul_f32_e32 v65, v59, v59
	v_mul_f32_e32 v65, 0xbf38aa3b, v65
	v_cndmask_b32_e32 v68, v72, v68, vcc
	v_cmp_gt_f32_e32 vcc, 0, v63
	v_mul_f32_e32 v63, v58, v58
	v_mul_f32_e32 v63, 0xbf38aa3b, v63
	v_cndmask_b32_e32 v67, v71, v67, vcc
	v_cmp_gt_f32_e32 vcc, 0, v62
	v_fma_f32 v62, |v58|, s76, 1.0
	v_exp_f32_e32 v64, v63
	v_fma_f32 v63, |v59|, s76, 1.0
	v_rcp_f32_e32 v62, v62
	v_rcp_f32_e32 v63, v63
	v_cndmask_b32_e32 v66, v70, v66, vcc
	v_exp_f32_e32 v65, v65
	v_cmp_gt_f32_e32 vcc, 0, v61
	v_fma_f32 v70, v62, s22, v78
	v_fma_f32 v71, v63, s22, v78
	s_nop 0
	v_fma_f32 v70, v62, v70, s26
	v_fma_f32 v71, v63, v71, s26
	s_nop 0
	v_fma_f32 v70, v62, v70, s28
	v_fma_f32 v71, v63, v71, s28
	s_nop 0
	v_fma_f32 v70, v62, v70, s30
	v_fma_f32 v71, v63, v71, s30
	s_nop 0
	v_mul_f32 v62, v62, v70
	v_mul_f32 v63, v63, v71
	v_mul_f32_e32 v71, v61, v61
	v_mul_f32 v62, v64, v62
	v_mul_f32 v63, v65, v63
	v_mul_f32_e32 v65, v60, v60
	v_mul_f32_e32 v65, 0xbf38aa3b, v65
	v_fma_f32 v64, |v60|, s76, 1.0
	v_exp_f32_e32 v70, v65
	v_fma_f32 v65, |v61|, s76, 1.0
	v_rcp_f32_e32 v64, v64
	v_rcp_f32_e32 v65, v65
	v_mul_f32_e32 v71, 0xbf38aa3b, v71
	v_exp_f32_e32 v71, v71
	v_mul_f32 v62, v58, v62
	v_mul_f32 v63, v59, v63
	v_fma_f32 v72, v64, s22, v78
	v_fma_f32 v73, v65, s22, v78
	s_nop 0
	v_fma_f32 v72, v64, v72, s26
	v_fma_f32 v73, v65, v73, s26
	s_nop 0
	v_fma_f32 v72, v64, v72, s28
	v_fma_f32 v73, v65, v73, s28
	s_nop 0
	v_fma_f32 v72, v64, v72, s30
	v_fma_f32 v73, v65, v73, s30
	s_nop 0
	v_mul_f32 v64, v64, v72
	v_mul_f32 v65, v65, v73
	s_nop 0
	v_mul_f32 v64, v70, v64
	v_mul_f32 v65, v71, v65
	v_sub_f32_e32 v71, v59, v63
	v_mul_f32 v64, v60, v64
	v_mul_f32 v65, v61, v65
	v_sub_f32_e32 v70, v58, v62
	v_sub_f32_e32 v73, v61, v65
	v_sub_f32_e32 v72, v60, v64
	v_cndmask_b32_e32 v73, v73, v65, vcc
	v_cmp_gt_f32_e32 vcc, 0, v60
	v_mul_f32_e32 v61, v55, v55
	v_mul_f32_e32 v61, 0xbf38aa3b, v61
	v_cndmask_b32_e32 v72, v72, v64, vcc
	v_cmp_gt_f32_e32 vcc, 0, v59
	v_mul_f32_e32 v59, v54, v54
	v_mul_f32_e32 v59, 0xbf38aa3b, v59
	v_cndmask_b32_e32 v71, v71, v63, vcc
	v_cmp_gt_f32_e32 vcc, 0, v58
	v_fma_f32 v58, |v54|, s76, 1.0
	v_exp_f32_e32 v60, v59
	v_fma_f32 v59, |v55|, s76, 1.0
	v_rcp_f32_e32 v58, v58
	v_rcp_f32_e32 v59, v59
	v_cndmask_b32_e32 v70, v70, v62, vcc
	v_exp_f32_e32 v61, v61
	v_cmp_gt_f32_e32 vcc, 0, v57
	v_fma_f32 v62, v58, s22, v78
	v_fma_f32 v63, v59, s22, v78
	s_nop 0
	v_fma_f32 v62, v58, v62, s26
	v_fma_f32 v63, v59, v63, s26
	s_nop 0
	v_fma_f32 v62, v58, v62, s28
	v_fma_f32 v63, v59, v63, s28
	s_nop 0
	v_fma_f32 v62, v58, v62, s30
	v_fma_f32 v63, v59, v63, s30
	s_nop 0
	v_mul_f32 v58, v58, v62
	v_mul_f32 v59, v59, v63
	v_mul_f32_e32 v63, v57, v57
	v_mul_f32 v58, v60, v58
	v_mul_f32 v59, v61, v59
	v_mul_f32_e32 v61, v56, v56
	v_mul_f32_e32 v61, 0xbf38aa3b, v61
	v_fma_f32 v60, |v56|, s76, 1.0
	v_exp_f32_e32 v62, v61
	v_fma_f32 v61, |v57|, s76, 1.0
	v_rcp_f32_e32 v60, v60
	v_rcp_f32_e32 v61, v61
	v_mul_f32_e32 v63, 0xbf38aa3b, v63
	v_exp_f32_e32 v63, v63
	v_mul_f32 v58, v54, v58
	v_mul_f32 v59, v55, v59
	v_fma_f32 v64, v60, s22, v78
	v_fma_f32 v65, v61, s22, v78
	s_nop 0
	v_fma_f32 v64, v60, v64, s26
	v_fma_f32 v65, v61, v65, s26
	s_nop 0
	v_fma_f32 v64, v60, v64, s28
	v_fma_f32 v65, v61, v65, s28
	s_nop 0
	v_fma_f32 v64, v60, v64, s30
	v_fma_f32 v65, v61, v65, s30
	s_nop 0
	v_mul_f32 v60, v60, v64
	v_mul_f32 v61, v61, v65
	s_nop 0
	v_mul_f32 v60, v62, v60
	v_mul_f32 v61, v63, v61
	v_sub_f32_e32 v63, v55, v59
	v_mul_f32 v60, v56, v60
	v_mul_f32 v61, v57, v61
	v_sub_f32_e32 v62, v54, v58
	v_sub_f32_e32 v65, v57, v61
	v_sub_f32_e32 v64, v56, v60
	v_cndmask_b32_e32 v77, v65, v61, vcc
	v_cmp_gt_f32_e32 vcc, 0, v56
	v_mul_f32_e32 v57, v51, v51
	v_mul_f32_e32 v57, 0xbf38aa3b, v57
	v_cndmask_b32_e32 v76, v64, v60, vcc
	v_cmp_gt_f32_e32 vcc, 0, v55
	v_mul_f32_e32 v55, v50, v50
	v_mul_f32_e32 v55, 0xbf38aa3b, v55
	v_cndmask_b32_e32 v75, v63, v59, vcc
	v_cmp_gt_f32_e32 vcc, 0, v54
	v_fma_f32 v54, |v50|, s76, 1.0
	v_exp_f32_e32 v56, v55
	v_fma_f32 v55, |v51|, s76, 1.0
	v_rcp_f32_e32 v54, v54
	v_rcp_f32_e32 v55, v55
	v_cndmask_b32_e32 v74, v62, v58, vcc
	v_exp_f32_e32 v57, v57
	v_cmp_gt_f32_e32 vcc, 0, v53
	v_fma_f32 v58, v54, s22, v78
	v_fma_f32 v59, v55, s22, v78
	s_nop 0
	v_fma_f32 v58, v54, v58, s26
	v_fma_f32 v59, v55, v59, s26
	s_nop 0
	v_fma_f32 v58, v54, v58, s28
	v_fma_f32 v59, v55, v59, s28
	s_nop 0
	v_fma_f32 v58, v54, v58, s30
	v_fma_f32 v59, v55, v59, s30
	s_nop 0
	v_mul_f32 v54, v54, v58
	v_mul_f32 v55, v55, v59
	v_mul_f32_e32 v59, v53, v53
	v_mul_f32 v54, v56, v54
	v_mul_f32 v55, v57, v55
	v_mul_f32_e32 v57, v52, v52
	v_mul_f32_e32 v57, 0xbf38aa3b, v57
	v_fma_f32 v56, |v52|, s76, 1.0
	v_exp_f32_e32 v58, v57
	v_fma_f32 v57, |v53|, s76, 1.0
	v_rcp_f32_e32 v56, v56
	v_rcp_f32_e32 v57, v57
	v_mul_f32_e32 v59, 0xbf38aa3b, v59
	v_exp_f32_e32 v59, v59
	v_mul_f32 v54, v50, v54
	v_mul_f32 v55, v51, v55
	v_fma_f32 v60, v56, s22, v78
	v_fma_f32 v61, v57, s22, v78
	s_nop 0
	v_fma_f32 v60, v56, v60, s26
	v_fma_f32 v61, v57, v61, s26
	s_nop 0
	v_fma_f32 v60, v56, v60, s28
	v_fma_f32 v61, v57, v61, s28
	s_nop 0
	v_fma_f32 v60, v56, v60, s30
	v_fma_f32 v61, v57, v61, s30
	s_nop 0
	v_mul_f32 v56, v56, v60
	v_mul_f32 v57, v57, v61
	s_nop 0
	v_mul_f32 v56, v58, v56
	v_mul_f32 v57, v59, v57
	v_sub_f32_e32 v59, v51, v55
	v_mul_f32 v56, v52, v56
	v_mul_f32 v57, v53, v57
	v_sub_f32_e32 v58, v50, v54
	v_sub_f32_e32 v61, v53, v57
	v_sub_f32_e32 v60, v52, v56
	v_cndmask_b32_e32 v81, v61, v57, vcc
	v_cmp_gt_f32_e32 vcc, 0, v52
	s_nop 1
	v_cndmask_b32_e32 v80, v60, v56, vcc
	v_cmp_gt_f32_e32 vcc, 0, v51
	s_nop 1
	v_cndmask_b32_e32 v79, v59, v55, vcc
	v_cmp_gt_f32_e32 vcc, 0, v50
	s_nop 1
	v_cndmask_b32_e32 v78, v58, v54, vcc
.LBB0_791:
	v_add_u32_e32 v50, 0x80, v166
	v_mad_i64_i32 v[54:55], s[38:39], v50, s77, v[160:161]
	v_cvt_pk_bf16_f32 v50, v66, v67
	v_cvt_pk_bf16_f32 v51, v68, v69
	v_cvt_pk_bf16_f32 v52, v70, v71
	v_cvt_pk_bf16_f32 v53, v72, v73
	global_store_dwordx4 v[54:55], v[50:53], off
	s_nop 1
	v_cvt_pk_bf16_f32 v50, v74, v75
	v_cvt_pk_bf16_f32 v51, v76, v77
	v_cvt_pk_bf16_f32 v52, v78, v79
	v_cvt_pk_bf16_f32 v53, v80, v81
	s_and_b64 vcc, exec, s[4:5]
	s_mov_b64 s[38:39], -1
	global_store_dwordx4 v[54:55], v[50:53], off offset:256
	s_cbranch_vccnz .LBB0_795
	s_nop 0
	v_mov_b64_e32 v[52:53], v[48:49]
	v_mov_b64_e32 v[64:65], v[36:37]
	v_mov_b64_e32 v[60:61], v[40:41]
	v_mov_b64_e32 v[56:57], v[44:45]
	s_and_b64 vcc, exec, s[2:3]
	v_mov_b64_e32 v[50:51], v[46:47]
	v_mov_b64_e32 v[62:63], v[34:35]
	v_mov_b64_e32 v[58:59], v[38:39]
	v_mov_b64_e32 v[54:55], v[42:43]
	s_cbranch_vccnz .LBB0_794
	v_mul_f32 v52, v48, s20
	v_mul_f32 v53, v49, s20
	v_mul_f32 v50, v46, s20
	v_mul_f32 v51, v47, s20
	v_mul_f32 v56, v44, s20
	v_mul_f32 v57, v45, s20
	v_mul_f32 v54, v42, s20
	v_mul_f32 v55, v43, s20
	v_mul_f32 v60, v40, s20
	v_mul_f32 v61, v41, s20
	v_mul_f32 v58, v38, s20
	v_mul_f32 v59, v39, s20
	v_mul_f32 v64, v36, s20
	v_mul_f32 v65, v37, s20
	v_mul_f32 v62, v34, s20
	v_mul_f32 v63, v35, s20

.LBB0_795:
	s_andn2_b64 vcc, exec, s[38:39]
	s_cbranch_vccnz .LBB0_797
	v_mul_f32_e32 v51, v46, v46
	v_mul_f32_e32 v51, 0xbf38aa3b, v51
	v_fma_f32 v50, |v46|, s76, 1.0
	v_exp_f32_e32 v52, v51
	v_fma_f32 v51, |v47|, s76, 1.0
	v_rcp_f32_e32 v50, v50
	v_rcp_f32_e32 v51, v51
	v_mul_f32_e32 v53, v47, v47
	v_mov_b64_e32 v[62:63], s[24:25]
	v_mul_f32_e32 v53, 0xbf38aa3b, v53
	v_fma_f32 v54, v50, s22, v62
	v_fma_f32 v55, v51, s22, v62
	v_exp_f32_e32 v53, v53
	v_fma_f32 v54, v50, v54, s26
	v_fma_f32 v55, v51, v55, s26
	v_cmp_gt_f32_e32 vcc, 0, v49
	v_fma_f32 v54, v50, v54, s28
	v_fma_f32 v55, v51, v55, s28
	s_nop 0
	v_fma_f32 v54, v50, v54, s30
	v_fma_f32 v55, v51, v55, s30
	s_nop 0
	v_mul_f32 v50, v50, v54
	v_mul_f32 v51, v51, v55
	v_mul_f32_e32 v55, v49, v49
	v_mul_f32 v50, v52, v50
	v_mul_f32 v51, v53, v51
	v_mul_f32_e32 v53, v48, v48
	v_mul_f32_e32 v53, 0xbf38aa3b, v53
	v_fma_f32 v52, |v48|, s76, 1.0
	v_exp_f32_e32 v54, v53
	v_fma_f32 v53, |v49|, s76, 1.0
	v_rcp_f32_e32 v52, v52
	v_rcp_f32_e32 v53, v53
	v_mul_f32_e32 v55, 0xbf38aa3b, v55
	v_exp_f32_e32 v55, v55
	v_mul_f32 v50, v46, v50
	v_mul_f32 v51, v47, v51
	v_fma_f32 v56, v52, s22, v62
	v_fma_f32 v57, v53, s22, v62
	s_nop 0
	v_fma_f32 v56, v52, v56, s26
	v_fma_f32 v57, v53, v57, s26
	s_nop 0
	v_fma_f32 v56, v52, v56, s28
	v_fma_f32 v57, v53, v57, s28
	s_nop 0
	v_fma_f32 v56, v52, v56, s30
	v_fma_f32 v57, v53, v57, s30
	s_nop 0
	v_mul_f32 v52, v52, v56
	v_mul_f32 v53, v53, v57
	s_nop 0
	v_mul_f32 v52, v54, v52
	v_mul_f32 v53, v55, v53
	v_sub_f32_e32 v55, v47, v51
	v_mul_f32 v52, v48, v52
	v_mul_f32 v53, v49, v53
	v_sub_f32_e32 v54, v46, v50
	v_sub_f32_e32 v57, v49, v53
	v_sub_f32_e32 v56, v48, v52
	v_cndmask_b32_e32 v53, v57, v53, vcc
	v_cmp_gt_f32_e32 vcc, 0, v48
	v_mul_f32_e32 v49, v43, v43
	v_mul_f32_e32 v49, 0xbf38aa3b, v49
	v_cndmask_b32_e32 v52, v56, v52, vcc
	v_cmp_gt_f32_e32 vcc, 0, v47
	v_mul_f32_e32 v47, v42, v42
	v_mul_f32_e32 v47, 0xbf38aa3b, v47
	v_cndmask_b32_e32 v51, v55, v51, vcc
	v_cmp_gt_f32_e32 vcc, 0, v46
	v_fma_f32 v46, |v42|, s76, 1.0
	v_exp_f32_e32 v48, v47
	v_fma_f32 v47, |v43|, s76, 1.0
	v_rcp_f32_e32 v46, v46
	v_rcp_f32_e32 v47, v47
	v_cndmask_b32_e32 v50, v54, v50, vcc
	v_exp_f32_e32 v49, v49
	v_cmp_gt_f32_e32 vcc, 0, v45
	v_fma_f32 v54, v46, s22, v62
	v_fma_f32 v55, v47, s22, v62
	s_nop 0
	v_fma_f32 v54, v46, v54, s26
	v_fma_f32 v55, v47, v55, s26
	s_nop 0
	v_fma_f32 v54, v46, v54, s28
	v_fma_f32 v55, v47, v55, s28
	s_nop 0
	v_fma_f32 v54, v46, v54, s30
	v_fma_f32 v55, v47, v55, s30
	s_nop 0
	v_mul_f32 v46, v46, v54
	v_mul_f32 v47, v47, v55
	v_mul_f32_e32 v55, v45, v45
	v_mul_f32 v46, v48, v46
	v_mul_f32 v47, v49, v47
	v_mul_f32_e32 v49, v44, v44
	v_mul_f32_e32 v49, 0xbf38aa3b, v49
	v_fma_f32 v48, |v44|, s76, 1.0
	v_exp_f32_e32 v54, v49
	v_fma_f32 v49, |v45|, s76, 1.0
	v_rcp_f32_e32 v48, v48
	v_rcp_f32_e32 v49, v49
	v_mul_f32_e32 v55, 0xbf38aa3b, v55
	v_exp_f32_e32 v55, v55
	v_mul_f32 v46, v42, v46
	v_mul_f32 v47, v43, v47
	v_fma_f32 v56, v48, s22, v62
	v_fma_f32 v57, v49, s22, v62
	s_nop 0
	v_fma_f32 v56, v48, v56, s26
	v_fma_f32 v57, v49, v57, s26
	s_nop 0
	v_fma_f32 v56, v48, v56, s28
	v_fma_f32 v57, v49, v57, s28
	s_nop 0
	v_fma_f32 v56, v48, v56, s30
	v_fma_f32 v57, v49, v57, s30
	s_nop 0
	v_mul_f32 v48, v48, v56
	v_mul_f32 v49, v49, v57
	s_nop 0
	v_mul_f32 v48, v54, v48
	v_mul_f32 v49, v55, v49
	v_sub_f32_e32 v55, v43, v47
	v_mul_f32 v48, v44, v48
	v_mul_f32 v49, v45, v49
	v_sub_f32_e32 v54, v42, v46
	v_sub_f32_e32 v57, v45, v49
	v_sub_f32_e32 v56, v44, v48
	v_cndmask_b32_e32 v57, v57, v49, vcc
	v_cmp_gt_f32_e32 vcc, 0, v44
	v_mul_f32_e32 v45, v39, v39
	v_mul_f32_e32 v45, 0xbf38aa3b, v45
	v_cndmask_b32_e32 v56, v56, v48, vcc
	v_cmp_gt_f32_e32 vcc, 0, v43
	v_mul_f32_e32 v43, v38, v38
	v_mul_f32_e32 v43, 0xbf38aa3b, v43
	v_cndmask_b32_e32 v55, v55, v47, vcc
	v_cmp_gt_f32_e32 vcc, 0, v42
	v_fma_f32 v42, |v38|, s76, 1.0
	v_exp_f32_e32 v44, v43
	v_fma_f32 v43, |v39|, s76, 1.0
	v_rcp_f32_e32 v42, v42
	v_rcp_f32_e32 v43, v43
	v_cndmask_b32_e32 v54, v54, v46, vcc
	v_exp_f32_e32 v45, v45
	v_cmp_gt_f32_e32 vcc, 0, v41
	v_fma_f32 v46, v42, s22, v62
	v_fma_f32 v47, v43, s22, v62
	s_nop 0
	v_fma_f32 v46, v42, v46, s26
	v_fma_f32 v47, v43, v47, s26
	s_nop 0
	v_fma_f32 v46, v42, v46, s28
	v_fma_f32 v47, v43, v47, s28
	s_nop 0
	v_fma_f32 v46, v42, v46, s30
	v_fma_f32 v47, v43, v47, s30
	s_nop 0
	v_mul_f32 v42, v42, v46
	v_mul_f32 v43, v43, v47
	v_mul_f32_e32 v47, v41, v41
	v_mul_f32 v42, v44, v42
	v_mul_f32 v43, v45, v43
	v_mul_f32_e32 v45, v40, v40
	v_mul_f32_e32 v45, 0xbf38aa3b, v45
	v_fma_f32 v44, |v40|, s76, 1.0
	v_exp_f32_e32 v46, v45
	v_fma_f32 v45, |v41|, s76, 1.0
	v_rcp_f32_e32 v44, v44
	v_rcp_f32_e32 v45, v45
	v_mul_f32_e32 v47, 0xbf38aa3b, v47
	v_exp_f32_e32 v47, v47
	v_mul_f32 v42, v38, v42
	v_mul_f32 v43, v39, v43
	v_fma_f32 v48, v44, s22, v62
	v_fma_f32 v49, v45, s22, v62
	s_nop 0
	v_fma_f32 v48, v44, v48, s26
	v_fma_f32 v49, v45, v49, s26
	s_nop 0
	v_fma_f32 v48, v44, v48, s28
	v_fma_f32 v49, v45, v49, s28
	s_nop 0
	v_fma_f32 v48, v44, v48, s30
	v_fma_f32 v49, v45, v49, s30
	s_nop 0
	v_mul_f32 v44, v44, v48
	v_mul_f32 v45, v45, v49
	s_nop 0
	v_mul_f32 v44, v46, v44
	v_mul_f32 v45, v47, v45
	v_sub_f32_e32 v47, v39, v43
	v_mul_f32 v44, v40, v44
	v_mul_f32 v45, v41, v45
	v_sub_f32_e32 v46, v38, v42
	v_sub_f32_e32 v49, v41, v45
	v_sub_f32_e32 v48, v40, v44
	v_cndmask_b32_e32 v61, v49, v45, vcc
	v_cmp_gt_f32_e32 vcc, 0, v40
	v_mul_f32_e32 v41, v35, v35
	v_mul_f32_e32 v41, 0xbf38aa3b, v41
	v_cndmask_b32_e32 v60, v48, v44, vcc
	v_cmp_gt_f32_e32 vcc, 0, v39
	v_mul_f32_e32 v39, v34, v34
	v_mul_f32_e32 v39, 0xbf38aa3b, v39
	v_cndmask_b32_e32 v59, v47, v43, vcc
	v_cmp_gt_f32_e32 vcc, 0, v38
	v_fma_f32 v38, |v34|, s76, 1.0
	v_exp_f32_e32 v40, v39
	v_fma_f32 v39, |v35|, s76, 1.0
	v_rcp_f32_e32 v38, v38
	v_rcp_f32_e32 v39, v39
	v_cndmask_b32_e32 v58, v46, v42, vcc
	v_exp_f32_e32 v41, v41
	v_cmp_gt_f32_e32 vcc, 0, v37
	v_fma_f32 v42, v38, s22, v62
	v_fma_f32 v43, v39, s22, v62
	s_nop 0
	v_fma_f32 v42, v38, v42, s26
	v_fma_f32 v43, v39, v43, s26
	s_nop 0
	v_fma_f32 v42, v38, v42, s28
	v_fma_f32 v43, v39, v43, s28
	s_nop 0
	v_fma_f32 v42, v38, v42, s30
	v_fma_f32 v43, v39, v43, s30
	s_nop 0
	v_mul_f32 v38, v38, v42
	v_mul_f32 v39, v39, v43
	v_mul_f32_e32 v43, v37, v37
	v_mul_f32 v38, v40, v38
	v_mul_f32 v39, v41, v39
	v_mul_f32_e32 v41, v36, v36
	v_mul_f32_e32 v41, 0xbf38aa3b, v41
	v_fma_f32 v40, |v36|, s76, 1.0
	v_exp_f32_e32 v42, v41
	v_fma_f32 v41, |v37|, s76, 1.0
	v_rcp_f32_e32 v40, v40
	v_rcp_f32_e32 v41, v41
	v_mul_f32_e32 v43, 0xbf38aa3b, v43
	v_exp_f32_e32 v43, v43
	v_mul_f32 v38, v34, v38
	v_mul_f32 v39, v35, v39
	v_fma_f32 v44, v40, s22, v62
	v_fma_f32 v45, v41, s22, v62
	s_nop 0
	v_fma_f32 v44, v40, v44, s26
	v_fma_f32 v45, v41, v45, s26
	s_nop 0
	v_fma_f32 v44, v40, v44, s28
	v_fma_f32 v45, v41, v45, s28
	s_nop 0
	v_fma_f32 v44, v40, v44, s30
	v_fma_f32 v45, v41, v45, s30
	s_nop 0
	v_mul_f32 v40, v40, v44
	v_mul_f32 v41, v41, v45
	s_nop 0
	v_mul_f32 v40, v42, v40
	v_mul_f32 v41, v43, v41
	v_sub_f32_e32 v43, v35, v39
	v_mul_f32 v40, v36, v40
	v_mul_f32 v41, v37, v41
	v_sub_f32_e32 v42, v34, v38
	v_sub_f32_e32 v45, v37, v41
	v_sub_f32_e32 v44, v36, v40
	v_cndmask_b32_e32 v65, v45, v41, vcc
	v_cmp_gt_f32_e32 vcc, 0, v36
	s_nop 1
	v_cndmask_b32_e32 v64, v44, v40, vcc
	v_cmp_gt_f32_e32 vcc, 0, v35
	s_nop 1
	v_cndmask_b32_e32 v63, v43, v39, vcc
	v_cmp_gt_f32_e32 vcc, 0, v34
	s_nop 1
	v_cndmask_b32_e32 v62, v42, v38, vcc
.LBB0_797:
	v_add_u32_e32 v34, 0x90, v166
	v_mad_i64_i32 v[38:39], s[38:39], v34, s77, v[160:161]
	v_cvt_pk_bf16_f32 v34, v50, v51
	v_cvt_pk_bf16_f32 v35, v52, v53
	v_cvt_pk_bf16_f32 v36, v54, v55
	v_cvt_pk_bf16_f32 v37, v56, v57
	global_store_dwordx4 v[38:39], v[34:37], off
	s_nop 1
	v_cvt_pk_bf16_f32 v34, v58, v59
	v_cvt_pk_bf16_f32 v35, v60, v61
	v_cvt_pk_bf16_f32 v36, v62, v63
	v_cvt_pk_bf16_f32 v37, v64, v65
	s_and_b64 vcc, exec, s[4:5]
	s_mov_b64 s[38:39], -1
	global_store_dwordx4 v[38:39], v[34:37], off offset:256
	s_cbranch_vccnz .LBB0_801
	s_nop 0
	v_mov_b64_e32 v[36:37], v[32:33]
	v_mov_b64_e32 v[48:49], v[20:21]
	v_mov_b64_e32 v[44:45], v[24:25]
	v_mov_b64_e32 v[40:41], v[28:29]
	s_and_b64 vcc, exec, s[2:3]
	v_mov_b64_e32 v[34:35], v[30:31]
	v_mov_b64_e32 v[46:47], v[18:19]
	v_mov_b64_e32 v[42:43], v[22:23]
	v_mov_b64_e32 v[38:39], v[26:27]
	s_cbranch_vccnz .LBB0_800
	v_mul_f32 v36, v32, s20
	v_mul_f32 v37, v33, s20
	v_mul_f32 v34, v30, s20
	v_mul_f32 v35, v31, s20
	v_mul_f32 v40, v28, s20
	v_mul_f32 v41, v29, s20
	v_mul_f32 v38, v26, s20
	v_mul_f32 v39, v27, s20
	v_mul_f32 v44, v24, s20
	v_mul_f32 v45, v25, s20
	v_mul_f32 v42, v22, s20
	v_mul_f32 v43, v23, s20
	v_mul_f32 v48, v20, s20
	v_mul_f32 v49, v21, s20
	v_mul_f32 v46, v18, s20
	v_mul_f32 v47, v19, s20

.LBB0_801:
	s_andn2_b64 vcc, exec, s[38:39]
	s_cbranch_vccnz .LBB0_803
	v_mul_f32_e32 v35, v30, v30
	v_mul_f32_e32 v35, 0xbf38aa3b, v35
	v_fma_f32 v34, |v30|, s76, 1.0
	v_exp_f32_e32 v36, v35
	v_fma_f32 v35, |v31|, s76, 1.0
	v_rcp_f32_e32 v34, v34
	v_rcp_f32_e32 v35, v35
	v_mul_f32_e32 v37, v31, v31
	v_mov_b64_e32 v[46:47], s[24:25]
	v_mul_f32_e32 v37, 0xbf38aa3b, v37
	v_fma_f32 v38, v34, s22, v46
	v_fma_f32 v39, v35, s22, v46
	v_exp_f32_e32 v37, v37
	v_fma_f32 v38, v34, v38, s26
	v_fma_f32 v39, v35, v39, s26
	v_cmp_gt_f32_e32 vcc, 0, v33
	v_fma_f32 v38, v34, v38, s28
	v_fma_f32 v39, v35, v39, s28
	s_nop 0
	v_fma_f32 v38, v34, v38, s30
	v_fma_f32 v39, v35, v39, s30
	s_nop 0
	v_mul_f32 v34, v34, v38
	v_mul_f32 v35, v35, v39
	v_mul_f32_e32 v39, v33, v33
	v_mul_f32 v34, v36, v34
	v_mul_f32 v35, v37, v35
	v_mul_f32_e32 v37, v32, v32
	v_mul_f32_e32 v37, 0xbf38aa3b, v37
	v_fma_f32 v36, |v32|, s76, 1.0
	v_exp_f32_e32 v38, v37
	v_fma_f32 v37, |v33|, s76, 1.0
	v_rcp_f32_e32 v36, v36
	v_rcp_f32_e32 v37, v37
	v_mul_f32_e32 v39, 0xbf38aa3b, v39
	v_exp_f32_e32 v39, v39
	v_mul_f32 v34, v30, v34
	v_mul_f32 v35, v31, v35
	v_fma_f32 v40, v36, s22, v46
	v_fma_f32 v41, v37, s22, v46
	s_nop 0
	v_fma_f32 v40, v36, v40, s26
	v_fma_f32 v41, v37, v41, s26
	s_nop 0
	v_fma_f32 v40, v36, v40, s28
	v_fma_f32 v41, v37, v41, s28
	s_nop 0
	v_fma_f32 v40, v36, v40, s30
	v_fma_f32 v41, v37, v41, s30
	s_nop 0
	v_mul_f32 v36, v36, v40
	v_mul_f32 v37, v37, v41
	s_nop 0
	v_mul_f32 v36, v38, v36
	v_mul_f32 v37, v39, v37
	v_sub_f32_e32 v39, v31, v35
	v_mul_f32 v36, v32, v36
	v_mul_f32 v37, v33, v37
	v_sub_f32_e32 v38, v30, v34
	v_sub_f32_e32 v41, v33, v37
	v_sub_f32_e32 v40, v32, v36
	v_cndmask_b32_e32 v37, v41, v37, vcc
	v_cmp_gt_f32_e32 vcc, 0, v32
	v_mul_f32_e32 v33, v27, v27
	v_mul_f32_e32 v33, 0xbf38aa3b, v33
	v_cndmask_b32_e32 v36, v40, v36, vcc
	v_cmp_gt_f32_e32 vcc, 0, v31
	v_mul_f32_e32 v31, v26, v26
	v_mul_f32_e32 v31, 0xbf38aa3b, v31
	v_cndmask_b32_e32 v35, v39, v35, vcc
	v_cmp_gt_f32_e32 vcc, 0, v30
	v_fma_f32 v30, |v26|, s76, 1.0
	v_exp_f32_e32 v32, v31
	v_fma_f32 v31, |v27|, s76, 1.0
	v_rcp_f32_e32 v30, v30
	v_rcp_f32_e32 v31, v31
	v_cndmask_b32_e32 v34, v38, v34, vcc
	v_exp_f32_e32 v33, v33
	v_cmp_gt_f32_e32 vcc, 0, v29
	v_fma_f32 v38, v30, s22, v46
	v_fma_f32 v39, v31, s22, v46
	s_nop 0
	v_fma_f32 v38, v30, v38, s26
	v_fma_f32 v39, v31, v39, s26
	s_nop 0
	v_fma_f32 v38, v30, v38, s28
	v_fma_f32 v39, v31, v39, s28
	s_nop 0
	v_fma_f32 v38, v30, v38, s30
	v_fma_f32 v39, v31, v39, s30
	s_nop 0
	v_mul_f32 v30, v30, v38
	v_mul_f32 v31, v31, v39
	v_mul_f32_e32 v39, v29, v29
	v_mul_f32 v30, v32, v30
	v_mul_f32 v31, v33, v31
	v_mul_f32_e32 v33, v28, v28
	v_mul_f32_e32 v33, 0xbf38aa3b, v33
	v_fma_f32 v32, |v28|, s76, 1.0
	v_exp_f32_e32 v38, v33
	v_fma_f32 v33, |v29|, s76, 1.0
	v_rcp_f32_e32 v32, v32
	v_rcp_f32_e32 v33, v33
	v_mul_f32_e32 v39, 0xbf38aa3b, v39
	v_exp_f32_e32 v39, v39
	v_mul_f32 v30, v26, v30
	v_mul_f32 v31, v27, v31
	v_fma_f32 v40, v32, s22, v46
	v_fma_f32 v41, v33, s22, v46
	s_nop 0
	v_fma_f32 v40, v32, v40, s26
	v_fma_f32 v41, v33, v41, s26
	s_nop 0
	v_fma_f32 v40, v32, v40, s28
	v_fma_f32 v41, v33, v41, s28
	s_nop 0
	v_fma_f32 v40, v32, v40, s30
	v_fma_f32 v41, v33, v41, s30
	s_nop 0
	v_mul_f32 v32, v32, v40
	v_mul_f32 v33, v33, v41
	s_nop 0
	v_mul_f32 v32, v38, v32
	v_mul_f32 v33, v39, v33
	v_sub_f32_e32 v39, v27, v31
	v_mul_f32 v32, v28, v32
	v_mul_f32 v33, v29, v33
	v_sub_f32_e32 v38, v26, v30
	v_sub_f32_e32 v41, v29, v33
	v_sub_f32_e32 v40, v28, v32
	v_cndmask_b32_e32 v41, v41, v33, vcc
	v_cmp_gt_f32_e32 vcc, 0, v28
	v_mul_f32_e32 v29, v23, v23
	v_mul_f32_e32 v29, 0xbf38aa3b, v29
	v_cndmask_b32_e32 v40, v40, v32, vcc
	v_cmp_gt_f32_e32 vcc, 0, v27
	v_mul_f32_e32 v27, v22, v22
	v_mul_f32_e32 v27, 0xbf38aa3b, v27
	v_cndmask_b32_e32 v39, v39, v31, vcc
	v_cmp_gt_f32_e32 vcc, 0, v26
	v_fma_f32 v26, |v22|, s76, 1.0
	v_exp_f32_e32 v28, v27
	v_fma_f32 v27, |v23|, s76, 1.0
	v_rcp_f32_e32 v26, v26
	v_rcp_f32_e32 v27, v27
	v_cndmask_b32_e32 v38, v38, v30, vcc
	v_exp_f32_e32 v29, v29
	v_cmp_gt_f32_e32 vcc, 0, v25
	v_fma_f32 v30, v26, s22, v46
	v_fma_f32 v31, v27, s22, v46
	s_nop 0
	v_fma_f32 v30, v26, v30, s26
	v_fma_f32 v31, v27, v31, s26
	s_nop 0
	v_fma_f32 v30, v26, v30, s28
	v_fma_f32 v31, v27, v31, s28
	s_nop 0
	v_fma_f32 v30, v26, v30, s30
	v_fma_f32 v31, v27, v31, s30
	s_nop 0
	v_mul_f32 v26, v26, v30
	v_mul_f32 v27, v27, v31
	v_mul_f32_e32 v31, v25, v25
	v_mul_f32 v26, v28, v26
	v_mul_f32 v27, v29, v27
	v_mul_f32_e32 v29, v24, v24
	v_mul_f32_e32 v29, 0xbf38aa3b, v29
	v_fma_f32 v28, |v24|, s76, 1.0
	v_exp_f32_e32 v30, v29
	v_fma_f32 v29, |v25|, s76, 1.0
	v_rcp_f32_e32 v28, v28
	v_rcp_f32_e32 v29, v29
	v_mul_f32_e32 v31, 0xbf38aa3b, v31
	v_exp_f32_e32 v31, v31
	v_mul_f32 v26, v22, v26
	v_mul_f32 v27, v23, v27
	v_fma_f32 v32, v28, s22, v46
	v_fma_f32 v33, v29, s22, v46
	s_nop 0
	v_fma_f32 v32, v28, v32, s26
	v_fma_f32 v33, v29, v33, s26
	s_nop 0
	v_fma_f32 v32, v28, v32, s28
	v_fma_f32 v33, v29, v33, s28
	s_nop 0
	v_fma_f32 v32, v28, v32, s30
	v_fma_f32 v33, v29, v33, s30
	s_nop 0
	v_mul_f32 v28, v28, v32
	v_mul_f32 v29, v29, v33
	s_nop 0
	v_mul_f32 v28, v30, v28
	v_mul_f32 v29, v31, v29
	v_sub_f32_e32 v31, v23, v27
	v_mul_f32 v28, v24, v28
	v_mul_f32 v29, v25, v29
	v_sub_f32_e32 v30, v22, v26
	v_sub_f32_e32 v33, v25, v29
	v_sub_f32_e32 v32, v24, v28
	v_cndmask_b32_e32 v45, v33, v29, vcc
	v_cmp_gt_f32_e32 vcc, 0, v24
	v_mul_f32_e32 v25, v19, v19
	v_mul_f32_e32 v25, 0xbf38aa3b, v25
	v_cndmask_b32_e32 v44, v32, v28, vcc
	v_cmp_gt_f32_e32 vcc, 0, v23
	v_mul_f32_e32 v23, v18, v18
	v_mul_f32_e32 v23, 0xbf38aa3b, v23
	v_cndmask_b32_e32 v43, v31, v27, vcc
	v_cmp_gt_f32_e32 vcc, 0, v22
	v_fma_f32 v22, |v18|, s76, 1.0
	v_exp_f32_e32 v24, v23
	v_fma_f32 v23, |v19|, s76, 1.0
	v_rcp_f32_e32 v22, v22
	v_rcp_f32_e32 v23, v23
	v_cndmask_b32_e32 v42, v30, v26, vcc
	v_exp_f32_e32 v25, v25
	v_cmp_gt_f32_e32 vcc, 0, v21
	v_fma_f32 v26, v22, s22, v46
	v_fma_f32 v27, v23, s22, v46
	s_nop 0
	v_fma_f32 v26, v22, v26, s26
	v_fma_f32 v27, v23, v27, s26
	s_nop 0
	v_fma_f32 v26, v22, v26, s28
	v_fma_f32 v27, v23, v27, s28
	s_nop 0
	v_fma_f32 v26, v22, v26, s30
	v_fma_f32 v27, v23, v27, s30
	s_nop 0
	v_mul_f32 v22, v22, v26
	v_mul_f32 v23, v23, v27
	v_mul_f32_e32 v27, v21, v21
	v_mul_f32 v22, v24, v22
	v_mul_f32 v23, v25, v23
	v_mul_f32_e32 v25, v20, v20
	v_mul_f32_e32 v25, 0xbf38aa3b, v25
	v_fma_f32 v24, |v20|, s76, 1.0
	v_exp_f32_e32 v26, v25
	v_fma_f32 v25, |v21|, s76, 1.0
	v_rcp_f32_e32 v24, v24
	v_rcp_f32_e32 v25, v25
	v_mul_f32_e32 v27, 0xbf38aa3b, v27
	v_exp_f32_e32 v27, v27
	v_mul_f32 v22, v18, v22
	v_mul_f32 v23, v19, v23
	v_fma_f32 v28, v24, s22, v46
	v_fma_f32 v29, v25, s22, v46
	s_nop 0
	v_fma_f32 v28, v24, v28, s26
	v_fma_f32 v29, v25, v29, s26
	s_nop 0
	v_fma_f32 v28, v24, v28, s28
	v_fma_f32 v29, v25, v29, s28
	s_nop 0
	v_fma_f32 v28, v24, v28, s30
	v_fma_f32 v29, v25, v29, s30
	s_nop 0
	v_mul_f32 v24, v24, v28
	v_mul_f32 v25, v25, v29
	s_nop 0
	v_mul_f32 v24, v26, v24
	v_mul_f32 v25, v27, v25
	v_sub_f32_e32 v27, v19, v23
	v_mul_f32 v24, v20, v24
	v_mul_f32 v25, v21, v25
	v_sub_f32_e32 v26, v18, v22
	v_sub_f32_e32 v29, v21, v25
	v_sub_f32_e32 v28, v20, v24
	v_cndmask_b32_e32 v49, v29, v25, vcc
	v_cmp_gt_f32_e32 vcc, 0, v20
	s_nop 1
	v_cndmask_b32_e32 v48, v28, v24, vcc
	v_cmp_gt_f32_e32 vcc, 0, v19
	s_nop 1
	v_cndmask_b32_e32 v47, v27, v23, vcc
	v_cmp_gt_f32_e32 vcc, 0, v18
	s_nop 1
	v_cndmask_b32_e32 v46, v26, v22, vcc
.LBB0_803:
	v_add_u32_e32 v18, 0xa0, v166
	v_mad_i64_i32 v[22:23], s[38:39], v18, s77, v[160:161]
	v_cvt_pk_bf16_f32 v18, v34, v35
	v_cvt_pk_bf16_f32 v19, v36, v37
	v_cvt_pk_bf16_f32 v20, v38, v39
	v_cvt_pk_bf16_f32 v21, v40, v41
	global_store_dwordx4 v[22:23], v[18:21], off
	s_nop 1
	v_cvt_pk_bf16_f32 v18, v42, v43
	v_cvt_pk_bf16_f32 v19, v44, v45
	v_cvt_pk_bf16_f32 v20, v46, v47
	v_cvt_pk_bf16_f32 v21, v48, v49
	s_and_b64 vcc, exec, s[4:5]
	s_mov_b64 s[4:5], -1
	global_store_dwordx4 v[22:23], v[18:21], off offset:256
	s_cbranch_vccnz .LBB0_807
	s_nop 0
	v_mov_b64_e32 v[20:21], v[16:17]
	v_mov_b64_e32 v[32:33], v[4:5]
	v_mov_b64_e32 v[28:29], v[8:9]
	v_mov_b64_e32 v[24:25], v[12:13]
	s_and_b64 vcc, exec, s[2:3]
	v_mov_b64_e32 v[18:19], v[14:15]
	v_mov_b64_e32 v[30:31], v[2:3]
	v_mov_b64_e32 v[26:27], v[6:7]
	v_mov_b64_e32 v[22:23], v[10:11]
	s_cbranch_vccnz .LBB0_806
	v_mul_f32 v20, v16, s20
	v_mul_f32 v21, v17, s20
	v_mul_f32 v18, v14, s20
	v_mul_f32 v19, v15, s20
	v_mul_f32 v24, v12, s20
	v_mul_f32 v25, v13, s20
	v_mul_f32 v22, v10, s20
	v_mul_f32 v23, v11, s20
	v_mul_f32 v28, v8, s20
	v_mul_f32 v29, v9, s20
	v_mul_f32 v26, v6, s20
	v_mul_f32 v27, v7, s20
	v_mul_f32 v32, v4, s20
	v_mul_f32 v33, v5, s20
	v_mul_f32 v30, v2, s20
	v_mul_f32 v31, v3, s20

.LBB0_807:
	s_andn2_b64 vcc, exec, s[4:5]
	s_cbranch_vccnz .LBB0_809
	v_mul_f32_e32 v19, v14, v14
	v_mul_f32_e32 v19, 0xbf38aa3b, v19
	v_fma_f32 v18, |v14|, s76, 1.0
	v_exp_f32_e32 v20, v19
	v_fma_f32 v19, |v15|, s76, 1.0
	v_rcp_f32_e32 v18, v18
	v_rcp_f32_e32 v19, v19
	v_mul_f32_e32 v21, v15, v15
	v_mov_b64_e32 v[30:31], s[24:25]
	v_mul_f32_e32 v21, 0xbf38aa3b, v21
	v_fma_f32 v22, v18, s22, v30
	v_fma_f32 v23, v19, s22, v30
	v_exp_f32_e32 v21, v21
	v_fma_f32 v22, v18, v22, s26
	v_fma_f32 v23, v19, v23, s26
	v_cmp_gt_f32_e32 vcc, 0, v17
	v_fma_f32 v22, v18, v22, s28
	v_fma_f32 v23, v19, v23, s28
	s_nop 0
	v_fma_f32 v22, v18, v22, s30
	v_fma_f32 v23, v19, v23, s30
	s_nop 0
	v_mul_f32 v18, v18, v22
	v_mul_f32 v19, v19, v23
	v_mul_f32_e32 v23, v17, v17
	v_mul_f32 v18, v20, v18
	v_mul_f32 v19, v21, v19
	v_mul_f32_e32 v21, v16, v16
	v_mul_f32_e32 v21, 0xbf38aa3b, v21
	v_fma_f32 v20, |v16|, s76, 1.0
	v_exp_f32_e32 v22, v21
	v_fma_f32 v21, |v17|, s76, 1.0
	v_rcp_f32_e32 v20, v20
	v_rcp_f32_e32 v21, v21
	v_mul_f32_e32 v23, 0xbf38aa3b, v23
	v_exp_f32_e32 v23, v23
	v_mul_f32 v18, v14, v18
	v_mul_f32 v19, v15, v19
	v_fma_f32 v24, v20, s22, v30
	v_fma_f32 v25, v21, s22, v30
	s_nop 0
	v_fma_f32 v24, v20, v24, s26
	v_fma_f32 v25, v21, v25, s26
	s_nop 0
	v_fma_f32 v24, v20, v24, s28
	v_fma_f32 v25, v21, v25, s28
	s_nop 0
	v_fma_f32 v24, v20, v24, s30
	v_fma_f32 v25, v21, v25, s30
	s_nop 0
	v_mul_f32 v20, v20, v24
	v_mul_f32 v21, v21, v25
	s_nop 0
	v_mul_f32 v20, v22, v20
	v_mul_f32 v21, v23, v21
	v_sub_f32_e32 v23, v15, v19
	v_mul_f32 v20, v16, v20
	v_mul_f32 v21, v17, v21
	v_sub_f32_e32 v22, v14, v18
	v_sub_f32_e32 v25, v17, v21
	v_sub_f32_e32 v24, v16, v20
	v_cndmask_b32_e32 v21, v25, v21, vcc
	v_cmp_gt_f32_e32 vcc, 0, v16
	v_mul_f32_e32 v17, v11, v11
	v_mul_f32_e32 v17, 0xbf38aa3b, v17
	v_cndmask_b32_e32 v20, v24, v20, vcc
	v_cmp_gt_f32_e32 vcc, 0, v15
	v_mul_f32_e32 v15, v10, v10
	v_mul_f32_e32 v15, 0xbf38aa3b, v15
	v_cndmask_b32_e32 v19, v23, v19, vcc
	v_cmp_gt_f32_e32 vcc, 0, v14
	v_fma_f32 v14, |v10|, s76, 1.0
	v_exp_f32_e32 v16, v15
	v_fma_f32 v15, |v11|, s76, 1.0
	v_rcp_f32_e32 v14, v14
	v_rcp_f32_e32 v15, v15
	v_cndmask_b32_e32 v18, v22, v18, vcc
	v_exp_f32_e32 v17, v17
	v_cmp_gt_f32_e32 vcc, 0, v13
	v_fma_f32 v22, v14, s22, v30
	v_fma_f32 v23, v15, s22, v30
	s_nop 0
	v_fma_f32 v22, v14, v22, s26
	v_fma_f32 v23, v15, v23, s26
	s_nop 0
	v_fma_f32 v22, v14, v22, s28
	v_fma_f32 v23, v15, v23, s28
	s_nop 0
	v_fma_f32 v22, v14, v22, s30
	v_fma_f32 v23, v15, v23, s30
	s_nop 0
	v_mul_f32 v14, v14, v22
	v_mul_f32 v15, v15, v23
	v_mul_f32_e32 v23, v13, v13
	v_mul_f32 v14, v16, v14
	v_mul_f32 v15, v17, v15
	v_mul_f32_e32 v17, v12, v12
	v_mul_f32_e32 v17, 0xbf38aa3b, v17
	v_fma_f32 v16, |v12|, s76, 1.0
	v_exp_f32_e32 v22, v17
	v_fma_f32 v17, |v13|, s76, 1.0
	v_rcp_f32_e32 v16, v16
	v_rcp_f32_e32 v17, v17
	v_mul_f32_e32 v23, 0xbf38aa3b, v23
	v_exp_f32_e32 v23, v23
	v_mul_f32 v14, v10, v14
	v_mul_f32 v15, v11, v15
	v_fma_f32 v24, v16, s22, v30
	v_fma_f32 v25, v17, s22, v30
	s_nop 0
	v_fma_f32 v24, v16, v24, s26
	v_fma_f32 v25, v17, v25, s26
	s_nop 0
	v_fma_f32 v24, v16, v24, s28
	v_fma_f32 v25, v17, v25, s28
	s_nop 0
	v_fma_f32 v24, v16, v24, s30
	v_fma_f32 v25, v17, v25, s30
	s_nop 0
	v_mul_f32 v16, v16, v24
	v_mul_f32 v17, v17, v25
	s_nop 0
	v_mul_f32 v16, v22, v16
	v_mul_f32 v17, v23, v17
	v_sub_f32_e32 v23, v11, v15
	v_mul_f32 v16, v12, v16
	v_mul_f32 v17, v13, v17
	v_sub_f32_e32 v22, v10, v14
	v_sub_f32_e32 v25, v13, v17
	v_sub_f32_e32 v24, v12, v16
	v_cndmask_b32_e32 v25, v25, v17, vcc
	v_cmp_gt_f32_e32 vcc, 0, v12
	v_mul_f32_e32 v13, v7, v7
	v_mul_f32_e32 v13, 0xbf38aa3b, v13
	v_cndmask_b32_e32 v24, v24, v16, vcc
	v_cmp_gt_f32_e32 vcc, 0, v11
	v_mul_f32_e32 v11, v6, v6
	v_mul_f32_e32 v11, 0xbf38aa3b, v11
	v_cndmask_b32_e32 v23, v23, v15, vcc
	v_cmp_gt_f32_e32 vcc, 0, v10
	v_fma_f32 v10, |v6|, s76, 1.0
	v_exp_f32_e32 v12, v11
	v_fma_f32 v11, |v7|, s76, 1.0
	v_rcp_f32_e32 v10, v10
	v_rcp_f32_e32 v11, v11
	v_cndmask_b32_e32 v22, v22, v14, vcc
	v_exp_f32_e32 v13, v13
	v_cmp_gt_f32_e32 vcc, 0, v9
	v_fma_f32 v14, v10, s22, v30
	v_fma_f32 v15, v11, s22, v30
	s_nop 0
	v_fma_f32 v14, v10, v14, s26
	v_fma_f32 v15, v11, v15, s26
	s_nop 0
	v_fma_f32 v14, v10, v14, s28
	v_fma_f32 v15, v11, v15, s28
	s_nop 0
	v_fma_f32 v14, v10, v14, s30
	v_fma_f32 v15, v11, v15, s30
	s_nop 0
	v_mul_f32 v10, v10, v14
	v_mul_f32 v11, v11, v15
	v_mul_f32_e32 v15, v9, v9
	v_mul_f32 v10, v12, v10
	v_mul_f32 v11, v13, v11
	v_mul_f32_e32 v13, v8, v8
	v_mul_f32_e32 v13, 0xbf38aa3b, v13
	v_fma_f32 v12, |v8|, s76, 1.0
	v_exp_f32_e32 v14, v13
	v_fma_f32 v13, |v9|, s76, 1.0
	v_rcp_f32_e32 v12, v12
	v_rcp_f32_e32 v13, v13
	v_mul_f32_e32 v15, 0xbf38aa3b, v15
	v_exp_f32_e32 v15, v15
	v_mul_f32 v10, v6, v10
	v_mul_f32 v11, v7, v11
	v_fma_f32 v16, v12, s22, v30
	v_fma_f32 v17, v13, s22, v30
	s_nop 0
	v_fma_f32 v16, v12, v16, s26
	v_fma_f32 v17, v13, v17, s26
	s_nop 0
	v_fma_f32 v16, v12, v16, s28
	v_fma_f32 v17, v13, v17, s28
	s_nop 0
	v_fma_f32 v16, v12, v16, s30
	v_fma_f32 v17, v13, v17, s30
	s_nop 0
	v_mul_f32 v12, v12, v16
	v_mul_f32 v13, v13, v17
	s_nop 0
	v_mul_f32 v12, v14, v12
	v_mul_f32 v13, v15, v13
	v_sub_f32_e32 v15, v7, v11
	v_mul_f32 v12, v8, v12
	v_mul_f32 v13, v9, v13
	v_sub_f32_e32 v14, v6, v10
	v_sub_f32_e32 v17, v9, v13
	v_sub_f32_e32 v16, v8, v12
	v_cndmask_b32_e32 v29, v17, v13, vcc
	v_cmp_gt_f32_e32 vcc, 0, v8
	v_mul_f32_e32 v9, v3, v3
	v_mul_f32_e32 v9, 0xbf38aa3b, v9
	v_cndmask_b32_e32 v28, v16, v12, vcc
	v_cmp_gt_f32_e32 vcc, 0, v7
	v_mul_f32_e32 v7, v2, v2
	v_mul_f32_e32 v7, 0xbf38aa3b, v7
	v_cndmask_b32_e32 v27, v15, v11, vcc
	v_cmp_gt_f32_e32 vcc, 0, v6
	v_fma_f32 v6, |v2|, s76, 1.0
	v_exp_f32_e32 v8, v7
	v_fma_f32 v7, |v3|, s76, 1.0
	v_rcp_f32_e32 v6, v6
	v_rcp_f32_e32 v7, v7
	v_cndmask_b32_e32 v26, v14, v10, vcc
	v_exp_f32_e32 v9, v9
	v_cmp_gt_f32_e32 vcc, 0, v5
	v_fma_f32 v10, v6, s22, v30
	v_fma_f32 v11, v7, s22, v30
	s_nop 0
	v_fma_f32 v10, v6, v10, s26
	v_fma_f32 v11, v7, v11, s26
	s_nop 0
	v_fma_f32 v10, v6, v10, s28
	v_fma_f32 v11, v7, v11, s28
	s_nop 0
	v_fma_f32 v10, v6, v10, s30
	v_fma_f32 v11, v7, v11, s30
	s_nop 0
	v_mul_f32 v6, v6, v10
	v_mul_f32 v7, v7, v11
	v_mul_f32_e32 v11, v5, v5
	v_mul_f32 v6, v8, v6
	v_mul_f32 v7, v9, v7
	v_mul_f32_e32 v9, v4, v4
	v_mul_f32_e32 v9, 0xbf38aa3b, v9
	v_fma_f32 v8, |v4|, s76, 1.0
	v_exp_f32_e32 v10, v9
	v_fma_f32 v9, |v5|, s76, 1.0
	v_rcp_f32_e32 v8, v8
	v_rcp_f32_e32 v9, v9
	v_mul_f32_e32 v11, 0xbf38aa3b, v11
	v_exp_f32_e32 v11, v11
	v_mul_f32 v6, v2, v6
	v_mul_f32 v7, v3, v7
	v_fma_f32 v12, v8, s22, v30
	v_fma_f32 v13, v9, s22, v30
	s_nop 0
	v_fma_f32 v12, v8, v12, s26
	v_fma_f32 v13, v9, v13, s26
	s_nop 0
	v_fma_f32 v12, v8, v12, s28
	v_fma_f32 v13, v9, v13, s28
	s_nop 0
	v_fma_f32 v12, v8, v12, s30
	v_fma_f32 v13, v9, v13, s30
	s_nop 0
	v_mul_f32 v8, v8, v12
	v_mul_f32 v9, v9, v13
	s_nop 0
	v_mul_f32 v8, v10, v8
	v_mul_f32 v9, v11, v9
	v_sub_f32_e32 v11, v3, v7
	v_mul_f32 v8, v4, v8
	v_mul_f32 v9, v5, v9
	v_sub_f32_e32 v10, v2, v6
	v_sub_f32_e32 v13, v5, v9
	v_sub_f32_e32 v12, v4, v8
	v_cndmask_b32_e32 v33, v13, v9, vcc
	v_cmp_gt_f32_e32 vcc, 0, v4
	s_nop 1
	v_cndmask_b32_e32 v32, v12, v8, vcc
	v_cmp_gt_f32_e32 vcc, 0, v3
	s_nop 1
	v_cndmask_b32_e32 v31, v11, v7, vcc
	v_cmp_gt_f32_e32 vcc, 0, v2
	s_nop 1
	v_cndmask_b32_e32 v30, v10, v6, vcc

.LBB0_1393:
	v_mul_f32_e32 v5, 0xbfb8aa3b, v190
	v_exp_f32_e32 v5, v5
	s_lshl_b32 s38, s42, 8
	v_mov_b32_e32 v2, v0
	s_add_i32 s38, s38, s31
	v_add_f32_e32 v5, 1.0, v5
	v_rcp_f32_e32 v6, v5
	v_mul_f32_e32 v5, 0xbfb8aa3b, v191
	v_exp_f32_e32 v5, v5
	s_nop 0
	v_and_or_b32 v4, v2, 15, s38
	v_add_f32_e32 v5, 1.0, v5
	v_rcp_f32_e32 v7, v5
	v_mul_f32_e32 v5, 0xbfb8aa3b, v192
	v_exp_f32_e32 v5, v5
	s_lshl_b32 s38, s45, 7
	v_mul_f32 v6, v190, v6
	v_mul_f32 v7, v191, v7
	s_ashr_i32 s39, s38, 31
	v_add_f32_e32 v5, 1.0, v5
	v_rcp_f32_e32 v8, v5
	v_mul_f32_e32 v5, 0xbfb8aa3b, v193
	v_exp_f32_e32 v5, v5
	v_mul_f32 v6, v6, v186
	v_mul_f32 v7, v7, v187
	v_lshrrev_b32_e32 v2, 1, v2
	v_mul_f32 v6, v6, s66
	v_mul_f32 v7, v7, s66
	v_add_f32_e32 v5, 1.0, v5
	v_rcp_f32_e32 v9, v5
	v_mul_f32_e32 v5, 0xbfb8aa3b, v182
	v_exp_f32_e32 v5, v5
	v_med3_f32 v7, v7, s29, v1
	v_mul_f32 v8, v192, v8
	v_mul_f32 v9, v193, v9
	s_add_u32 s38, s5, s38
	v_add_f32_e32 v5, 1.0, v5
	v_rcp_f32_e32 v10, v5
	v_mul_f32_e32 v5, 0xbfb8aa3b, v183
	v_exp_f32_e32 v5, v5
	v_mul_f32 v8, v8, v188
	v_mul_f32 v9, v9, v189
	v_and_or_b32 v194, v2, 24, s25
	v_mul_f32 v8, v8, s66
	v_mul_f32 v9, v9, s66
	v_add_f32_e32 v5, 1.0, v5
	v_rcp_f32_e32 v11, v5
	v_mul_f32_e32 v5, 0xbfb8aa3b, v184
	v_exp_f32_e32 v5, v5
	s_addc_u32 s39, s4, s39
	v_mul_f32 v10, v182, v10
	v_mul_f32 v11, v183, v11
	v_lshl_add_u64 v[2:3], s[38:39], 0, v[194:195]
	v_add_f32_e32 v5, 1.0, v5
	v_rcp_f32_e32 v12, v5
	v_mul_f32_e32 v5, 0xbfb8aa3b, v185
	v_exp_f32_e32 v5, v5
	v_mul_f32 v10, v10, v178
	v_mul_f32 v11, v11, v179
	s_andn2_b64 vcc, exec, s[92:93]
	v_mul_f32 v10, v10, s66
	v_mul_f32 v11, v11, s66
	v_add_f32_e32 v5, 1.0, v5
	v_rcp_f32_e32 v13, v5
	v_med3_f32 v5, v6, s29, v1
	v_mov_b32_e32 v6, v195
	v_cvt_pk_fp8_f32 v6, v5, v7
	v_med3_f32 v5, v8, s29, v1
	v_med3_f32 v7, v9, s29, v1
	v_med3_f32 v8, v11, s29, v1
	v_cvt_pk_fp8_f32 v6, v5, v7 op_sel:[0,0,1]
	v_med3_f32 v5, v10, s29, v1
	v_mov_b32_e32 v7, v195
	v_mul_f32 v12, v184, v12
	v_mul_f32 v13, v185, v13
	v_cvt_pk_fp8_f32 v7, v5, v8
	v_mul_f32 v12, v12, v180
	v_mul_f32 v13, v13, v181
	v_mul_f32_e32 v10, 0xbfb8aa3b, v166
	v_mul_f32 v12, v12, s66
	v_mul_f32 v13, v13, s66
	v_mul_f32_e32 v11, 0xbfb8aa3b, v167
	v_med3_f32 v5, v12, s29, v1
	v_med3_f32 v8, v13, s29, v1
	v_cvt_pk_fp8_f32 v7, v5, v8 op_sel:[0,0,1]
	v_mad_i64_i32 v[8:9], s[38:39], v4, s2, v[2:3]
	v_exp_f32_e32 v10, v10
	global_store_dwordx2 v[8:9], v[6:7], off
	v_mul_f32_e32 v6, 0xbfb8aa3b, v174
	v_mul_f32_e32 v7, 0xbfb8aa3b, v175
	v_exp_f32_e32 v6, v6
	v_exp_f32_e32 v7, v7
	v_mul_f32_e32 v8, 0xbfb8aa3b, v176
	v_mul_f32_e32 v9, 0xbfb8aa3b, v177
	v_add_f32_e32 v6, 1.0, v6
	v_add_f32_e32 v7, 1.0, v7
	v_exp_f32_e32 v8, v8
	v_exp_f32_e32 v9, v9
	v_rcp_f32_e32 v6, v6
	v_rcp_f32_e32 v7, v7
	v_exp_f32_e32 v11, v11
	v_add_f32_e32 v8, 1.0, v8
	v_add_f32_e32 v9, 1.0, v9
	v_mul_f32_e32 v12, 0xbfb8aa3b, v168
	v_mul_f32_e32 v13, 0xbfb8aa3b, v169
	v_rcp_f32_e32 v8, v8
	v_rcp_f32_e32 v9, v9
	v_mul_f32 v6, v174, v6
	v_mul_f32 v7, v175, v7
	v_add_f32_e32 v10, 1.0, v10
	v_add_f32_e32 v11, 1.0, v11
	v_exp_f32_e32 v12, v12
	v_exp_f32_e32 v13, v13
	v_mul_f32 v6, v6, v170
	v_mul_f32 v7, v7, v171
	v_rcp_f32_e32 v10, v10
	v_rcp_f32_e32 v11, v11
	v_mul_f32 v6, v6, s66
	v_mul_f32 v7, v7, s66
	v_mul_f32 v8, v176, v8
	v_mul_f32 v9, v177, v9
	v_med3_f32 v14, v6, s29, v1
	v_med3_f32 v7, v7, s29, v1
	v_mov_b32_e32 v6, v195
	v_add_f32_e32 v12, 1.0, v12
	v_add_f32_e32 v13, 1.0, v13
	v_cvt_pk_fp8_f32 v6, v14, v7
	v_mul_f32 v8, v8, v172
	v_mul_f32 v9, v9, v173
	v_rcp_f32_e32 v12, v12
	v_rcp_f32_e32 v13, v13
	v_mul_f32 v10, v166, v10
	v_mul_f32 v11, v167, v11
	v_mul_f32 v8, v8, s66
	v_mul_f32 v9, v9, s66
	v_mul_f32 v10, v10, v162
	v_mul_f32 v11, v11, v163
	v_med3_f32 v7, v8, s29, v1
	v_mul_f32 v10, v10, s66
	v_mul_f32 v11, v11, s66
	v_med3_f32 v8, v9, s29, v1
	v_cvt_pk_fp8_f32 v6, v7, v8 op_sel:[0,0,1]
	v_med3_f32 v8, v10, s29, v1
	v_med3_f32 v9, v11, s29, v1
	v_mov_b32_e32 v7, v195
	v_mul_f32 v12, v168, v12
	v_mul_f32 v13, v169, v13
	v_cvt_pk_fp8_f32 v7, v8, v9
	v_mul_f32 v12, v12, v164
	v_mul_f32 v13, v13, v165
	v_or_b32_e32 v5, 16, v4
	v_mul_f32 v12, v12, s66
	v_mul_f32 v13, v13, s66
	v_mul_f32_e32 v10, 0xbfb8aa3b, v150
	v_med3_f32 v8, v12, s29, v1
	v_med3_f32 v9, v13, s29, v1
	v_cvt_pk_fp8_f32 v7, v8, v9 op_sel:[0,0,1]
	v_mad_i64_i32 v[8:9], s[38:39], v5, s2, v[2:3]
	v_mul_f32_e32 v11, 0xbfb8aa3b, v151
	global_store_dwordx2 v[8:9], v[6:7], off
	v_mul_f32_e32 v6, 0xbfb8aa3b, v158
	v_mul_f32_e32 v7, 0xbfb8aa3b, v159
	v_exp_f32_e32 v6, v6
	v_exp_f32_e32 v7, v7
	v_mul_f32_e32 v8, 0xbfb8aa3b, v160
	v_mul_f32_e32 v9, 0xbfb8aa3b, v161
	v_add_f32_e32 v6, 1.0, v6
	v_add_f32_e32 v7, 1.0, v7
	v_exp_f32_e32 v8, v8
	v_exp_f32_e32 v9, v9
	v_rcp_f32_e32 v6, v6
	v_rcp_f32_e32 v7, v7
	v_exp_f32_e32 v10, v10
	v_exp_f32_e32 v11, v11
	v_add_f32_e32 v8, 1.0, v8
	v_add_f32_e32 v9, 1.0, v9
	v_mul_f32_e32 v12, 0xbfb8aa3b, v152
	v_mul_f32_e32 v13, 0xbfb8aa3b, v153
	v_rcp_f32_e32 v8, v8
	v_rcp_f32_e32 v9, v9
	v_mul_f32 v6, v158, v6
	v_mul_f32 v7, v159, v7
	v_add_f32_e32 v10, 1.0, v10
	v_add_f32_e32 v11, 1.0, v11
	v_exp_f32_e32 v12, v12
	v_exp_f32_e32 v13, v13
	v_mul_f32 v6, v6, v154
	v_mul_f32 v7, v7, v155
	v_rcp_f32_e32 v10, v10
	v_rcp_f32_e32 v11, v11
	v_mul_f32 v6, v6, s66
	v_mul_f32 v7, v7, s66
	v_mul_f32 v8, v160, v8
	v_mul_f32 v9, v161, v9
	v_med3_f32 v14, v6, s29, v1
	v_med3_f32 v7, v7, s29, v1
	v_mov_b32_e32 v6, v195
	v_add_f32_e32 v12, 1.0, v12
	v_add_f32_e32 v13, 1.0, v13
	v_cvt_pk_fp8_f32 v6, v14, v7
	v_mul_f32 v8, v8, v156
	v_mul_f32 v9, v9, v157
	v_rcp_f32_e32 v12, v12
	v_rcp_f32_e32 v13, v13
	v_mul_f32 v10, v150, v10
	v_mul_f32 v11, v151, v11
	v_mul_f32 v8, v8, s66
	v_mul_f32 v9, v9, s66
	v_mul_f32 v10, v10, v146
	v_mul_f32 v11, v11, v147
	v_med3_f32 v7, v8, s29, v1
	v_mul_f32 v10, v10, s66
	v_mul_f32 v11, v11, s66
	v_med3_f32 v8, v9, s29, v1
	v_cvt_pk_fp8_f32 v6, v7, v8 op_sel:[0,0,1]
	v_med3_f32 v8, v10, s29, v1
	v_med3_f32 v9, v11, s29, v1
	v_mov_b32_e32 v7, v195
	v_mul_f32 v12, v152, v12
	v_mul_f32 v13, v153, v13
	v_cvt_pk_fp8_f32 v7, v8, v9
	v_mul_f32 v12, v12, v148
	v_mul_f32 v13, v13, v149
	v_or_b32_e32 v5, 32, v4
	v_mul_f32 v12, v12, s66
	v_mul_f32 v13, v13, s66
	v_mul_f32_e32 v10, 0xbfb8aa3b, v134
	v_med3_f32 v8, v12, s29, v1
	v_med3_f32 v9, v13, s29, v1
	v_cvt_pk_fp8_f32 v7, v8, v9 op_sel:[0,0,1]
	v_mad_i64_i32 v[8:9], s[38:39], v5, s2, v[2:3]
	v_mul_f32_e32 v11, 0xbfb8aa3b, v135
	global_store_dwordx2 v[8:9], v[6:7], off
	v_mul_f32_e32 v6, 0xbfb8aa3b, v142
	v_mul_f32_e32 v7, 0xbfb8aa3b, v143
	v_exp_f32_e32 v6, v6
	v_exp_f32_e32 v7, v7
	v_mul_f32_e32 v8, 0xbfb8aa3b, v144
	v_mul_f32_e32 v9, 0xbfb8aa3b, v145
	v_add_f32_e32 v6, 1.0, v6
	v_add_f32_e32 v7, 1.0, v7
	v_exp_f32_e32 v8, v8
	v_exp_f32_e32 v9, v9
	v_rcp_f32_e32 v6, v6
	v_rcp_f32_e32 v7, v7
	v_exp_f32_e32 v10, v10
	v_exp_f32_e32 v11, v11
	v_add_f32_e32 v8, 1.0, v8
	v_add_f32_e32 v9, 1.0, v9
	v_mul_f32_e32 v12, 0xbfb8aa3b, v136
	v_mul_f32_e32 v13, 0xbfb8aa3b, v137
	v_rcp_f32_e32 v8, v8
	v_rcp_f32_e32 v9, v9
	v_mul_f32 v6, v142, v6
	v_mul_f32 v7, v143, v7
	v_add_f32_e32 v10, 1.0, v10
	v_add_f32_e32 v11, 1.0, v11
	v_exp_f32_e32 v12, v12
	v_exp_f32_e32 v13, v13
	v_mul_f32 v6, v6, v138
	v_mul_f32 v7, v7, v139
	v_rcp_f32_e32 v10, v10
	v_rcp_f32_e32 v11, v11
	v_mul_f32 v6, v6, s66
	v_mul_f32 v7, v7, s66
	v_mul_f32 v8, v144, v8
	v_mul_f32 v9, v145, v9
	v_med3_f32 v14, v6, s29, v1
	v_med3_f32 v7, v7, s29, v1
	v_mov_b32_e32 v6, v195
	v_add_f32_e32 v12, 1.0, v12
	v_add_f32_e32 v13, 1.0, v13
	v_cvt_pk_fp8_f32 v6, v14, v7
	v_mul_f32 v8, v8, v140
	v_mul_f32 v9, v9, v141
	v_rcp_f32_e32 v12, v12
	v_rcp_f32_e32 v13, v13
	v_mul_f32 v10, v134, v10
	v_mul_f32 v11, v135, v11
	v_mul_f32 v8, v8, s66
	v_mul_f32 v9, v9, s66
	v_mul_f32 v10, v10, v130
	v_mul_f32 v11, v11, v131
	v_med3_f32 v7, v8, s29, v1
	v_mul_f32 v10, v10, s66
	v_mul_f32 v11, v11, s66
	v_med3_f32 v8, v9, s29, v1
	v_cvt_pk_fp8_f32 v6, v7, v8 op_sel:[0,0,1]
	v_med3_f32 v8, v10, s29, v1
	v_med3_f32 v9, v11, s29, v1
	v_mov_b32_e32 v7, v195
	v_mul_f32 v12, v136, v12
	v_mul_f32 v13, v137, v13
	v_cvt_pk_fp8_f32 v7, v8, v9
	v_mul_f32 v12, v12, v132
	v_mul_f32 v13, v13, v133
	v_or_b32_e32 v5, 48, v4
	v_mul_f32 v12, v12, s66
	v_mul_f32 v13, v13, s66
	v_mul_f32_e32 v10, 0xbfb8aa3b, v118
	v_med3_f32 v8, v12, s29, v1
	v_med3_f32 v9, v13, s29, v1
	v_cvt_pk_fp8_f32 v7, v8, v9 op_sel:[0,0,1]
	v_mad_i64_i32 v[8:9], s[38:39], v5, s2, v[2:3]
	v_mul_f32_e32 v11, 0xbfb8aa3b, v119
	global_store_dwordx2 v[8:9], v[6:7], off
	v_mul_f32_e32 v6, 0xbfb8aa3b, v126
	v_mul_f32_e32 v7, 0xbfb8aa3b, v127
	v_exp_f32_e32 v6, v6
	v_exp_f32_e32 v7, v7
	v_mul_f32_e32 v8, 0xbfb8aa3b, v128
	v_mul_f32_e32 v9, 0xbfb8aa3b, v129
	v_add_f32_e32 v6, 1.0, v6
	v_add_f32_e32 v7, 1.0, v7
	v_exp_f32_e32 v8, v8
	v_exp_f32_e32 v9, v9
	v_rcp_f32_e32 v6, v6
	v_rcp_f32_e32 v7, v7
	v_exp_f32_e32 v10, v10
	v_exp_f32_e32 v11, v11
	v_add_f32_e32 v8, 1.0, v8
	v_add_f32_e32 v9, 1.0, v9
	v_mul_f32_e32 v12, 0xbfb8aa3b, v120
	v_mul_f32_e32 v13, 0xbfb8aa3b, v121
	v_rcp_f32_e32 v8, v8
	v_rcp_f32_e32 v9, v9
	v_mul_f32 v6, v126, v6
	v_mul_f32 v7, v127, v7
	v_add_f32_e32 v10, 1.0, v10
	v_add_f32_e32 v11, 1.0, v11
	v_exp_f32_e32 v12, v12
	v_exp_f32_e32 v13, v13
	v_mul_f32 v6, v6, v122
	v_mul_f32 v7, v7, v123
	v_rcp_f32_e32 v10, v10
	v_rcp_f32_e32 v11, v11
	v_mul_f32 v6, v6, s66
	v_mul_f32 v7, v7, s66
	v_mul_f32 v8, v128, v8
	v_mul_f32 v9, v129, v9
	v_med3_f32 v14, v6, s29, v1
	v_med3_f32 v7, v7, s29, v1
	v_mov_b32_e32 v6, v195
	v_add_f32_e32 v12, 1.0, v12
	v_add_f32_e32 v13, 1.0, v13
	v_cvt_pk_fp8_f32 v6, v14, v7
	v_mul_f32 v8, v8, v124
	v_mul_f32 v9, v9, v125
	v_rcp_f32_e32 v12, v12
	v_rcp_f32_e32 v13, v13
	v_mul_f32 v10, v118, v10
	v_mul_f32 v11, v119, v11
	v_mul_f32 v8, v8, s66
	v_mul_f32 v9, v9, s66
	v_mul_f32 v10, v10, v114
	v_mul_f32 v11, v11, v115
	v_med3_f32 v7, v8, s29, v1
	v_mul_f32 v10, v10, s66
	v_mul_f32 v11, v11, s66
	v_med3_f32 v8, v9, s29, v1
	v_cvt_pk_fp8_f32 v6, v7, v8 op_sel:[0,0,1]
	v_med3_f32 v8, v10, s29, v1
	v_med3_f32 v9, v11, s29, v1
	v_mov_b32_e32 v7, v195
	v_mul_f32 v12, v120, v12
	v_mul_f32 v13, v121, v13
	v_cvt_pk_fp8_f32 v7, v8, v9
	v_mul_f32 v12, v12, v116
	v_mul_f32 v13, v13, v117
	v_add_u32_e32 v5, 0x80, v4
	v_mul_f32 v12, v12, s66
	v_mul_f32 v13, v13, s66
	v_mul_f32_e32 v10, 0xbfb8aa3b, v102
	v_med3_f32 v8, v12, s29, v1
	v_med3_f32 v9, v13, s29, v1
	v_cvt_pk_fp8_f32 v7, v8, v9 op_sel:[0,0,1]
	v_mad_i64_i32 v[8:9], s[38:39], v5, s2, v[2:3]
	v_mul_f32_e32 v11, 0xbfb8aa3b, v103
	global_store_dwordx2 v[8:9], v[6:7], off
	v_mul_f32_e32 v6, 0xbfb8aa3b, v110
	v_mul_f32_e32 v7, 0xbfb8aa3b, v111
	v_exp_f32_e32 v6, v6
	v_exp_f32_e32 v7, v7
	v_mul_f32_e32 v8, 0xbfb8aa3b, v112
	v_mul_f32_e32 v9, 0xbfb8aa3b, v113
	v_add_f32_e32 v6, 1.0, v6
	v_add_f32_e32 v7, 1.0, v7
	v_exp_f32_e32 v8, v8
	v_exp_f32_e32 v9, v9
	v_rcp_f32_e32 v6, v6
	v_rcp_f32_e32 v7, v7
	v_exp_f32_e32 v10, v10
	v_exp_f32_e32 v11, v11
	v_add_f32_e32 v8, 1.0, v8
	v_add_f32_e32 v9, 1.0, v9
	v_mul_f32_e32 v12, 0xbfb8aa3b, v104
	v_mul_f32_e32 v13, 0xbfb8aa3b, v105
	v_rcp_f32_e32 v8, v8
	v_rcp_f32_e32 v9, v9
	v_mul_f32 v6, v110, v6
	v_mul_f32 v7, v111, v7
	v_add_f32_e32 v10, 1.0, v10
	v_add_f32_e32 v11, 1.0, v11
	v_exp_f32_e32 v12, v12
	v_exp_f32_e32 v13, v13
	v_mul_f32 v6, v6, v106
	v_mul_f32 v7, v7, v107
	v_rcp_f32_e32 v10, v10
	v_rcp_f32_e32 v11, v11
	v_mul_f32 v6, v6, s66
	v_mul_f32 v7, v7, s66
	v_mul_f32 v8, v112, v8
	v_mul_f32 v9, v113, v9
	v_med3_f32 v14, v6, s29, v1
	v_med3_f32 v7, v7, s29, v1
	v_mov_b32_e32 v6, v195
	v_add_f32_e32 v12, 1.0, v12
	v_add_f32_e32 v13, 1.0, v13
	v_cvt_pk_fp8_f32 v6, v14, v7
	v_mul_f32 v8, v8, v108
	v_mul_f32 v9, v9, v109
	v_rcp_f32_e32 v12, v12
	v_rcp_f32_e32 v13, v13
	v_mul_f32 v10, v102, v10
	v_mul_f32 v11, v103, v11
	v_mul_f32 v8, v8, s66
	v_mul_f32 v9, v9, s66
	v_mul_f32 v10, v10, v98
	v_mul_f32 v11, v11, v99
	v_med3_f32 v7, v8, s29, v1
	v_mul_f32 v10, v10, s66
	v_mul_f32 v11, v11, s66
	v_med3_f32 v8, v9, s29, v1
	v_cvt_pk_fp8_f32 v6, v7, v8 op_sel:[0,0,1]
	v_med3_f32 v8, v10, s29, v1
	v_med3_f32 v9, v11, s29, v1
	v_mov_b32_e32 v7, v195
	v_mul_f32 v12, v104, v12
	v_mul_f32 v13, v105, v13
	v_cvt_pk_fp8_f32 v7, v8, v9
	v_mul_f32 v12, v12, v100
	v_mul_f32 v13, v13, v101
	v_add_u32_e32 v5, 0x90, v4
	v_mul_f32 v12, v12, s66
	v_mul_f32 v13, v13, s66
	v_mul_f32_e32 v10, 0xbfb8aa3b, v86
	v_med3_f32 v8, v12, s29, v1
	v_med3_f32 v9, v13, s29, v1
	v_cvt_pk_fp8_f32 v7, v8, v9 op_sel:[0,0,1]
	v_mad_i64_i32 v[8:9], s[38:39], v5, s2, v[2:3]
	v_mul_f32_e32 v11, 0xbfb8aa3b, v87
	global_store_dwordx2 v[8:9], v[6:7], off
	v_mul_f32_e32 v6, 0xbfb8aa3b, v94
	v_mul_f32_e32 v7, 0xbfb8aa3b, v95
	v_exp_f32_e32 v6, v6
	v_exp_f32_e32 v7, v7
	v_mul_f32_e32 v8, 0xbfb8aa3b, v96
	v_mul_f32_e32 v9, 0xbfb8aa3b, v97
	v_add_f32_e32 v6, 1.0, v6
	v_add_f32_e32 v7, 1.0, v7
	v_exp_f32_e32 v8, v8
	v_exp_f32_e32 v9, v9
	v_rcp_f32_e32 v6, v6
	v_rcp_f32_e32 v7, v7
	v_exp_f32_e32 v10, v10
	v_exp_f32_e32 v11, v11
	v_add_f32_e32 v8, 1.0, v8
	v_add_f32_e32 v9, 1.0, v9
	v_mul_f32_e32 v12, 0xbfb8aa3b, v88
	v_mul_f32_e32 v13, 0xbfb8aa3b, v89
	v_rcp_f32_e32 v8, v8
	v_rcp_f32_e32 v9, v9
	v_mul_f32 v6, v94, v6
	v_mul_f32 v7, v95, v7
	v_add_f32_e32 v10, 1.0, v10
	v_add_f32_e32 v11, 1.0, v11
	v_exp_f32_e32 v12, v12
	v_exp_f32_e32 v13, v13
	v_mul_f32 v6, v6, v90
	v_mul_f32 v7, v7, v91
	v_rcp_f32_e32 v10, v10
	v_rcp_f32_e32 v11, v11
	v_mul_f32 v6, v6, s66
	v_mul_f32 v7, v7, s66
	v_mul_f32 v8, v96, v8
	v_mul_f32 v9, v97, v9
	v_med3_f32 v14, v6, s29, v1
	v_med3_f32 v7, v7, s29, v1
	v_mov_b32_e32 v6, v195
	v_add_f32_e32 v12, 1.0, v12
	v_add_f32_e32 v13, 1.0, v13
	v_cvt_pk_fp8_f32 v6, v14, v7
	v_mul_f32 v8, v8, v92
	v_mul_f32 v9, v9, v93
	v_rcp_f32_e32 v12, v12
	v_rcp_f32_e32 v13, v13
	v_mul_f32 v10, v86, v10
	v_mul_f32 v11, v87, v11
	v_mul_f32 v8, v8, s66
	v_mul_f32 v9, v9, s66
	v_mul_f32 v10, v10, v82
	v_mul_f32 v11, v11, v83
	v_med3_f32 v7, v8, s29, v1
	v_mul_f32 v10, v10, s66
	v_mul_f32 v11, v11, s66
	v_med3_f32 v8, v9, s29, v1
	v_cvt_pk_fp8_f32 v6, v7, v8 op_sel:[0,0,1]
	v_med3_f32 v8, v10, s29, v1
	v_med3_f32 v9, v11, s29, v1
	v_mov_b32_e32 v7, v195
	v_mul_f32 v12, v88, v12
	v_mul_f32 v13, v89, v13
	v_cvt_pk_fp8_f32 v7, v8, v9
	v_mul_f32 v12, v12, v84
	v_mul_f32 v13, v13, v85
	v_add_u32_e32 v5, 0xa0, v4
	v_mul_f32 v12, v12, s66
	v_mul_f32 v13, v13, s66
	v_mul_f32_e32 v10, 0xbfb8aa3b, v72
	v_med3_f32 v8, v12, s29, v1
	v_med3_f32 v9, v13, s29, v1
	v_cvt_pk_fp8_f32 v7, v8, v9 op_sel:[0,0,1]
	v_mad_i64_i32 v[8:9], s[38:39], v5, s2, v[2:3]
	v_add_u32_e32 v12, 0xb0, v4
	v_mul_f32_e32 v4, 0xbfb8aa3b, v78
	v_mul_f32_e32 v5, 0xbfb8aa3b, v79
	v_exp_f32_e32 v4, v4
	v_exp_f32_e32 v5, v5
	global_store_dwordx2 v[8:9], v[6:7], off
	v_mul_f32_e32 v6, 0xbfb8aa3b, v80
	v_mul_f32_e32 v7, 0xbfb8aa3b, v81
	v_add_f32_e32 v4, 1.0, v4
	v_add_f32_e32 v5, 1.0, v5
	v_exp_f32_e32 v6, v6
	v_exp_f32_e32 v7, v7
	v_mul_f32_e32 v8, 0xbfb8aa3b, v70
	v_mul_f32_e32 v9, 0xbfb8aa3b, v71
	v_rcp_f32_e32 v4, v4
	v_rcp_f32_e32 v5, v5
	v_exp_f32_e32 v8, v8
	v_exp_f32_e32 v9, v9
	v_add_f32_e32 v6, 1.0, v6
	v_add_f32_e32 v7, 1.0, v7
	v_mul_f32_e32 v11, 0xbfb8aa3b, v73
	v_rcp_f32_e32 v6, v6
	v_rcp_f32_e32 v7, v7
	v_mul_f32 v4, v78, v4
	v_mul_f32 v5, v79, v5
	v_add_f32_e32 v8, 1.0, v8
	v_add_f32_e32 v9, 1.0, v9
	v_exp_f32_e32 v10, v10
	v_exp_f32_e32 v11, v11
	v_mul_f32 v4, v4, v74
	v_mul_f32 v5, v5, v75
	v_rcp_f32_e32 v8, v8
	v_rcp_f32_e32 v9, v9
	v_mul_f32 v4, v4, s66
	v_mul_f32 v5, v5, s66
	v_mul_f32 v6, v80, v6
	v_mul_f32 v7, v81, v7
	v_med3_f32 v13, v4, s29, v1
	v_med3_f32 v5, v5, s29, v1
	v_mov_b32_e32 v4, v195
	v_add_f32_e32 v10, 1.0, v10
	v_add_f32_e32 v11, 1.0, v11
	v_cvt_pk_fp8_f32 v4, v13, v5
	v_mul_f32 v6, v6, v76
	v_mul_f32 v7, v7, v77
	v_rcp_f32_e32 v10, v10
	v_rcp_f32_e32 v11, v11
	v_mul_f32 v8, v70, v8
	v_mul_f32 v9, v71, v9
	v_mul_f32 v6, v6, s66
	v_mul_f32 v7, v7, s66
	v_mul_f32 v8, v8, v66
	v_mul_f32 v9, v9, v67
	v_med3_f32 v5, v6, s29, v1
	v_mul_f32 v8, v8, s66
	v_mul_f32 v9, v9, s66
	v_med3_f32 v6, v7, s29, v1
	v_cvt_pk_fp8_f32 v4, v5, v6 op_sel:[0,0,1]
	v_med3_f32 v6, v8, s29, v1
	v_med3_f32 v7, v9, s29, v1
	v_mov_b32_e32 v5, v195
	v_mul_f32 v10, v72, v10
	v_mul_f32 v11, v73, v11
	v_cvt_pk_fp8_f32 v5, v6, v7
	v_mul_f32 v10, v10, v68
	v_mul_f32 v11, v11, v69
	v_mad_i64_i32 v[2:3], s[38:39], v12, s2, v[2:3]
	v_mul_f32 v10, v10, s66
	v_mul_f32 v11, v11, s66
	s_mov_b64 s[38:39], -1
	v_med3_f32 v6, v10, s29, v1
	v_med3_f32 v7, v11, s29, v1
	v_cvt_pk_fp8_f32 v5, v6, v7 op_sel:[0,0,1]
	global_store_dwordx2 v[2:3], v[4:5], off
	s_cbranch_vccnz .LBB0_1362
	s_andn2_b64 vcc, exec, s[80:81]
	s_cbranch_vccnz .LBB0_1361
	s_barrier
	s_branch .LBB0_1361
